# one counted vmcnt wait per four table rows instead of one per row in the two sliced passes
# baseline (speedup 1.0000x reference)
.Lpa_tok:
	v_lshlrev_b32_e32 v124, 16, v116
	v_and_b32_e32 v125, 0xffff0000, v116
	v_pk_mul_f32 v[108:109], v[124:125], v[100:101]
	v_lshlrev_b32_e32 v124, 16, v117
	v_and_b32_e32 v125, 0xffff0000, v117
	v_pk_mul_f32 v[110:111], v[124:125], v[102:103]
	v_lshlrev_b32_e32 v124, 16, v118
	v_and_b32_e32 v125, 0xffff0000, v118
	v_pk_mul_f32 v[112:113], v[124:125], v[104:105]
	v_lshlrev_b32_e32 v124, 16, v119
	v_and_b32_e32 v125, 0xffff0000, v119
	v_pk_mul_f32 v[114:115], v[124:125], v[106:107]
	v_add_f32_e32 v16, v108, v109
	v_add_f32_e32 v17, v110, v111
	v_add_f32_e32 v18, v112, v113
	v_add_f32_e32 v19, v114, v115
	v_add_f32_e32 v16, v16, v17
	v_add_f32_e32 v18, v18, v19
	v_add_f32_e32 v16, v16, v18
	s_nop 1
	v_add_f32_dpp v17, v16, v16 quad_perm:[1,0,3,2] row_mask:0xf bank_mask:0xf
	s_nop 1
	v_add_f32_dpp v16, v17, v17 quad_perm:[2,3,0,1] row_mask:0xf bank_mask:0xf
	s_nop 1
	v_add_f32_dpp v17, v16, v16 row_half_mirror row_mask:0xf bank_mask:0xf
	s_nop 1
	v_add_f32_dpp v16, v17, v17 row_ror:8 row_mask:0xf bank_mask:0xf
	v_mov_b32_e32 v17, v16
	s_nop 1
	v_permlane16_swap_b32_e32 v16, v17
	v_add_f32_e32 v16, v16, v17
	v_mov_b32_e32 v17, v16
	s_nop 1
	v_permlane32_swap_b32_e32 v16, v17
	v_add_f32_e32 v16, v16, v17
	s_lshl_b32 s30, s16, 7
	s_add_u32 s28, s22, s30
	s_addc_u32 s29, s23, 0
	v_lshlrev_b32_e32 v19, 1, v1
	s_mov_b64 exec, s[2:3]
	global_store_dword v19, v16, s[28:29]
	s_mov_b64 exec, -1
	v_mov_b32_e32 v120, v122
	v_mov_b32_e32 v121, v123
	s_lshl_b32 s30, s16, 9
	v_lshl_add_u64 v[22:23], v[176:177], 0, s[30:31]
	s_add_i32 s18, s16, 1
	s_min_i32 s18, s18, s24
	s_lshl_b32 s30, s16, 9
	s_add_u32 s36, s40, s30
	s_addc_u32 s37, s41, 0
	s_lshl_b32 s30, s18, 9
	s_add_u32 s38, s40, s30
	s_addc_u32 s39, s41, 0
	s_lshl_b32 s30, s18, 13
	v_lshl_add_u64 v[160:161], v[172:173], 0, s[30:31]
	global_load_dwordx4 v[116:119], v[160:161], off
	s_lshl_b32 s30, s18, 9
	v_lshl_add_u64 v[160:161], v[174:175], 0, s[30:31]
	global_load_dword v122, v[160:161], off
	global_load_dword v123, v[160:161], off offset:256
	s_waitcnt vmcnt(31)
	v_cvt_f32_ubyte0_e32 v124, v24
	v_cvt_f32_ubyte1_e32 v126, v24
	v_cvt_f32_ubyte2_e32 v128, v24
	v_cvt_f32_ubyte3_e32 v130, v24
	v_cvt_f32_ubyte0_e32 v132, v25
	v_cvt_f32_ubyte1_e32 v134, v25
	v_cvt_f32_ubyte2_e32 v136, v25
	v_cvt_f32_ubyte3_e32 v138, v25
	s_waitcnt lgkmcnt(0)
	s_load_dwordx16 s[84:99], s[36:37], 0xc0 glc
	s_lshl_b32 s30, s68, 12
	s_add_u32 s28, s26, s30
	s_addc_u32 s29, s27, 0
	global_load_dwordx2 v[24:25], v162, s[28:29]
	v_cvt_f32_ubyte0_e32 v125, v26
	v_cvt_f32_ubyte1_e32 v127, v26
	v_cvt_f32_ubyte2_e32 v129, v26
	v_cvt_f32_ubyte3_e32 v131, v26
	v_cvt_f32_ubyte0_e32 v133, v27
	v_cvt_f32_ubyte1_e32 v135, v27
	v_cvt_f32_ubyte2_e32 v137, v27
	v_cvt_f32_ubyte3_e32 v139, v27
	s_lshl_b32 s30, s69, 12
	s_add_u32 s28, s26, s30
	s_addc_u32 s29, s27, 0
	global_load_dwordx2 v[26:27], v162, s[28:29]
	v_cvt_f32_ubyte0_e32 v140, v28
	v_cvt_f32_ubyte1_e32 v142, v28
	v_cvt_f32_ubyte2_e32 v144, v28
	v_cvt_f32_ubyte3_e32 v146, v28
	v_cvt_f32_ubyte0_e32 v148, v29
	v_cvt_f32_ubyte1_e32 v150, v29
	v_cvt_f32_ubyte2_e32 v152, v29
	v_cvt_f32_ubyte3_e32 v154, v29
	s_lshl_b32 s30, s70, 12
	s_add_u32 s28, s26, s30
	s_addc_u32 s29, s27, 0
	global_load_dwordx2 v[28:29], v162, s[28:29]
	v_cvt_f32_ubyte0_e32 v141, v30
	v_cvt_f32_ubyte1_e32 v143, v30
	v_cvt_f32_ubyte2_e32 v145, v30
	v_cvt_f32_ubyte3_e32 v147, v30
	v_cvt_f32_ubyte0_e32 v149, v31
	v_cvt_f32_ubyte1_e32 v151, v31
	v_cvt_f32_ubyte2_e32 v153, v31
	v_cvt_f32_ubyte3_e32 v155, v31
	s_lshl_b32 s30, s71, 12
	s_add_u32 s28, s26, s30
	s_addc_u32 s29, s27, 0
	global_load_dwordx2 v[30:31], v162, s[28:29]
	v_mul_f32_e32 v178, v124, v108
	v_mul_f32_e32 v179, v125, v108
	v_mul_f32_e32 v180, v140, v108
	v_mul_f32_e32 v181, v141, v108
	v_fmac_f32_e32 v178, v126, v109
	v_fmac_f32_e32 v179, v127, v109
	v_fmac_f32_e32 v180, v142, v109
	v_fmac_f32_e32 v181, v143, v109
	v_fmac_f32_e32 v178, v128, v110
	v_fmac_f32_e32 v179, v129, v110
	v_fmac_f32_e32 v180, v144, v110
	v_fmac_f32_e32 v181, v145, v110
	v_fmac_f32_e32 v178, v130, v111
	v_fmac_f32_e32 v179, v131, v111
	v_fmac_f32_e32 v180, v146, v111
	v_fmac_f32_e32 v181, v147, v111
	v_fmac_f32_e32 v178, v132, v112
	v_fmac_f32_e32 v179, v133, v112
	v_fmac_f32_e32 v180, v148, v112
	v_fmac_f32_e32 v181, v149, v112
	v_fmac_f32_e32 v178, v134, v113
	v_fmac_f32_e32 v179, v135, v113
	v_fmac_f32_e32 v180, v150, v113
	v_fmac_f32_e32 v181, v151, v113
	v_fmac_f32_e32 v178, v136, v114
	v_fmac_f32_e32 v179, v137, v114
	v_fmac_f32_e32 v180, v152, v114
	v_fmac_f32_e32 v181, v153, v114
	v_fmac_f32_e32 v178, v138, v115
	v_fmac_f32_e32 v179, v139, v115
	v_fmac_f32_e32 v180, v154, v115
	v_fmac_f32_e32 v181, v155, v115
	s_waitcnt vmcnt(31)
	v_cvt_f32_ubyte0_e32 v124, v32
	v_cvt_f32_ubyte1_e32 v126, v32
	v_cvt_f32_ubyte2_e32 v128, v32
	v_cvt_f32_ubyte3_e32 v130, v32
	v_cvt_f32_ubyte0_e32 v132, v33
	v_cvt_f32_ubyte1_e32 v134, v33
	v_cvt_f32_ubyte2_e32 v136, v33
	v_cvt_f32_ubyte3_e32 v138, v33
	s_lshl_b32 s30, s72, 12
	s_add_u32 s28, s26, s30
	s_addc_u32 s29, s27, 0
	global_load_dwordx2 v[32:33], v162, s[28:29]
	v_cvt_f32_ubyte0_e32 v125, v34
	v_cvt_f32_ubyte1_e32 v127, v34
	v_cvt_f32_ubyte2_e32 v129, v34
	v_cvt_f32_ubyte3_e32 v131, v34
	v_cvt_f32_ubyte0_e32 v133, v35
	v_cvt_f32_ubyte1_e32 v135, v35
	v_cvt_f32_ubyte2_e32 v137, v35
	v_cvt_f32_ubyte3_e32 v139, v35
	s_lshl_b32 s30, s73, 12
	s_add_u32 s28, s26, s30
	s_addc_u32 s29, s27, 0
	global_load_dwordx2 v[34:35], v162, s[28:29]
	v_cvt_f32_ubyte0_e32 v140, v36
	v_cvt_f32_ubyte1_e32 v142, v36
	v_cvt_f32_ubyte2_e32 v144, v36
	v_cvt_f32_ubyte3_e32 v146, v36
	v_cvt_f32_ubyte0_e32 v148, v37
	v_cvt_f32_ubyte1_e32 v150, v37
	v_cvt_f32_ubyte2_e32 v152, v37
	v_cvt_f32_ubyte3_e32 v154, v37
	s_lshl_b32 s30, s74, 12
	s_add_u32 s28, s26, s30
	s_addc_u32 s29, s27, 0
	global_load_dwordx2 v[36:37], v162, s[28:29]
	v_cvt_f32_ubyte0_e32 v141, v38
	v_cvt_f32_ubyte1_e32 v143, v38
	v_cvt_f32_ubyte2_e32 v145, v38
	v_cvt_f32_ubyte3_e32 v147, v38
	v_cvt_f32_ubyte0_e32 v149, v39
	v_cvt_f32_ubyte1_e32 v151, v39
	v_cvt_f32_ubyte2_e32 v153, v39
	v_cvt_f32_ubyte3_e32 v155, v39
	s_lshl_b32 s30, s75, 12
	s_add_u32 s28, s26, s30
	s_addc_u32 s29, s27, 0
	global_load_dwordx2 v[38:39], v162, s[28:29]
	v_mul_f32_e32 v182, v124, v108
	v_mul_f32_e32 v183, v125, v108
	v_mul_f32_e32 v184, v140, v108
	v_mul_f32_e32 v185, v141, v108
	v_fmac_f32_e32 v182, v126, v109
	v_fmac_f32_e32 v183, v127, v109
	v_fmac_f32_e32 v184, v142, v109
	v_fmac_f32_e32 v185, v143, v109
	v_fmac_f32_e32 v182, v128, v110
	v_fmac_f32_e32 v183, v129, v110
	v_fmac_f32_e32 v184, v144, v110
	v_fmac_f32_e32 v185, v145, v110
	v_fmac_f32_e32 v182, v130, v111
	v_fmac_f32_e32 v183, v131, v111
	v_fmac_f32_e32 v184, v146, v111
	v_fmac_f32_e32 v185, v147, v111
	v_fmac_f32_e32 v182, v132, v112
	v_fmac_f32_e32 v183, v133, v112
	v_fmac_f32_e32 v184, v148, v112
	v_fmac_f32_e32 v185, v149, v112
	v_fmac_f32_e32 v182, v134, v113
	v_fmac_f32_e32 v183, v135, v113
	v_fmac_f32_e32 v184, v150, v113
	v_fmac_f32_e32 v185, v151, v113
	v_fmac_f32_e32 v182, v136, v114
	v_fmac_f32_e32 v183, v137, v114
	v_fmac_f32_e32 v184, v152, v114
	v_fmac_f32_e32 v185, v153, v114
	v_fmac_f32_e32 v182, v138, v115
	v_fmac_f32_e32 v183, v139, v115
	v_fmac_f32_e32 v184, v154, v115
	v_fmac_f32_e32 v185, v155, v115
	s_waitcnt vmcnt(31)
	v_cvt_f32_ubyte0_e32 v124, v40
	v_cvt_f32_ubyte1_e32 v126, v40
	v_cvt_f32_ubyte2_e32 v128, v40
	v_cvt_f32_ubyte3_e32 v130, v40
	v_cvt_f32_ubyte0_e32 v132, v41
	v_cvt_f32_ubyte1_e32 v134, v41
	v_cvt_f32_ubyte2_e32 v136, v41
	v_cvt_f32_ubyte3_e32 v138, v41
	s_lshl_b32 s30, s76, 12
	s_add_u32 s28, s26, s30
	s_addc_u32 s29, s27, 0
	global_load_dwordx2 v[40:41], v162, s[28:29]
	v_cvt_f32_ubyte0_e32 v125, v42
	v_cvt_f32_ubyte1_e32 v127, v42
	v_cvt_f32_ubyte2_e32 v129, v42
	v_cvt_f32_ubyte3_e32 v131, v42
	v_cvt_f32_ubyte0_e32 v133, v43
	v_cvt_f32_ubyte1_e32 v135, v43
	v_cvt_f32_ubyte2_e32 v137, v43
	v_cvt_f32_ubyte3_e32 v139, v43
	s_lshl_b32 s30, s77, 12
	s_add_u32 s28, s26, s30
	s_addc_u32 s29, s27, 0
	global_load_dwordx2 v[42:43], v162, s[28:29]
	v_cvt_f32_ubyte0_e32 v140, v44
	v_cvt_f32_ubyte1_e32 v142, v44
	v_cvt_f32_ubyte2_e32 v144, v44
	v_cvt_f32_ubyte3_e32 v146, v44
	v_cvt_f32_ubyte0_e32 v148, v45
	v_cvt_f32_ubyte1_e32 v150, v45
	v_cvt_f32_ubyte2_e32 v152, v45
	v_cvt_f32_ubyte3_e32 v154, v45
	s_lshl_b32 s30, s78, 12
	s_add_u32 s28, s26, s30
	s_addc_u32 s29, s27, 0
	global_load_dwordx2 v[44:45], v162, s[28:29]
	v_cvt_f32_ubyte0_e32 v141, v46
	v_cvt_f32_ubyte1_e32 v143, v46
	v_cvt_f32_ubyte2_e32 v145, v46
	v_cvt_f32_ubyte3_e32 v147, v46
	v_cvt_f32_ubyte0_e32 v149, v47
	v_cvt_f32_ubyte1_e32 v151, v47
	v_cvt_f32_ubyte2_e32 v153, v47
	v_cvt_f32_ubyte3_e32 v155, v47
	s_lshl_b32 s30, s79, 12
	s_add_u32 s28, s26, s30
	s_addc_u32 s29, s27, 0
	global_load_dwordx2 v[46:47], v162, s[28:29]
	v_mul_f32_e32 v186, v124, v108
	v_mul_f32_e32 v187, v125, v108
	v_mul_f32_e32 v188, v140, v108
	v_mul_f32_e32 v189, v141, v108
	v_fmac_f32_e32 v186, v126, v109
	v_fmac_f32_e32 v187, v127, v109
	v_fmac_f32_e32 v188, v142, v109
	v_fmac_f32_e32 v189, v143, v109
	v_fmac_f32_e32 v186, v128, v110
	v_fmac_f32_e32 v187, v129, v110
	v_fmac_f32_e32 v188, v144, v110
	v_fmac_f32_e32 v189, v145, v110
	v_fmac_f32_e32 v186, v130, v111
	v_fmac_f32_e32 v187, v131, v111
	v_fmac_f32_e32 v188, v146, v111
	v_fmac_f32_e32 v189, v147, v111
	v_fmac_f32_e32 v186, v132, v112
	v_fmac_f32_e32 v187, v133, v112
	v_fmac_f32_e32 v188, v148, v112
	v_fmac_f32_e32 v189, v149, v112
	v_fmac_f32_e32 v186, v134, v113
	v_fmac_f32_e32 v187, v135, v113
	v_fmac_f32_e32 v188, v150, v113
	v_fmac_f32_e32 v189, v151, v113
	v_fmac_f32_e32 v186, v136, v114
	v_fmac_f32_e32 v187, v137, v114
	v_fmac_f32_e32 v188, v152, v114
	v_fmac_f32_e32 v189, v153, v114
	v_fmac_f32_e32 v186, v138, v115
	v_fmac_f32_e32 v187, v139, v115
	v_fmac_f32_e32 v188, v154, v115
	v_fmac_f32_e32 v189, v155, v115
	s_waitcnt vmcnt(31)
	v_cvt_f32_ubyte0_e32 v124, v48
	v_cvt_f32_ubyte1_e32 v126, v48
	v_cvt_f32_ubyte2_e32 v128, v48
	v_cvt_f32_ubyte3_e32 v130, v48
	v_cvt_f32_ubyte0_e32 v132, v49
	v_cvt_f32_ubyte1_e32 v134, v49
	v_cvt_f32_ubyte2_e32 v136, v49
	v_cvt_f32_ubyte3_e32 v138, v49
	s_lshl_b32 s30, s80, 12
	s_add_u32 s28, s26, s30
	s_addc_u32 s29, s27, 0
	global_load_dwordx2 v[48:49], v162, s[28:29]
	v_cvt_f32_ubyte0_e32 v125, v50
	v_cvt_f32_ubyte1_e32 v127, v50
	v_cvt_f32_ubyte2_e32 v129, v50
	v_cvt_f32_ubyte3_e32 v131, v50
	v_cvt_f32_ubyte0_e32 v133, v51
	v_cvt_f32_ubyte1_e32 v135, v51
	v_cvt_f32_ubyte2_e32 v137, v51
	v_cvt_f32_ubyte3_e32 v139, v51
	s_lshl_b32 s30, s81, 12
	s_add_u32 s28, s26, s30
	s_addc_u32 s29, s27, 0
	global_load_dwordx2 v[50:51], v162, s[28:29]
	v_cvt_f32_ubyte0_e32 v140, v52
	v_cvt_f32_ubyte1_e32 v142, v52
	v_cvt_f32_ubyte2_e32 v144, v52
	v_cvt_f32_ubyte3_e32 v146, v52
	v_cvt_f32_ubyte0_e32 v148, v53
	v_cvt_f32_ubyte1_e32 v150, v53
	v_cvt_f32_ubyte2_e32 v152, v53
	v_cvt_f32_ubyte3_e32 v154, v53
	s_lshl_b32 s30, s82, 12
	s_add_u32 s28, s26, s30
	s_addc_u32 s29, s27, 0
	global_load_dwordx2 v[52:53], v162, s[28:29]
	v_cvt_f32_ubyte0_e32 v141, v54
	v_cvt_f32_ubyte1_e32 v143, v54
	v_cvt_f32_ubyte2_e32 v145, v54
	v_cvt_f32_ubyte3_e32 v147, v54
	v_cvt_f32_ubyte0_e32 v149, v55
	v_cvt_f32_ubyte1_e32 v151, v55
	v_cvt_f32_ubyte2_e32 v153, v55
	v_cvt_f32_ubyte3_e32 v155, v55
	s_lshl_b32 s30, s83, 12
	s_add_u32 s28, s26, s30
	s_addc_u32 s29, s27, 0
	global_load_dwordx2 v[54:55], v162, s[28:29]
	v_mul_f32_e32 v190, v124, v108
	v_mul_f32_e32 v191, v125, v108
	v_mul_f32_e32 v192, v140, v108
	v_mul_f32_e32 v193, v141, v108
	v_fmac_f32_e32 v190, v126, v109
	v_fmac_f32_e32 v191, v127, v109
	v_fmac_f32_e32 v192, v142, v109
	v_fmac_f32_e32 v193, v143, v109
	v_fmac_f32_e32 v190, v128, v110
	v_fmac_f32_e32 v191, v129, v110
	v_fmac_f32_e32 v192, v144, v110
	v_fmac_f32_e32 v193, v145, v110
	v_fmac_f32_e32 v190, v130, v111
	v_fmac_f32_e32 v191, v131, v111
	v_fmac_f32_e32 v192, v146, v111
	v_fmac_f32_e32 v193, v147, v111
	v_fmac_f32_e32 v190, v132, v112
	v_fmac_f32_e32 v191, v133, v112
	v_fmac_f32_e32 v192, v148, v112
	v_fmac_f32_e32 v193, v149, v112
	v_fmac_f32_e32 v190, v134, v113
	v_fmac_f32_e32 v191, v135, v113
	v_fmac_f32_e32 v192, v150, v113
	v_fmac_f32_e32 v193, v151, v113
	v_fmac_f32_e32 v190, v136, v114
	v_fmac_f32_e32 v191, v137, v114
	v_fmac_f32_e32 v192, v152, v114
	v_fmac_f32_e32 v193, v153, v114
	v_fmac_f32_e32 v190, v138, v115
	v_fmac_f32_e32 v191, v139, v115
	v_fmac_f32_e32 v192, v154, v115
	v_fmac_f32_e32 v193, v155, v115
	s_waitcnt vmcnt(31)
	v_cvt_f32_ubyte0_e32 v124, v56
	v_cvt_f32_ubyte1_e32 v126, v56
	v_cvt_f32_ubyte2_e32 v128, v56
	v_cvt_f32_ubyte3_e32 v130, v56
	v_cvt_f32_ubyte0_e32 v132, v57
	v_cvt_f32_ubyte1_e32 v134, v57
	v_cvt_f32_ubyte2_e32 v136, v57
	v_cvt_f32_ubyte3_e32 v138, v57
	s_waitcnt lgkmcnt(0)
	s_load_dwordx16 s[68:83], s[36:37], 0x100 glc
	s_lshl_b32 s30, s84, 12
	s_add_u32 s28, s26, s30
	s_addc_u32 s29, s27, 0
	global_load_dwordx2 v[56:57], v162, s[28:29]
	v_cvt_f32_ubyte0_e32 v125, v58
	v_cvt_f32_ubyte1_e32 v127, v58
	v_cvt_f32_ubyte2_e32 v129, v58
	v_cvt_f32_ubyte3_e32 v131, v58
	v_cvt_f32_ubyte0_e32 v133, v59
	v_cvt_f32_ubyte1_e32 v135, v59
	v_cvt_f32_ubyte2_e32 v137, v59
	v_cvt_f32_ubyte3_e32 v139, v59
	s_lshl_b32 s30, s85, 12
	s_add_u32 s28, s26, s30
	s_addc_u32 s29, s27, 0
	global_load_dwordx2 v[58:59], v162, s[28:29]
	v_cvt_f32_ubyte0_e32 v140, v60
	v_cvt_f32_ubyte1_e32 v142, v60
	v_cvt_f32_ubyte2_e32 v144, v60
	v_cvt_f32_ubyte3_e32 v146, v60
	v_cvt_f32_ubyte0_e32 v148, v61
	v_cvt_f32_ubyte1_e32 v150, v61
	v_cvt_f32_ubyte2_e32 v152, v61
	v_cvt_f32_ubyte3_e32 v154, v61
	s_lshl_b32 s30, s86, 12
	s_add_u32 s28, s26, s30
	s_addc_u32 s29, s27, 0
	global_load_dwordx2 v[60:61], v162, s[28:29]
	v_cvt_f32_ubyte0_e32 v141, v62
	v_cvt_f32_ubyte1_e32 v143, v62
	v_cvt_f32_ubyte2_e32 v145, v62
	v_cvt_f32_ubyte3_e32 v147, v62
	v_cvt_f32_ubyte0_e32 v149, v63
	v_cvt_f32_ubyte1_e32 v151, v63
	v_cvt_f32_ubyte2_e32 v153, v63
	v_cvt_f32_ubyte3_e32 v155, v63
	s_lshl_b32 s30, s87, 12
	s_add_u32 s28, s26, s30
	s_addc_u32 s29, s27, 0
	global_load_dwordx2 v[62:63], v162, s[28:29]
	v_mul_f32_e32 v194, v124, v108
	v_mul_f32_e32 v195, v125, v108
	v_mul_f32_e32 v196, v140, v108
	v_mul_f32_e32 v197, v141, v108
	v_fmac_f32_e32 v194, v126, v109
	v_fmac_f32_e32 v195, v127, v109
	v_fmac_f32_e32 v196, v142, v109
	v_fmac_f32_e32 v197, v143, v109
	v_fmac_f32_e32 v194, v128, v110
	v_fmac_f32_e32 v195, v129, v110
	v_fmac_f32_e32 v196, v144, v110
	v_fmac_f32_e32 v197, v145, v110
	v_fmac_f32_e32 v194, v130, v111
	v_fmac_f32_e32 v195, v131, v111
	v_fmac_f32_e32 v196, v146, v111
	v_fmac_f32_e32 v197, v147, v111
	v_fmac_f32_e32 v194, v132, v112
	v_fmac_f32_e32 v195, v133, v112
	v_fmac_f32_e32 v196, v148, v112
	v_fmac_f32_e32 v197, v149, v112
	v_fmac_f32_e32 v194, v134, v113
	v_fmac_f32_e32 v195, v135, v113
	v_fmac_f32_e32 v196, v150, v113
	v_fmac_f32_e32 v197, v151, v113
	v_fmac_f32_e32 v194, v136, v114
	v_fmac_f32_e32 v195, v137, v114
	v_fmac_f32_e32 v196, v152, v114
	v_fmac_f32_e32 v197, v153, v114
	v_fmac_f32_e32 v194, v138, v115
	v_fmac_f32_e32 v195, v139, v115
	v_fmac_f32_e32 v196, v154, v115
	v_fmac_f32_e32 v197, v155, v115
	s_waitcnt vmcnt(31)
	v_cvt_f32_ubyte0_e32 v124, v64
	v_cvt_f32_ubyte1_e32 v126, v64
	v_cvt_f32_ubyte2_e32 v128, v64
	v_cvt_f32_ubyte3_e32 v130, v64
	v_cvt_f32_ubyte0_e32 v132, v65
	v_cvt_f32_ubyte1_e32 v134, v65
	v_cvt_f32_ubyte2_e32 v136, v65
	v_cvt_f32_ubyte3_e32 v138, v65
	s_lshl_b32 s30, s88, 12
	s_add_u32 s28, s26, s30
	s_addc_u32 s29, s27, 0
	global_load_dwordx2 v[64:65], v162, s[28:29]
	v_cvt_f32_ubyte0_e32 v125, v66
	v_cvt_f32_ubyte1_e32 v127, v66
	v_cvt_f32_ubyte2_e32 v129, v66
	v_cvt_f32_ubyte3_e32 v131, v66
	v_cvt_f32_ubyte0_e32 v133, v67
	v_cvt_f32_ubyte1_e32 v135, v67
	v_cvt_f32_ubyte2_e32 v137, v67
	v_cvt_f32_ubyte3_e32 v139, v67
	s_lshl_b32 s30, s89, 12
	s_add_u32 s28, s26, s30
	s_addc_u32 s29, s27, 0
	global_load_dwordx2 v[66:67], v162, s[28:29]
	v_cvt_f32_ubyte0_e32 v140, v68
	v_cvt_f32_ubyte1_e32 v142, v68
	v_cvt_f32_ubyte2_e32 v144, v68
	v_cvt_f32_ubyte3_e32 v146, v68
	v_cvt_f32_ubyte0_e32 v148, v69
	v_cvt_f32_ubyte1_e32 v150, v69
	v_cvt_f32_ubyte2_e32 v152, v69
	v_cvt_f32_ubyte3_e32 v154, v69
	s_lshl_b32 s30, s90, 12
	s_add_u32 s28, s26, s30
	s_addc_u32 s29, s27, 0
	global_load_dwordx2 v[68:69], v162, s[28:29]
	v_cvt_f32_ubyte0_e32 v141, v70
	v_cvt_f32_ubyte1_e32 v143, v70
	v_cvt_f32_ubyte2_e32 v145, v70
	v_cvt_f32_ubyte3_e32 v147, v70
	v_cvt_f32_ubyte0_e32 v149, v71
	v_cvt_f32_ubyte1_e32 v151, v71
	v_cvt_f32_ubyte2_e32 v153, v71
	v_cvt_f32_ubyte3_e32 v155, v71
	s_lshl_b32 s30, s91, 12
	s_add_u32 s28, s26, s30
	s_addc_u32 s29, s27, 0
	global_load_dwordx2 v[70:71], v162, s[28:29]
	v_mul_f32_e32 v198, v124, v108
	v_mul_f32_e32 v199, v125, v108
	v_mul_f32_e32 v200, v140, v108
	v_mul_f32_e32 v201, v141, v108
	v_fmac_f32_e32 v198, v126, v109
	v_fmac_f32_e32 v199, v127, v109
	v_fmac_f32_e32 v200, v142, v109
	v_fmac_f32_e32 v201, v143, v109
	v_fmac_f32_e32 v198, v128, v110
	v_fmac_f32_e32 v199, v129, v110
	v_fmac_f32_e32 v200, v144, v110
	v_fmac_f32_e32 v201, v145, v110
	v_fmac_f32_e32 v198, v130, v111
	v_fmac_f32_e32 v199, v131, v111
	v_fmac_f32_e32 v200, v146, v111
	v_fmac_f32_e32 v201, v147, v111
	v_fmac_f32_e32 v198, v132, v112
	v_fmac_f32_e32 v199, v133, v112
	v_fmac_f32_e32 v200, v148, v112
	v_fmac_f32_e32 v201, v149, v112
	v_fmac_f32_e32 v198, v134, v113
	v_fmac_f32_e32 v199, v135, v113
	v_fmac_f32_e32 v200, v150, v113
	v_fmac_f32_e32 v201, v151, v113
	v_fmac_f32_e32 v198, v136, v114
	v_fmac_f32_e32 v199, v137, v114
	v_fmac_f32_e32 v200, v152, v114
	v_fmac_f32_e32 v201, v153, v114
	v_fmac_f32_e32 v198, v138, v115
	v_fmac_f32_e32 v199, v139, v115
	v_fmac_f32_e32 v200, v154, v115
	v_fmac_f32_e32 v201, v155, v115
	s_waitcnt vmcnt(31)
	v_cvt_f32_ubyte0_e32 v124, v72
	v_cvt_f32_ubyte1_e32 v126, v72
	v_cvt_f32_ubyte2_e32 v128, v72
	v_cvt_f32_ubyte3_e32 v130, v72
	v_cvt_f32_ubyte0_e32 v132, v73
	v_cvt_f32_ubyte1_e32 v134, v73
	v_cvt_f32_ubyte2_e32 v136, v73
	v_cvt_f32_ubyte3_e32 v138, v73
	s_lshl_b32 s30, s92, 12
	s_add_u32 s28, s26, s30
	s_addc_u32 s29, s27, 0
	global_load_dwordx2 v[72:73], v162, s[28:29]
	v_cvt_f32_ubyte0_e32 v125, v74
	v_cvt_f32_ubyte1_e32 v127, v74
	v_cvt_f32_ubyte2_e32 v129, v74
	v_cvt_f32_ubyte3_e32 v131, v74
	v_cvt_f32_ubyte0_e32 v133, v75
	v_cvt_f32_ubyte1_e32 v135, v75
	v_cvt_f32_ubyte2_e32 v137, v75
	v_cvt_f32_ubyte3_e32 v139, v75
	s_lshl_b32 s30, s93, 12
	s_add_u32 s28, s26, s30
	s_addc_u32 s29, s27, 0
	global_load_dwordx2 v[74:75], v162, s[28:29]
	v_cvt_f32_ubyte0_e32 v140, v76
	v_cvt_f32_ubyte1_e32 v142, v76
	v_cvt_f32_ubyte2_e32 v144, v76
	v_cvt_f32_ubyte3_e32 v146, v76
	v_cvt_f32_ubyte0_e32 v148, v77
	v_cvt_f32_ubyte1_e32 v150, v77
	v_cvt_f32_ubyte2_e32 v152, v77
	v_cvt_f32_ubyte3_e32 v154, v77
	s_lshl_b32 s30, s94, 12
	s_add_u32 s28, s26, s30
	s_addc_u32 s29, s27, 0
	global_load_dwordx2 v[76:77], v162, s[28:29]
	v_cvt_f32_ubyte0_e32 v141, v78
	v_cvt_f32_ubyte1_e32 v143, v78
	v_cvt_f32_ubyte2_e32 v145, v78
	v_cvt_f32_ubyte3_e32 v147, v78
	v_cvt_f32_ubyte0_e32 v149, v79
	v_cvt_f32_ubyte1_e32 v151, v79
	v_cvt_f32_ubyte2_e32 v153, v79
	v_cvt_f32_ubyte3_e32 v155, v79
	s_lshl_b32 s30, s95, 12
	s_add_u32 s28, s26, s30
	s_addc_u32 s29, s27, 0
	global_load_dwordx2 v[78:79], v162, s[28:29]
	v_mul_f32_e32 v202, v124, v108
	v_mul_f32_e32 v203, v125, v108
	v_mul_f32_e32 v204, v140, v108
	v_mul_f32_e32 v205, v141, v108
	v_fmac_f32_e32 v202, v126, v109
	v_fmac_f32_e32 v203, v127, v109
	v_fmac_f32_e32 v204, v142, v109
	v_fmac_f32_e32 v205, v143, v109
	v_fmac_f32_e32 v202, v128, v110
	v_fmac_f32_e32 v203, v129, v110
	v_fmac_f32_e32 v204, v144, v110
	v_fmac_f32_e32 v205, v145, v110
	v_fmac_f32_e32 v202, v130, v111
	v_fmac_f32_e32 v203, v131, v111
	v_fmac_f32_e32 v204, v146, v111
	v_fmac_f32_e32 v205, v147, v111
	v_fmac_f32_e32 v202, v132, v112
	v_fmac_f32_e32 v203, v133, v112
	v_fmac_f32_e32 v204, v148, v112
	v_fmac_f32_e32 v205, v149, v112
	v_fmac_f32_e32 v202, v134, v113
	v_fmac_f32_e32 v203, v135, v113
	v_fmac_f32_e32 v204, v150, v113
	v_fmac_f32_e32 v205, v151, v113
	v_fmac_f32_e32 v202, v136, v114
	v_fmac_f32_e32 v203, v137, v114
	v_fmac_f32_e32 v204, v152, v114
	v_fmac_f32_e32 v205, v153, v114
	v_fmac_f32_e32 v202, v138, v115
	v_fmac_f32_e32 v203, v139, v115
	v_fmac_f32_e32 v204, v154, v115
	v_fmac_f32_e32 v205, v155, v115
	s_waitcnt vmcnt(31)
	v_cvt_f32_ubyte0_e32 v124, v80
	v_cvt_f32_ubyte1_e32 v126, v80
	v_cvt_f32_ubyte2_e32 v128, v80
	v_cvt_f32_ubyte3_e32 v130, v80
	v_cvt_f32_ubyte0_e32 v132, v81
	v_cvt_f32_ubyte1_e32 v134, v81
	v_cvt_f32_ubyte2_e32 v136, v81
	v_cvt_f32_ubyte3_e32 v138, v81
	s_lshl_b32 s30, s96, 12
	s_add_u32 s28, s26, s30
	s_addc_u32 s29, s27, 0
	global_load_dwordx2 v[80:81], v162, s[28:29]
	v_cvt_f32_ubyte0_e32 v125, v82
	v_cvt_f32_ubyte1_e32 v127, v82
	v_cvt_f32_ubyte2_e32 v129, v82
	v_cvt_f32_ubyte3_e32 v131, v82
	v_cvt_f32_ubyte0_e32 v133, v83
	v_cvt_f32_ubyte1_e32 v135, v83
	v_cvt_f32_ubyte2_e32 v137, v83
	v_cvt_f32_ubyte3_e32 v139, v83
	s_lshl_b32 s30, s97, 12
	s_add_u32 s28, s26, s30
	s_addc_u32 s29, s27, 0
	global_load_dwordx2 v[82:83], v162, s[28:29]
	v_cvt_f32_ubyte0_e32 v140, v84
	v_cvt_f32_ubyte1_e32 v142, v84
	v_cvt_f32_ubyte2_e32 v144, v84
	v_cvt_f32_ubyte3_e32 v146, v84
	v_cvt_f32_ubyte0_e32 v148, v85
	v_cvt_f32_ubyte1_e32 v150, v85
	v_cvt_f32_ubyte2_e32 v152, v85
	v_cvt_f32_ubyte3_e32 v154, v85
	s_lshl_b32 s30, s98, 12
	s_add_u32 s28, s26, s30
	s_addc_u32 s29, s27, 0
	global_load_dwordx2 v[84:85], v162, s[28:29]
	v_cvt_f32_ubyte0_e32 v141, v86
	v_cvt_f32_ubyte1_e32 v143, v86
	v_cvt_f32_ubyte2_e32 v145, v86
	v_cvt_f32_ubyte3_e32 v147, v86
	v_cvt_f32_ubyte0_e32 v149, v87
	v_cvt_f32_ubyte1_e32 v151, v87
	v_cvt_f32_ubyte2_e32 v153, v87
	v_cvt_f32_ubyte3_e32 v155, v87
	s_lshl_b32 s30, s99, 12
	s_add_u32 s28, s26, s30
	s_addc_u32 s29, s27, 0
	global_load_dwordx2 v[86:87], v162, s[28:29]
	v_mul_f32_e32 v206, v124, v108
	v_mul_f32_e32 v207, v125, v108
	v_mul_f32_e32 v208, v140, v108
	v_mul_f32_e32 v209, v141, v108
	v_fmac_f32_e32 v206, v126, v109
	v_fmac_f32_e32 v207, v127, v109
	v_fmac_f32_e32 v208, v142, v109
	v_fmac_f32_e32 v209, v143, v109
	v_fmac_f32_e32 v206, v128, v110
	v_fmac_f32_e32 v207, v129, v110
	v_fmac_f32_e32 v208, v144, v110
	v_fmac_f32_e32 v209, v145, v110
	v_fmac_f32_e32 v206, v130, v111
	v_fmac_f32_e32 v207, v131, v111
	v_fmac_f32_e32 v208, v146, v111
	v_fmac_f32_e32 v209, v147, v111
	v_fmac_f32_e32 v206, v132, v112
	v_fmac_f32_e32 v207, v133, v112
	v_fmac_f32_e32 v208, v148, v112
	v_fmac_f32_e32 v209, v149, v112
	v_fmac_f32_e32 v206, v134, v113
	v_fmac_f32_e32 v207, v135, v113
	v_fmac_f32_e32 v208, v150, v113
	v_fmac_f32_e32 v209, v151, v113
	v_fmac_f32_e32 v206, v136, v114
	v_fmac_f32_e32 v207, v137, v114
	v_fmac_f32_e32 v208, v152, v114
	v_fmac_f32_e32 v209, v153, v114
	v_fmac_f32_e32 v206, v138, v115
	v_fmac_f32_e32 v207, v139, v115
	v_fmac_f32_e32 v208, v154, v115
	v_fmac_f32_e32 v209, v155, v115
	v_permlane32_swap_b32_e32 v178, v194
	v_permlane32_swap_b32_e32 v179, v195
	v_permlane32_swap_b32_e32 v180, v196
	v_permlane32_swap_b32_e32 v181, v197
	v_permlane32_swap_b32_e32 v182, v198
	v_permlane32_swap_b32_e32 v183, v199
	v_permlane32_swap_b32_e32 v184, v200
	v_permlane32_swap_b32_e32 v185, v201
	v_permlane32_swap_b32_e32 v186, v202
	v_permlane32_swap_b32_e32 v187, v203
	v_permlane32_swap_b32_e32 v188, v204
	v_permlane32_swap_b32_e32 v189, v205
	v_permlane32_swap_b32_e32 v190, v206
	v_permlane32_swap_b32_e32 v191, v207
	v_permlane32_swap_b32_e32 v192, v208
	v_permlane32_swap_b32_e32 v193, v209
	v_add_f32_e32 v178, v178, v194
	v_add_f32_e32 v179, v179, v195
	v_add_f32_e32 v180, v180, v196
	v_add_f32_e32 v181, v181, v197
	v_add_f32_e32 v182, v182, v198
	v_add_f32_e32 v183, v183, v199
	v_add_f32_e32 v184, v184, v200
	v_add_f32_e32 v185, v185, v201
	v_add_f32_e32 v186, v186, v202
	v_add_f32_e32 v187, v187, v203
	v_add_f32_e32 v188, v188, v204
	v_add_f32_e32 v189, v189, v205
	v_add_f32_e32 v190, v190, v206
	v_add_f32_e32 v191, v191, v207
	v_add_f32_e32 v192, v192, v208
	v_add_f32_e32 v193, v193, v209
	v_permlane16_swap_b32_e32 v178, v186
	v_permlane16_swap_b32_e32 v179, v187
	v_permlane16_swap_b32_e32 v180, v188
	v_permlane16_swap_b32_e32 v181, v189
	v_permlane16_swap_b32_e32 v182, v190
	v_permlane16_swap_b32_e32 v183, v191
	v_permlane16_swap_b32_e32 v184, v192
	v_permlane16_swap_b32_e32 v185, v193
	v_add_f32_e32 v178, v178, v186
	v_add_f32_e32 v179, v179, v187
	v_add_f32_e32 v180, v180, v188
	v_add_f32_e32 v181, v181, v189
	v_add_f32_e32 v182, v182, v190
	v_add_f32_e32 v183, v183, v191
	v_add_f32_e32 v184, v184, v192
	v_add_f32_e32 v185, v185, v193
	v_cndmask_b32_e64 v2, v178, v182, s[8:9]
	v_cndmask_b32_e64 v3, v179, v183, s[8:9]
	v_cndmask_b32_e64 v4, v180, v184, s[8:9]
	v_cndmask_b32_e64 v5, v181, v185, s[8:9]
	v_cndmask_b32_e64 v6, v182, v178, s[8:9]
	v_cndmask_b32_e64 v7, v183, v179, s[8:9]
	v_cndmask_b32_e64 v8, v184, v180, s[8:9]
	v_cndmask_b32_e64 v9, v185, v181, s[8:9]
	v_add_f32_dpp v6, v2, v6 row_ror:8 row_mask:0xf bank_mask:0xf
	v_add_f32_dpp v7, v3, v7 row_ror:8 row_mask:0xf bank_mask:0xf
	v_add_f32_dpp v8, v4, v8 row_ror:8 row_mask:0xf bank_mask:0xf
	v_add_f32_dpp v9, v5, v9 row_ror:8 row_mask:0xf bank_mask:0xf
	v_cndmask_b32_e64 v2, v6, v8, s[10:11]
	v_cndmask_b32_e64 v3, v7, v9, s[10:11]
	v_cndmask_b32_e64 v4, v8, v6, s[10:11]
	v_cndmask_b32_e64 v5, v9, v7, s[10:11]
	v_add_f32_dpp v4, v2, v4 row_half_mirror row_mask:0xf bank_mask:0xf
	v_add_f32_dpp v5, v3, v5 row_half_mirror row_mask:0xf bank_mask:0xf
	v_cndmask_b32_e64 v2, v4, v5, s[14:15]
	v_cndmask_b32_e64 v3, v5, v4, s[14:15]
	s_nop 0
	v_add_f32_dpp v3, v2, v3 quad_perm:[2,3,0,1] row_mask:0xf bank_mask:0xf
	s_nop 1
	v_add_f32_dpp v11, v3, v3 quad_perm:[1,0,3,2] row_mask:0xf bank_mask:0xf
	s_mov_b64 exec, s[2:3]
	global_store_dword v[22:23], v11, off
	s_mov_b64 exec, -1
	s_waitcnt vmcnt(29)
	v_cvt_f32_ubyte0_e32 v124, v24
	v_cvt_f32_ubyte1_e32 v126, v24
	v_cvt_f32_ubyte2_e32 v128, v24
	v_cvt_f32_ubyte3_e32 v130, v24
	v_cvt_f32_ubyte0_e32 v132, v25
	v_cvt_f32_ubyte1_e32 v134, v25
	v_cvt_f32_ubyte2_e32 v136, v25
	v_cvt_f32_ubyte3_e32 v138, v25
	s_waitcnt lgkmcnt(0)
	s_load_dwordx16 s[84:99], s[36:37], 0x140 glc
	s_lshl_b32 s30, s68, 12
	s_add_u32 s28, s26, s30
	s_addc_u32 s29, s27, 0
	global_load_dwordx2 v[24:25], v162, s[28:29]
	v_cvt_f32_ubyte0_e32 v125, v26
	v_cvt_f32_ubyte1_e32 v127, v26
	v_cvt_f32_ubyte2_e32 v129, v26
	v_cvt_f32_ubyte3_e32 v131, v26
	v_cvt_f32_ubyte0_e32 v133, v27
	v_cvt_f32_ubyte1_e32 v135, v27
	v_cvt_f32_ubyte2_e32 v137, v27
	v_cvt_f32_ubyte3_e32 v139, v27
	s_lshl_b32 s30, s69, 12
	s_add_u32 s28, s26, s30
	s_addc_u32 s29, s27, 0
	global_load_dwordx2 v[26:27], v162, s[28:29]
	v_cvt_f32_ubyte0_e32 v140, v28
	v_cvt_f32_ubyte1_e32 v142, v28
	v_cvt_f32_ubyte2_e32 v144, v28
	v_cvt_f32_ubyte3_e32 v146, v28
	v_cvt_f32_ubyte0_e32 v148, v29
	v_cvt_f32_ubyte1_e32 v150, v29
	v_cvt_f32_ubyte2_e32 v152, v29
	v_cvt_f32_ubyte3_e32 v154, v29
	s_lshl_b32 s30, s70, 12
	s_add_u32 s28, s26, s30
	s_addc_u32 s29, s27, 0
	global_load_dwordx2 v[28:29], v162, s[28:29]
	v_cvt_f32_ubyte0_e32 v141, v30
	v_cvt_f32_ubyte1_e32 v143, v30
	v_cvt_f32_ubyte2_e32 v145, v30
	v_cvt_f32_ubyte3_e32 v147, v30
	v_cvt_f32_ubyte0_e32 v149, v31
	v_cvt_f32_ubyte1_e32 v151, v31
	v_cvt_f32_ubyte2_e32 v153, v31
	v_cvt_f32_ubyte3_e32 v155, v31
	s_lshl_b32 s30, s71, 12
	s_add_u32 s28, s26, s30
	s_addc_u32 s29, s27, 0
	global_load_dwordx2 v[30:31], v162, s[28:29]
	v_mul_f32_e32 v178, v124, v108
	v_mul_f32_e32 v179, v125, v108
	v_mul_f32_e32 v180, v140, v108
	v_mul_f32_e32 v181, v141, v108
	v_fmac_f32_e32 v178, v126, v109
	v_fmac_f32_e32 v179, v127, v109
	v_fmac_f32_e32 v180, v142, v109
	v_fmac_f32_e32 v181, v143, v109
	v_fmac_f32_e32 v178, v128, v110
	v_fmac_f32_e32 v179, v129, v110
	v_fmac_f32_e32 v180, v144, v110
	v_fmac_f32_e32 v181, v145, v110
	v_fmac_f32_e32 v178, v130, v111
	v_fmac_f32_e32 v179, v131, v111
	v_fmac_f32_e32 v180, v146, v111
	v_fmac_f32_e32 v181, v147, v111
	v_fmac_f32_e32 v178, v132, v112
	v_fmac_f32_e32 v179, v133, v112
	v_fmac_f32_e32 v180, v148, v112
	v_fmac_f32_e32 v181, v149, v112
	v_fmac_f32_e32 v178, v134, v113
	v_fmac_f32_e32 v179, v135, v113
	v_fmac_f32_e32 v180, v150, v113
	v_fmac_f32_e32 v181, v151, v113
	v_fmac_f32_e32 v178, v136, v114
	v_fmac_f32_e32 v179, v137, v114
	v_fmac_f32_e32 v180, v152, v114
	v_fmac_f32_e32 v181, v153, v114
	v_fmac_f32_e32 v178, v138, v115
	v_fmac_f32_e32 v179, v139, v115
	v_fmac_f32_e32 v180, v154, v115
	v_fmac_f32_e32 v181, v155, v115
	s_waitcnt vmcnt(29)
	v_cvt_f32_ubyte0_e32 v124, v32
	v_cvt_f32_ubyte1_e32 v126, v32
	v_cvt_f32_ubyte2_e32 v128, v32
	v_cvt_f32_ubyte3_e32 v130, v32
	v_cvt_f32_ubyte0_e32 v132, v33
	v_cvt_f32_ubyte1_e32 v134, v33
	v_cvt_f32_ubyte2_e32 v136, v33
	v_cvt_f32_ubyte3_e32 v138, v33
	s_lshl_b32 s30, s72, 12
	s_add_u32 s28, s26, s30
	s_addc_u32 s29, s27, 0
	global_load_dwordx2 v[32:33], v162, s[28:29]
	v_cvt_f32_ubyte0_e32 v125, v34
	v_cvt_f32_ubyte1_e32 v127, v34
	v_cvt_f32_ubyte2_e32 v129, v34
	v_cvt_f32_ubyte3_e32 v131, v34
	v_cvt_f32_ubyte0_e32 v133, v35
	v_cvt_f32_ubyte1_e32 v135, v35
	v_cvt_f32_ubyte2_e32 v137, v35
	v_cvt_f32_ubyte3_e32 v139, v35
	s_lshl_b32 s30, s73, 12
	s_add_u32 s28, s26, s30
	s_addc_u32 s29, s27, 0
	global_load_dwordx2 v[34:35], v162, s[28:29]
	v_cvt_f32_ubyte0_e32 v140, v36
	v_cvt_f32_ubyte1_e32 v142, v36
	v_cvt_f32_ubyte2_e32 v144, v36
	v_cvt_f32_ubyte3_e32 v146, v36
	v_cvt_f32_ubyte0_e32 v148, v37
	v_cvt_f32_ubyte1_e32 v150, v37
	v_cvt_f32_ubyte2_e32 v152, v37
	v_cvt_f32_ubyte3_e32 v154, v37
	s_lshl_b32 s30, s74, 12
	s_add_u32 s28, s26, s30
	s_addc_u32 s29, s27, 0
	global_load_dwordx2 v[36:37], v162, s[28:29]
	v_cvt_f32_ubyte0_e32 v141, v38
	v_cvt_f32_ubyte1_e32 v143, v38
	v_cvt_f32_ubyte2_e32 v145, v38
	v_cvt_f32_ubyte3_e32 v147, v38
	v_cvt_f32_ubyte0_e32 v149, v39
	v_cvt_f32_ubyte1_e32 v151, v39
	v_cvt_f32_ubyte2_e32 v153, v39
	v_cvt_f32_ubyte3_e32 v155, v39
	s_lshl_b32 s30, s75, 12
	s_add_u32 s28, s26, s30
	s_addc_u32 s29, s27, 0
	global_load_dwordx2 v[38:39], v162, s[28:29]
	v_mul_f32_e32 v182, v124, v108
	v_mul_f32_e32 v183, v125, v108
	v_mul_f32_e32 v184, v140, v108
	v_mul_f32_e32 v185, v141, v108
	v_fmac_f32_e32 v182, v126, v109
	v_fmac_f32_e32 v183, v127, v109
	v_fmac_f32_e32 v184, v142, v109
	v_fmac_f32_e32 v185, v143, v109
	v_fmac_f32_e32 v182, v128, v110
	v_fmac_f32_e32 v183, v129, v110
	v_fmac_f32_e32 v184, v144, v110
	v_fmac_f32_e32 v185, v145, v110
	v_fmac_f32_e32 v182, v130, v111
	v_fmac_f32_e32 v183, v131, v111
	v_fmac_f32_e32 v184, v146, v111
	v_fmac_f32_e32 v185, v147, v111
	v_fmac_f32_e32 v182, v132, v112
	v_fmac_f32_e32 v183, v133, v112
	v_fmac_f32_e32 v184, v148, v112
	v_fmac_f32_e32 v185, v149, v112
	v_fmac_f32_e32 v182, v134, v113
	v_fmac_f32_e32 v183, v135, v113
	v_fmac_f32_e32 v184, v150, v113
	v_fmac_f32_e32 v185, v151, v113
	v_fmac_f32_e32 v182, v136, v114
	v_fmac_f32_e32 v183, v137, v114
	v_fmac_f32_e32 v184, v152, v114
	v_fmac_f32_e32 v185, v153, v114
	v_fmac_f32_e32 v182, v138, v115
	v_fmac_f32_e32 v183, v139, v115
	v_fmac_f32_e32 v184, v154, v115
	v_fmac_f32_e32 v185, v155, v115
	s_waitcnt vmcnt(29)
	v_cvt_f32_ubyte0_e32 v124, v40
	v_cvt_f32_ubyte1_e32 v126, v40
	v_cvt_f32_ubyte2_e32 v128, v40
	v_cvt_f32_ubyte3_e32 v130, v40
	v_cvt_f32_ubyte0_e32 v132, v41
	v_cvt_f32_ubyte1_e32 v134, v41
	v_cvt_f32_ubyte2_e32 v136, v41
	v_cvt_f32_ubyte3_e32 v138, v41
	s_lshl_b32 s30, s76, 12
	s_add_u32 s28, s26, s30
	s_addc_u32 s29, s27, 0
	global_load_dwordx2 v[40:41], v162, s[28:29]
	v_cvt_f32_ubyte0_e32 v125, v42
	v_cvt_f32_ubyte1_e32 v127, v42
	v_cvt_f32_ubyte2_e32 v129, v42
	v_cvt_f32_ubyte3_e32 v131, v42
	v_cvt_f32_ubyte0_e32 v133, v43
	v_cvt_f32_ubyte1_e32 v135, v43
	v_cvt_f32_ubyte2_e32 v137, v43
	v_cvt_f32_ubyte3_e32 v139, v43
	s_lshl_b32 s30, s77, 12
	s_add_u32 s28, s26, s30
	s_addc_u32 s29, s27, 0
	global_load_dwordx2 v[42:43], v162, s[28:29]
	v_cvt_f32_ubyte0_e32 v140, v44
	v_cvt_f32_ubyte1_e32 v142, v44
	v_cvt_f32_ubyte2_e32 v144, v44
	v_cvt_f32_ubyte3_e32 v146, v44
	v_cvt_f32_ubyte0_e32 v148, v45
	v_cvt_f32_ubyte1_e32 v150, v45
	v_cvt_f32_ubyte2_e32 v152, v45
	v_cvt_f32_ubyte3_e32 v154, v45
	s_lshl_b32 s30, s78, 12
	s_add_u32 s28, s26, s30
	s_addc_u32 s29, s27, 0
	global_load_dwordx2 v[44:45], v162, s[28:29]
	v_cvt_f32_ubyte0_e32 v141, v46
	v_cvt_f32_ubyte1_e32 v143, v46
	v_cvt_f32_ubyte2_e32 v145, v46
	v_cvt_f32_ubyte3_e32 v147, v46
	v_cvt_f32_ubyte0_e32 v149, v47
	v_cvt_f32_ubyte1_e32 v151, v47
	v_cvt_f32_ubyte2_e32 v153, v47
	v_cvt_f32_ubyte3_e32 v155, v47
	s_lshl_b32 s30, s79, 12
	s_add_u32 s28, s26, s30
	s_addc_u32 s29, s27, 0
	global_load_dwordx2 v[46:47], v162, s[28:29]
	v_mul_f32_e32 v186, v124, v108
	v_mul_f32_e32 v187, v125, v108
	v_mul_f32_e32 v188, v140, v108
	v_mul_f32_e32 v189, v141, v108
	v_fmac_f32_e32 v186, v126, v109
	v_fmac_f32_e32 v187, v127, v109
	v_fmac_f32_e32 v188, v142, v109
	v_fmac_f32_e32 v189, v143, v109
	v_fmac_f32_e32 v186, v128, v110
	v_fmac_f32_e32 v187, v129, v110
	v_fmac_f32_e32 v188, v144, v110
	v_fmac_f32_e32 v189, v145, v110
	v_fmac_f32_e32 v186, v130, v111
	v_fmac_f32_e32 v187, v131, v111
	v_fmac_f32_e32 v188, v146, v111
	v_fmac_f32_e32 v189, v147, v111
	v_fmac_f32_e32 v186, v132, v112
	v_fmac_f32_e32 v187, v133, v112
	v_fmac_f32_e32 v188, v148, v112
	v_fmac_f32_e32 v189, v149, v112
	v_fmac_f32_e32 v186, v134, v113
	v_fmac_f32_e32 v187, v135, v113
	v_fmac_f32_e32 v188, v150, v113
	v_fmac_f32_e32 v189, v151, v113
	v_fmac_f32_e32 v186, v136, v114
	v_fmac_f32_e32 v187, v137, v114
	v_fmac_f32_e32 v188, v152, v114
	v_fmac_f32_e32 v189, v153, v114
	v_fmac_f32_e32 v186, v138, v115
	v_fmac_f32_e32 v187, v139, v115
	v_fmac_f32_e32 v188, v154, v115
	v_fmac_f32_e32 v189, v155, v115
	s_waitcnt vmcnt(29)
	v_cvt_f32_ubyte0_e32 v124, v48
	v_cvt_f32_ubyte1_e32 v126, v48
	v_cvt_f32_ubyte2_e32 v128, v48
	v_cvt_f32_ubyte3_e32 v130, v48
	v_cvt_f32_ubyte0_e32 v132, v49
	v_cvt_f32_ubyte1_e32 v134, v49
	v_cvt_f32_ubyte2_e32 v136, v49
	v_cvt_f32_ubyte3_e32 v138, v49
	s_lshl_b32 s30, s80, 12
	s_add_u32 s28, s26, s30
	s_addc_u32 s29, s27, 0
	global_load_dwordx2 v[48:49], v162, s[28:29]
	v_cvt_f32_ubyte0_e32 v125, v50
	v_cvt_f32_ubyte1_e32 v127, v50
	v_cvt_f32_ubyte2_e32 v129, v50
	v_cvt_f32_ubyte3_e32 v131, v50
	v_cvt_f32_ubyte0_e32 v133, v51
	v_cvt_f32_ubyte1_e32 v135, v51
	v_cvt_f32_ubyte2_e32 v137, v51
	v_cvt_f32_ubyte3_e32 v139, v51
	s_lshl_b32 s30, s81, 12
	s_add_u32 s28, s26, s30
	s_addc_u32 s29, s27, 0
	global_load_dwordx2 v[50:51], v162, s[28:29]
	v_cvt_f32_ubyte0_e32 v140, v52
	v_cvt_f32_ubyte1_e32 v142, v52
	v_cvt_f32_ubyte2_e32 v144, v52
	v_cvt_f32_ubyte3_e32 v146, v52
	v_cvt_f32_ubyte0_e32 v148, v53
	v_cvt_f32_ubyte1_e32 v150, v53
	v_cvt_f32_ubyte2_e32 v152, v53
	v_cvt_f32_ubyte3_e32 v154, v53
	s_lshl_b32 s30, s82, 12
	s_add_u32 s28, s26, s30
	s_addc_u32 s29, s27, 0
	global_load_dwordx2 v[52:53], v162, s[28:29]
	v_cvt_f32_ubyte0_e32 v141, v54
	v_cvt_f32_ubyte1_e32 v143, v54
	v_cvt_f32_ubyte2_e32 v145, v54
	v_cvt_f32_ubyte3_e32 v147, v54
	v_cvt_f32_ubyte0_e32 v149, v55
	v_cvt_f32_ubyte1_e32 v151, v55
	v_cvt_f32_ubyte2_e32 v153, v55
	v_cvt_f32_ubyte3_e32 v155, v55
	s_lshl_b32 s30, s83, 12
	s_add_u32 s28, s26, s30
	s_addc_u32 s29, s27, 0
	global_load_dwordx2 v[54:55], v162, s[28:29]
	v_mul_f32_e32 v190, v124, v108
	v_mul_f32_e32 v191, v125, v108
	v_mul_f32_e32 v192, v140, v108
	v_mul_f32_e32 v193, v141, v108
	v_fmac_f32_e32 v190, v126, v109
	v_fmac_f32_e32 v191, v127, v109
	v_fmac_f32_e32 v192, v142, v109
	v_fmac_f32_e32 v193, v143, v109
	v_fmac_f32_e32 v190, v128, v110
	v_fmac_f32_e32 v191, v129, v110
	v_fmac_f32_e32 v192, v144, v110
	v_fmac_f32_e32 v193, v145, v110
	v_fmac_f32_e32 v190, v130, v111
	v_fmac_f32_e32 v191, v131, v111
	v_fmac_f32_e32 v192, v146, v111
	v_fmac_f32_e32 v193, v147, v111
	v_fmac_f32_e32 v190, v132, v112
	v_fmac_f32_e32 v191, v133, v112
	v_fmac_f32_e32 v192, v148, v112
	v_fmac_f32_e32 v193, v149, v112
	v_fmac_f32_e32 v190, v134, v113
	v_fmac_f32_e32 v191, v135, v113
	v_fmac_f32_e32 v192, v150, v113
	v_fmac_f32_e32 v193, v151, v113
	v_fmac_f32_e32 v190, v136, v114
	v_fmac_f32_e32 v191, v137, v114
	v_fmac_f32_e32 v192, v152, v114
	v_fmac_f32_e32 v193, v153, v114
	v_fmac_f32_e32 v190, v138, v115
	v_fmac_f32_e32 v191, v139, v115
	v_fmac_f32_e32 v192, v154, v115
	v_fmac_f32_e32 v193, v155, v115
	s_waitcnt vmcnt(29)
	v_cvt_f32_ubyte0_e32 v124, v56
	v_cvt_f32_ubyte1_e32 v126, v56
	v_cvt_f32_ubyte2_e32 v128, v56
	v_cvt_f32_ubyte3_e32 v130, v56
	v_cvt_f32_ubyte0_e32 v132, v57
	v_cvt_f32_ubyte1_e32 v134, v57
	v_cvt_f32_ubyte2_e32 v136, v57
	v_cvt_f32_ubyte3_e32 v138, v57
	s_waitcnt lgkmcnt(0)
	s_load_dwordx16 s[68:83], s[36:37], 0x180 glc
	s_lshl_b32 s30, s84, 12
	s_add_u32 s28, s26, s30
	s_addc_u32 s29, s27, 0
	global_load_dwordx2 v[56:57], v162, s[28:29]
	v_cvt_f32_ubyte0_e32 v125, v58
	v_cvt_f32_ubyte1_e32 v127, v58
	v_cvt_f32_ubyte2_e32 v129, v58
	v_cvt_f32_ubyte3_e32 v131, v58
	v_cvt_f32_ubyte0_e32 v133, v59
	v_cvt_f32_ubyte1_e32 v135, v59
	v_cvt_f32_ubyte2_e32 v137, v59
	v_cvt_f32_ubyte3_e32 v139, v59
	s_lshl_b32 s30, s85, 12
	s_add_u32 s28, s26, s30
	s_addc_u32 s29, s27, 0
	global_load_dwordx2 v[58:59], v162, s[28:29]
	v_cvt_f32_ubyte0_e32 v140, v60
	v_cvt_f32_ubyte1_e32 v142, v60
	v_cvt_f32_ubyte2_e32 v144, v60
	v_cvt_f32_ubyte3_e32 v146, v60
	v_cvt_f32_ubyte0_e32 v148, v61
	v_cvt_f32_ubyte1_e32 v150, v61
	v_cvt_f32_ubyte2_e32 v152, v61
	v_cvt_f32_ubyte3_e32 v154, v61
	s_lshl_b32 s30, s86, 12
	s_add_u32 s28, s26, s30
	s_addc_u32 s29, s27, 0
	global_load_dwordx2 v[60:61], v162, s[28:29]
	v_cvt_f32_ubyte0_e32 v141, v62
	v_cvt_f32_ubyte1_e32 v143, v62
	v_cvt_f32_ubyte2_e32 v145, v62
	v_cvt_f32_ubyte3_e32 v147, v62
	v_cvt_f32_ubyte0_e32 v149, v63
	v_cvt_f32_ubyte1_e32 v151, v63
	v_cvt_f32_ubyte2_e32 v153, v63
	v_cvt_f32_ubyte3_e32 v155, v63
	s_lshl_b32 s30, s87, 12
	s_add_u32 s28, s26, s30
	s_addc_u32 s29, s27, 0
	global_load_dwordx2 v[62:63], v162, s[28:29]
	v_mul_f32_e32 v194, v124, v108
	v_mul_f32_e32 v195, v125, v108
	v_mul_f32_e32 v196, v140, v108
	v_mul_f32_e32 v197, v141, v108
	v_fmac_f32_e32 v194, v126, v109
	v_fmac_f32_e32 v195, v127, v109
	v_fmac_f32_e32 v196, v142, v109
	v_fmac_f32_e32 v197, v143, v109
	v_fmac_f32_e32 v194, v128, v110
	v_fmac_f32_e32 v195, v129, v110
	v_fmac_f32_e32 v196, v144, v110
	v_fmac_f32_e32 v197, v145, v110
	v_fmac_f32_e32 v194, v130, v111
	v_fmac_f32_e32 v195, v131, v111
	v_fmac_f32_e32 v196, v146, v111
	v_fmac_f32_e32 v197, v147, v111
	v_fmac_f32_e32 v194, v132, v112
	v_fmac_f32_e32 v195, v133, v112
	v_fmac_f32_e32 v196, v148, v112
	v_fmac_f32_e32 v197, v149, v112
	v_fmac_f32_e32 v194, v134, v113
	v_fmac_f32_e32 v195, v135, v113
	v_fmac_f32_e32 v196, v150, v113
	v_fmac_f32_e32 v197, v151, v113
	v_fmac_f32_e32 v194, v136, v114
	v_fmac_f32_e32 v195, v137, v114
	v_fmac_f32_e32 v196, v152, v114
	v_fmac_f32_e32 v197, v153, v114
	v_fmac_f32_e32 v194, v138, v115
	v_fmac_f32_e32 v195, v139, v115
	v_fmac_f32_e32 v196, v154, v115
	v_fmac_f32_e32 v197, v155, v115
	s_waitcnt vmcnt(29)
	v_cvt_f32_ubyte0_e32 v124, v64
	v_cvt_f32_ubyte1_e32 v126, v64
	v_cvt_f32_ubyte2_e32 v128, v64
	v_cvt_f32_ubyte3_e32 v130, v64
	v_cvt_f32_ubyte0_e32 v132, v65
	v_cvt_f32_ubyte1_e32 v134, v65
	v_cvt_f32_ubyte2_e32 v136, v65
	v_cvt_f32_ubyte3_e32 v138, v65
	s_lshl_b32 s30, s88, 12
	s_add_u32 s28, s26, s30
	s_addc_u32 s29, s27, 0
	global_load_dwordx2 v[64:65], v162, s[28:29]
	v_cvt_f32_ubyte0_e32 v125, v66
	v_cvt_f32_ubyte1_e32 v127, v66
	v_cvt_f32_ubyte2_e32 v129, v66
	v_cvt_f32_ubyte3_e32 v131, v66
	v_cvt_f32_ubyte0_e32 v133, v67
	v_cvt_f32_ubyte1_e32 v135, v67
	v_cvt_f32_ubyte2_e32 v137, v67
	v_cvt_f32_ubyte3_e32 v139, v67
	s_lshl_b32 s30, s89, 12
	s_add_u32 s28, s26, s30
	s_addc_u32 s29, s27, 0
	global_load_dwordx2 v[66:67], v162, s[28:29]
	v_cvt_f32_ubyte0_e32 v140, v68
	v_cvt_f32_ubyte1_e32 v142, v68
	v_cvt_f32_ubyte2_e32 v144, v68
	v_cvt_f32_ubyte3_e32 v146, v68
	v_cvt_f32_ubyte0_e32 v148, v69
	v_cvt_f32_ubyte1_e32 v150, v69
	v_cvt_f32_ubyte2_e32 v152, v69
	v_cvt_f32_ubyte3_e32 v154, v69
	s_lshl_b32 s30, s90, 12
	s_add_u32 s28, s26, s30
	s_addc_u32 s29, s27, 0
	global_load_dwordx2 v[68:69], v162, s[28:29]
	v_cvt_f32_ubyte0_e32 v141, v70
	v_cvt_f32_ubyte1_e32 v143, v70
	v_cvt_f32_ubyte2_e32 v145, v70
	v_cvt_f32_ubyte3_e32 v147, v70
	v_cvt_f32_ubyte0_e32 v149, v71
	v_cvt_f32_ubyte1_e32 v151, v71
	v_cvt_f32_ubyte2_e32 v153, v71
	v_cvt_f32_ubyte3_e32 v155, v71
	s_lshl_b32 s30, s91, 12
	s_add_u32 s28, s26, s30
	s_addc_u32 s29, s27, 0
	global_load_dwordx2 v[70:71], v162, s[28:29]
	v_mul_f32_e32 v198, v124, v108
	v_mul_f32_e32 v199, v125, v108
	v_mul_f32_e32 v200, v140, v108
	v_mul_f32_e32 v201, v141, v108
	v_fmac_f32_e32 v198, v126, v109
	v_fmac_f32_e32 v199, v127, v109
	v_fmac_f32_e32 v200, v142, v109
	v_fmac_f32_e32 v201, v143, v109
	v_fmac_f32_e32 v198, v128, v110
	v_fmac_f32_e32 v199, v129, v110
	v_fmac_f32_e32 v200, v144, v110
	v_fmac_f32_e32 v201, v145, v110
	v_fmac_f32_e32 v198, v130, v111
	v_fmac_f32_e32 v199, v131, v111
	v_fmac_f32_e32 v200, v146, v111
	v_fmac_f32_e32 v201, v147, v111
	v_fmac_f32_e32 v198, v132, v112
	v_fmac_f32_e32 v199, v133, v112
	v_fmac_f32_e32 v200, v148, v112
	v_fmac_f32_e32 v201, v149, v112
	v_fmac_f32_e32 v198, v134, v113
	v_fmac_f32_e32 v199, v135, v113
	v_fmac_f32_e32 v200, v150, v113
	v_fmac_f32_e32 v201, v151, v113
	v_fmac_f32_e32 v198, v136, v114
	v_fmac_f32_e32 v199, v137, v114
	v_fmac_f32_e32 v200, v152, v114
	v_fmac_f32_e32 v201, v153, v114
	v_fmac_f32_e32 v198, v138, v115
	v_fmac_f32_e32 v199, v139, v115
	v_fmac_f32_e32 v200, v154, v115
	v_fmac_f32_e32 v201, v155, v115
	s_waitcnt vmcnt(29)
	v_cvt_f32_ubyte0_e32 v124, v72
	v_cvt_f32_ubyte1_e32 v126, v72
	v_cvt_f32_ubyte2_e32 v128, v72
	v_cvt_f32_ubyte3_e32 v130, v72
	v_cvt_f32_ubyte0_e32 v132, v73
	v_cvt_f32_ubyte1_e32 v134, v73
	v_cvt_f32_ubyte2_e32 v136, v73
	v_cvt_f32_ubyte3_e32 v138, v73
	s_lshl_b32 s30, s92, 12
	s_add_u32 s28, s26, s30
	s_addc_u32 s29, s27, 0
	global_load_dwordx2 v[72:73], v162, s[28:29]
	v_cvt_f32_ubyte0_e32 v125, v74
	v_cvt_f32_ubyte1_e32 v127, v74
	v_cvt_f32_ubyte2_e32 v129, v74
	v_cvt_f32_ubyte3_e32 v131, v74
	v_cvt_f32_ubyte0_e32 v133, v75
	v_cvt_f32_ubyte1_e32 v135, v75
	v_cvt_f32_ubyte2_e32 v137, v75
	v_cvt_f32_ubyte3_e32 v139, v75
	s_lshl_b32 s30, s93, 12
	s_add_u32 s28, s26, s30
	s_addc_u32 s29, s27, 0
	global_load_dwordx2 v[74:75], v162, s[28:29]
	v_cvt_f32_ubyte0_e32 v140, v76
	v_cvt_f32_ubyte1_e32 v142, v76
	v_cvt_f32_ubyte2_e32 v144, v76
	v_cvt_f32_ubyte3_e32 v146, v76
	v_cvt_f32_ubyte0_e32 v148, v77
	v_cvt_f32_ubyte1_e32 v150, v77
	v_cvt_f32_ubyte2_e32 v152, v77
	v_cvt_f32_ubyte3_e32 v154, v77
	s_lshl_b32 s30, s94, 12
	s_add_u32 s28, s26, s30
	s_addc_u32 s29, s27, 0
	global_load_dwordx2 v[76:77], v162, s[28:29]
	v_cvt_f32_ubyte0_e32 v141, v78
	v_cvt_f32_ubyte1_e32 v143, v78
	v_cvt_f32_ubyte2_e32 v145, v78
	v_cvt_f32_ubyte3_e32 v147, v78
	v_cvt_f32_ubyte0_e32 v149, v79
	v_cvt_f32_ubyte1_e32 v151, v79
	v_cvt_f32_ubyte2_e32 v153, v79
	v_cvt_f32_ubyte3_e32 v155, v79
	s_lshl_b32 s30, s95, 12
	s_add_u32 s28, s26, s30
	s_addc_u32 s29, s27, 0
	global_load_dwordx2 v[78:79], v162, s[28:29]
	v_mul_f32_e32 v202, v124, v108
	v_mul_f32_e32 v203, v125, v108
	v_mul_f32_e32 v204, v140, v108
	v_mul_f32_e32 v205, v141, v108
	v_fmac_f32_e32 v202, v126, v109
	v_fmac_f32_e32 v203, v127, v109
	v_fmac_f32_e32 v204, v142, v109
	v_fmac_f32_e32 v205, v143, v109
	v_fmac_f32_e32 v202, v128, v110
	v_fmac_f32_e32 v203, v129, v110
	v_fmac_f32_e32 v204, v144, v110
	v_fmac_f32_e32 v205, v145, v110
	v_fmac_f32_e32 v202, v130, v111
	v_fmac_f32_e32 v203, v131, v111
	v_fmac_f32_e32 v204, v146, v111
	v_fmac_f32_e32 v205, v147, v111
	v_fmac_f32_e32 v202, v132, v112
	v_fmac_f32_e32 v203, v133, v112
	v_fmac_f32_e32 v204, v148, v112
	v_fmac_f32_e32 v205, v149, v112
	v_fmac_f32_e32 v202, v134, v113
	v_fmac_f32_e32 v203, v135, v113
	v_fmac_f32_e32 v204, v150, v113
	v_fmac_f32_e32 v205, v151, v113
	v_fmac_f32_e32 v202, v136, v114
	v_fmac_f32_e32 v203, v137, v114
	v_fmac_f32_e32 v204, v152, v114
	v_fmac_f32_e32 v205, v153, v114
	v_fmac_f32_e32 v202, v138, v115
	v_fmac_f32_e32 v203, v139, v115
	v_fmac_f32_e32 v204, v154, v115
	v_fmac_f32_e32 v205, v155, v115
	s_waitcnt vmcnt(29)
	v_cvt_f32_ubyte0_e32 v124, v80
	v_cvt_f32_ubyte1_e32 v126, v80
	v_cvt_f32_ubyte2_e32 v128, v80
	v_cvt_f32_ubyte3_e32 v130, v80
	v_cvt_f32_ubyte0_e32 v132, v81
	v_cvt_f32_ubyte1_e32 v134, v81
	v_cvt_f32_ubyte2_e32 v136, v81
	v_cvt_f32_ubyte3_e32 v138, v81
	s_lshl_b32 s30, s96, 12
	s_add_u32 s28, s26, s30
	s_addc_u32 s29, s27, 0
	global_load_dwordx2 v[80:81], v162, s[28:29]
	v_cvt_f32_ubyte0_e32 v125, v82
	v_cvt_f32_ubyte1_e32 v127, v82
	v_cvt_f32_ubyte2_e32 v129, v82
	v_cvt_f32_ubyte3_e32 v131, v82
	v_cvt_f32_ubyte0_e32 v133, v83
	v_cvt_f32_ubyte1_e32 v135, v83
	v_cvt_f32_ubyte2_e32 v137, v83
	v_cvt_f32_ubyte3_e32 v139, v83
	s_lshl_b32 s30, s97, 12
	s_add_u32 s28, s26, s30
	s_addc_u32 s29, s27, 0
	global_load_dwordx2 v[82:83], v162, s[28:29]
	v_cvt_f32_ubyte0_e32 v140, v84
	v_cvt_f32_ubyte1_e32 v142, v84
	v_cvt_f32_ubyte2_e32 v144, v84
	v_cvt_f32_ubyte3_e32 v146, v84
	v_cvt_f32_ubyte0_e32 v148, v85
	v_cvt_f32_ubyte1_e32 v150, v85
	v_cvt_f32_ubyte2_e32 v152, v85
	v_cvt_f32_ubyte3_e32 v154, v85
	s_lshl_b32 s30, s98, 12
	s_add_u32 s28, s26, s30
	s_addc_u32 s29, s27, 0
	global_load_dwordx2 v[84:85], v162, s[28:29]
	v_cvt_f32_ubyte0_e32 v141, v86
	v_cvt_f32_ubyte1_e32 v143, v86
	v_cvt_f32_ubyte2_e32 v145, v86
	v_cvt_f32_ubyte3_e32 v147, v86
	v_cvt_f32_ubyte0_e32 v149, v87
	v_cvt_f32_ubyte1_e32 v151, v87
	v_cvt_f32_ubyte2_e32 v153, v87
	v_cvt_f32_ubyte3_e32 v155, v87
	s_lshl_b32 s30, s99, 12
	s_add_u32 s28, s26, s30
	s_addc_u32 s29, s27, 0
	global_load_dwordx2 v[86:87], v162, s[28:29]
	v_mul_f32_e32 v206, v124, v108
	v_mul_f32_e32 v207, v125, v108
	v_mul_f32_e32 v208, v140, v108
	v_mul_f32_e32 v209, v141, v108
	v_fmac_f32_e32 v206, v126, v109
	v_fmac_f32_e32 v207, v127, v109
	v_fmac_f32_e32 v208, v142, v109
	v_fmac_f32_e32 v209, v143, v109
	v_fmac_f32_e32 v206, v128, v110
	v_fmac_f32_e32 v207, v129, v110
	v_fmac_f32_e32 v208, v144, v110
	v_fmac_f32_e32 v209, v145, v110
	v_fmac_f32_e32 v206, v130, v111
	v_fmac_f32_e32 v207, v131, v111
	v_fmac_f32_e32 v208, v146, v111
	v_fmac_f32_e32 v209, v147, v111
	v_fmac_f32_e32 v206, v132, v112
	v_fmac_f32_e32 v207, v133, v112
	v_fmac_f32_e32 v208, v148, v112
	v_fmac_f32_e32 v209, v149, v112
	v_fmac_f32_e32 v206, v134, v113
	v_fmac_f32_e32 v207, v135, v113
	v_fmac_f32_e32 v208, v150, v113
	v_fmac_f32_e32 v209, v151, v113
	v_fmac_f32_e32 v206, v136, v114
	v_fmac_f32_e32 v207, v137, v114
	v_fmac_f32_e32 v208, v152, v114
	v_fmac_f32_e32 v209, v153, v114
	v_fmac_f32_e32 v206, v138, v115
	v_fmac_f32_e32 v207, v139, v115
	v_fmac_f32_e32 v208, v154, v115
	v_fmac_f32_e32 v209, v155, v115
	v_permlane32_swap_b32_e32 v178, v194
	v_permlane32_swap_b32_e32 v179, v195
	v_permlane32_swap_b32_e32 v180, v196
	v_permlane32_swap_b32_e32 v181, v197
	v_permlane32_swap_b32_e32 v182, v198
	v_permlane32_swap_b32_e32 v183, v199
	v_permlane32_swap_b32_e32 v184, v200
	v_permlane32_swap_b32_e32 v185, v201
	v_permlane32_swap_b32_e32 v186, v202
	v_permlane32_swap_b32_e32 v187, v203
	v_permlane32_swap_b32_e32 v188, v204
	v_permlane32_swap_b32_e32 v189, v205
	v_permlane32_swap_b32_e32 v190, v206
	v_permlane32_swap_b32_e32 v191, v207
	v_permlane32_swap_b32_e32 v192, v208
	v_permlane32_swap_b32_e32 v193, v209
	v_add_f32_e32 v178, v178, v194
	v_add_f32_e32 v179, v179, v195
	v_add_f32_e32 v180, v180, v196
	v_add_f32_e32 v181, v181, v197
	v_add_f32_e32 v182, v182, v198
	v_add_f32_e32 v183, v183, v199
	v_add_f32_e32 v184, v184, v200
	v_add_f32_e32 v185, v185, v201
	v_add_f32_e32 v186, v186, v202
	v_add_f32_e32 v187, v187, v203
	v_add_f32_e32 v188, v188, v204
	v_add_f32_e32 v189, v189, v205
	v_add_f32_e32 v190, v190, v206
	v_add_f32_e32 v191, v191, v207
	v_add_f32_e32 v192, v192, v208
	v_add_f32_e32 v193, v193, v209
	v_permlane16_swap_b32_e32 v178, v186
	v_permlane16_swap_b32_e32 v179, v187
	v_permlane16_swap_b32_e32 v180, v188
	v_permlane16_swap_b32_e32 v181, v189
	v_permlane16_swap_b32_e32 v182, v190
	v_permlane16_swap_b32_e32 v183, v191
	v_permlane16_swap_b32_e32 v184, v192
	v_permlane16_swap_b32_e32 v185, v193
	v_add_f32_e32 v178, v178, v186
	v_add_f32_e32 v179, v179, v187
	v_add_f32_e32 v180, v180, v188
	v_add_f32_e32 v181, v181, v189
	v_add_f32_e32 v182, v182, v190
	v_add_f32_e32 v183, v183, v191
	v_add_f32_e32 v184, v184, v192
	v_add_f32_e32 v185, v185, v193
	v_cndmask_b32_e64 v2, v178, v182, s[8:9]
	v_cndmask_b32_e64 v3, v179, v183, s[8:9]
	v_cndmask_b32_e64 v4, v180, v184, s[8:9]
	v_cndmask_b32_e64 v5, v181, v185, s[8:9]
	v_cndmask_b32_e64 v6, v182, v178, s[8:9]
	v_cndmask_b32_e64 v7, v183, v179, s[8:9]
	v_cndmask_b32_e64 v8, v184, v180, s[8:9]
	v_cndmask_b32_e64 v9, v185, v181, s[8:9]
	v_add_f32_dpp v6, v2, v6 row_ror:8 row_mask:0xf bank_mask:0xf
	v_add_f32_dpp v7, v3, v7 row_ror:8 row_mask:0xf bank_mask:0xf
	v_add_f32_dpp v8, v4, v8 row_ror:8 row_mask:0xf bank_mask:0xf
	v_add_f32_dpp v9, v5, v9 row_ror:8 row_mask:0xf bank_mask:0xf
	v_cndmask_b32_e64 v2, v6, v8, s[10:11]
	v_cndmask_b32_e64 v3, v7, v9, s[10:11]
	v_cndmask_b32_e64 v4, v8, v6, s[10:11]
	v_cndmask_b32_e64 v5, v9, v7, s[10:11]
	v_add_f32_dpp v4, v2, v4 row_half_mirror row_mask:0xf bank_mask:0xf
	v_add_f32_dpp v5, v3, v5 row_half_mirror row_mask:0xf bank_mask:0xf
	v_cndmask_b32_e64 v2, v4, v5, s[14:15]
	v_cndmask_b32_e64 v3, v5, v4, s[14:15]
	s_nop 0
	v_add_f32_dpp v3, v2, v3 quad_perm:[2,3,0,1] row_mask:0xf bank_mask:0xf
	s_nop 1
	v_add_f32_dpp v11, v3, v3 quad_perm:[1,0,3,2] row_mask:0xf bank_mask:0xf
	s_mov_b64 exec, s[2:3]
	global_store_dword v[22:23], v11, off offset:128
	s_mov_b64 exec, -1
	s_waitcnt vmcnt(29)
	v_cvt_f32_ubyte0_e32 v124, v24
	v_cvt_f32_ubyte1_e32 v126, v24
	v_cvt_f32_ubyte2_e32 v128, v24
	v_cvt_f32_ubyte3_e32 v130, v24
	v_cvt_f32_ubyte0_e32 v132, v25
	v_cvt_f32_ubyte1_e32 v134, v25
	v_cvt_f32_ubyte2_e32 v136, v25
	v_cvt_f32_ubyte3_e32 v138, v25
	s_waitcnt lgkmcnt(0)
	s_load_dwordx16 s[84:99], s[36:37], 0x1c0 glc
	s_lshl_b32 s30, s68, 12
	s_add_u32 s28, s26, s30
	s_addc_u32 s29, s27, 0
	global_load_dwordx2 v[24:25], v162, s[28:29]
	v_cvt_f32_ubyte0_e32 v125, v26
	v_cvt_f32_ubyte1_e32 v127, v26
	v_cvt_f32_ubyte2_e32 v129, v26
	v_cvt_f32_ubyte3_e32 v131, v26
	v_cvt_f32_ubyte0_e32 v133, v27
	v_cvt_f32_ubyte1_e32 v135, v27
	v_cvt_f32_ubyte2_e32 v137, v27
	v_cvt_f32_ubyte3_e32 v139, v27
	s_lshl_b32 s30, s69, 12
	s_add_u32 s28, s26, s30
	s_addc_u32 s29, s27, 0
	global_load_dwordx2 v[26:27], v162, s[28:29]
	v_cvt_f32_ubyte0_e32 v140, v28
	v_cvt_f32_ubyte1_e32 v142, v28
	v_cvt_f32_ubyte2_e32 v144, v28
	v_cvt_f32_ubyte3_e32 v146, v28
	v_cvt_f32_ubyte0_e32 v148, v29
	v_cvt_f32_ubyte1_e32 v150, v29
	v_cvt_f32_ubyte2_e32 v152, v29
	v_cvt_f32_ubyte3_e32 v154, v29
	s_lshl_b32 s30, s70, 12
	s_add_u32 s28, s26, s30
	s_addc_u32 s29, s27, 0
	global_load_dwordx2 v[28:29], v162, s[28:29]
	v_cvt_f32_ubyte0_e32 v141, v30
	v_cvt_f32_ubyte1_e32 v143, v30
	v_cvt_f32_ubyte2_e32 v145, v30
	v_cvt_f32_ubyte3_e32 v147, v30
	v_cvt_f32_ubyte0_e32 v149, v31
	v_cvt_f32_ubyte1_e32 v151, v31
	v_cvt_f32_ubyte2_e32 v153, v31
	v_cvt_f32_ubyte3_e32 v155, v31
	s_lshl_b32 s30, s71, 12
	s_add_u32 s28, s26, s30
	s_addc_u32 s29, s27, 0
	global_load_dwordx2 v[30:31], v162, s[28:29]
	v_mul_f32_e32 v178, v124, v108
	v_mul_f32_e32 v179, v125, v108
	v_mul_f32_e32 v180, v140, v108
	v_mul_f32_e32 v181, v141, v108
	v_fmac_f32_e32 v178, v126, v109
	v_fmac_f32_e32 v179, v127, v109
	v_fmac_f32_e32 v180, v142, v109
	v_fmac_f32_e32 v181, v143, v109
	v_fmac_f32_e32 v178, v128, v110
	v_fmac_f32_e32 v179, v129, v110
	v_fmac_f32_e32 v180, v144, v110
	v_fmac_f32_e32 v181, v145, v110
	v_fmac_f32_e32 v178, v130, v111
	v_fmac_f32_e32 v179, v131, v111
	v_fmac_f32_e32 v180, v146, v111
	v_fmac_f32_e32 v181, v147, v111
	v_fmac_f32_e32 v178, v132, v112
	v_fmac_f32_e32 v179, v133, v112
	v_fmac_f32_e32 v180, v148, v112
	v_fmac_f32_e32 v181, v149, v112
	v_fmac_f32_e32 v178, v134, v113
	v_fmac_f32_e32 v179, v135, v113
	v_fmac_f32_e32 v180, v150, v113
	v_fmac_f32_e32 v181, v151, v113
	v_fmac_f32_e32 v178, v136, v114
	v_fmac_f32_e32 v179, v137, v114
	v_fmac_f32_e32 v180, v152, v114
	v_fmac_f32_e32 v181, v153, v114
	v_fmac_f32_e32 v178, v138, v115
	v_fmac_f32_e32 v179, v139, v115
	v_fmac_f32_e32 v180, v154, v115
	v_fmac_f32_e32 v181, v155, v115
	s_waitcnt vmcnt(29)
	v_cvt_f32_ubyte0_e32 v124, v32
	v_cvt_f32_ubyte1_e32 v126, v32
	v_cvt_f32_ubyte2_e32 v128, v32
	v_cvt_f32_ubyte3_e32 v130, v32
	v_cvt_f32_ubyte0_e32 v132, v33
	v_cvt_f32_ubyte1_e32 v134, v33
	v_cvt_f32_ubyte2_e32 v136, v33
	v_cvt_f32_ubyte3_e32 v138, v33
	s_lshl_b32 s30, s72, 12
	s_add_u32 s28, s26, s30
	s_addc_u32 s29, s27, 0
	global_load_dwordx2 v[32:33], v162, s[28:29]
	v_cvt_f32_ubyte0_e32 v125, v34
	v_cvt_f32_ubyte1_e32 v127, v34
	v_cvt_f32_ubyte2_e32 v129, v34
	v_cvt_f32_ubyte3_e32 v131, v34
	v_cvt_f32_ubyte0_e32 v133, v35
	v_cvt_f32_ubyte1_e32 v135, v35
	v_cvt_f32_ubyte2_e32 v137, v35
	v_cvt_f32_ubyte3_e32 v139, v35
	s_lshl_b32 s30, s73, 12
	s_add_u32 s28, s26, s30
	s_addc_u32 s29, s27, 0
	global_load_dwordx2 v[34:35], v162, s[28:29]
	v_cvt_f32_ubyte0_e32 v140, v36
	v_cvt_f32_ubyte1_e32 v142, v36
	v_cvt_f32_ubyte2_e32 v144, v36
	v_cvt_f32_ubyte3_e32 v146, v36
	v_cvt_f32_ubyte0_e32 v148, v37
	v_cvt_f32_ubyte1_e32 v150, v37
	v_cvt_f32_ubyte2_e32 v152, v37
	v_cvt_f32_ubyte3_e32 v154, v37
	s_lshl_b32 s30, s74, 12
	s_add_u32 s28, s26, s30
	s_addc_u32 s29, s27, 0
	global_load_dwordx2 v[36:37], v162, s[28:29]
	v_cvt_f32_ubyte0_e32 v141, v38
	v_cvt_f32_ubyte1_e32 v143, v38
	v_cvt_f32_ubyte2_e32 v145, v38
	v_cvt_f32_ubyte3_e32 v147, v38
	v_cvt_f32_ubyte0_e32 v149, v39
	v_cvt_f32_ubyte1_e32 v151, v39
	v_cvt_f32_ubyte2_e32 v153, v39
	v_cvt_f32_ubyte3_e32 v155, v39
	s_lshl_b32 s30, s75, 12
	s_add_u32 s28, s26, s30
	s_addc_u32 s29, s27, 0
	global_load_dwordx2 v[38:39], v162, s[28:29]
	v_mul_f32_e32 v182, v124, v108
	v_mul_f32_e32 v183, v125, v108
	v_mul_f32_e32 v184, v140, v108
	v_mul_f32_e32 v185, v141, v108
	v_fmac_f32_e32 v182, v126, v109
	v_fmac_f32_e32 v183, v127, v109
	v_fmac_f32_e32 v184, v142, v109
	v_fmac_f32_e32 v185, v143, v109
	v_fmac_f32_e32 v182, v128, v110
	v_fmac_f32_e32 v183, v129, v110
	v_fmac_f32_e32 v184, v144, v110
	v_fmac_f32_e32 v185, v145, v110
	v_fmac_f32_e32 v182, v130, v111
	v_fmac_f32_e32 v183, v131, v111
	v_fmac_f32_e32 v184, v146, v111
	v_fmac_f32_e32 v185, v147, v111
	v_fmac_f32_e32 v182, v132, v112
	v_fmac_f32_e32 v183, v133, v112
	v_fmac_f32_e32 v184, v148, v112
	v_fmac_f32_e32 v185, v149, v112
	v_fmac_f32_e32 v182, v134, v113
	v_fmac_f32_e32 v183, v135, v113
	v_fmac_f32_e32 v184, v150, v113
	v_fmac_f32_e32 v185, v151, v113
	v_fmac_f32_e32 v182, v136, v114
	v_fmac_f32_e32 v183, v137, v114
	v_fmac_f32_e32 v184, v152, v114
	v_fmac_f32_e32 v185, v153, v114
	v_fmac_f32_e32 v182, v138, v115
	v_fmac_f32_e32 v183, v139, v115
	v_fmac_f32_e32 v184, v154, v115
	v_fmac_f32_e32 v185, v155, v115
	s_waitcnt vmcnt(29)
	v_cvt_f32_ubyte0_e32 v124, v40
	v_cvt_f32_ubyte1_e32 v126, v40
	v_cvt_f32_ubyte2_e32 v128, v40
	v_cvt_f32_ubyte3_e32 v130, v40
	v_cvt_f32_ubyte0_e32 v132, v41
	v_cvt_f32_ubyte1_e32 v134, v41
	v_cvt_f32_ubyte2_e32 v136, v41
	v_cvt_f32_ubyte3_e32 v138, v41
	s_lshl_b32 s30, s76, 12
	s_add_u32 s28, s26, s30
	s_addc_u32 s29, s27, 0
	global_load_dwordx2 v[40:41], v162, s[28:29]
	v_cvt_f32_ubyte0_e32 v125, v42
	v_cvt_f32_ubyte1_e32 v127, v42
	v_cvt_f32_ubyte2_e32 v129, v42
	v_cvt_f32_ubyte3_e32 v131, v42
	v_cvt_f32_ubyte0_e32 v133, v43
	v_cvt_f32_ubyte1_e32 v135, v43
	v_cvt_f32_ubyte2_e32 v137, v43
	v_cvt_f32_ubyte3_e32 v139, v43
	s_lshl_b32 s30, s77, 12
	s_add_u32 s28, s26, s30
	s_addc_u32 s29, s27, 0
	global_load_dwordx2 v[42:43], v162, s[28:29]
	v_cvt_f32_ubyte0_e32 v140, v44
	v_cvt_f32_ubyte1_e32 v142, v44
	v_cvt_f32_ubyte2_e32 v144, v44
	v_cvt_f32_ubyte3_e32 v146, v44
	v_cvt_f32_ubyte0_e32 v148, v45
	v_cvt_f32_ubyte1_e32 v150, v45
	v_cvt_f32_ubyte2_e32 v152, v45
	v_cvt_f32_ubyte3_e32 v154, v45
	s_lshl_b32 s30, s78, 12
	s_add_u32 s28, s26, s30
	s_addc_u32 s29, s27, 0
	global_load_dwordx2 v[44:45], v162, s[28:29]
	v_cvt_f32_ubyte0_e32 v141, v46
	v_cvt_f32_ubyte1_e32 v143, v46
	v_cvt_f32_ubyte2_e32 v145, v46
	v_cvt_f32_ubyte3_e32 v147, v46
	v_cvt_f32_ubyte0_e32 v149, v47
	v_cvt_f32_ubyte1_e32 v151, v47
	v_cvt_f32_ubyte2_e32 v153, v47
	v_cvt_f32_ubyte3_e32 v155, v47
	s_lshl_b32 s30, s79, 12
	s_add_u32 s28, s26, s30
	s_addc_u32 s29, s27, 0
	global_load_dwordx2 v[46:47], v162, s[28:29]
	v_mul_f32_e32 v186, v124, v108
	v_mul_f32_e32 v187, v125, v108
	v_mul_f32_e32 v188, v140, v108
	v_mul_f32_e32 v189, v141, v108
	v_fmac_f32_e32 v186, v126, v109
	v_fmac_f32_e32 v187, v127, v109
	v_fmac_f32_e32 v188, v142, v109
	v_fmac_f32_e32 v189, v143, v109
	v_fmac_f32_e32 v186, v128, v110
	v_fmac_f32_e32 v187, v129, v110
	v_fmac_f32_e32 v188, v144, v110
	v_fmac_f32_e32 v189, v145, v110
	v_fmac_f32_e32 v186, v130, v111
	v_fmac_f32_e32 v187, v131, v111
	v_fmac_f32_e32 v188, v146, v111
	v_fmac_f32_e32 v189, v147, v111
	v_fmac_f32_e32 v186, v132, v112
	v_fmac_f32_e32 v187, v133, v112
	v_fmac_f32_e32 v188, v148, v112
	v_fmac_f32_e32 v189, v149, v112
	v_fmac_f32_e32 v186, v134, v113
	v_fmac_f32_e32 v187, v135, v113
	v_fmac_f32_e32 v188, v150, v113
	v_fmac_f32_e32 v189, v151, v113
	v_fmac_f32_e32 v186, v136, v114
	v_fmac_f32_e32 v187, v137, v114
	v_fmac_f32_e32 v188, v152, v114
	v_fmac_f32_e32 v189, v153, v114
	v_fmac_f32_e32 v186, v138, v115
	v_fmac_f32_e32 v187, v139, v115
	v_fmac_f32_e32 v188, v154, v115
	v_fmac_f32_e32 v189, v155, v115
	s_waitcnt vmcnt(29)
	v_cvt_f32_ubyte0_e32 v124, v48
	v_cvt_f32_ubyte1_e32 v126, v48
	v_cvt_f32_ubyte2_e32 v128, v48
	v_cvt_f32_ubyte3_e32 v130, v48
	v_cvt_f32_ubyte0_e32 v132, v49
	v_cvt_f32_ubyte1_e32 v134, v49
	v_cvt_f32_ubyte2_e32 v136, v49
	v_cvt_f32_ubyte3_e32 v138, v49
	s_lshl_b32 s30, s80, 12
	s_add_u32 s28, s26, s30
	s_addc_u32 s29, s27, 0
	global_load_dwordx2 v[48:49], v162, s[28:29]
	v_cvt_f32_ubyte0_e32 v125, v50
	v_cvt_f32_ubyte1_e32 v127, v50
	v_cvt_f32_ubyte2_e32 v129, v50
	v_cvt_f32_ubyte3_e32 v131, v50
	v_cvt_f32_ubyte0_e32 v133, v51
	v_cvt_f32_ubyte1_e32 v135, v51
	v_cvt_f32_ubyte2_e32 v137, v51
	v_cvt_f32_ubyte3_e32 v139, v51
	s_lshl_b32 s30, s81, 12
	s_add_u32 s28, s26, s30
	s_addc_u32 s29, s27, 0
	global_load_dwordx2 v[50:51], v162, s[28:29]
	v_cvt_f32_ubyte0_e32 v140, v52
	v_cvt_f32_ubyte1_e32 v142, v52
	v_cvt_f32_ubyte2_e32 v144, v52
	v_cvt_f32_ubyte3_e32 v146, v52
	v_cvt_f32_ubyte0_e32 v148, v53
	v_cvt_f32_ubyte1_e32 v150, v53
	v_cvt_f32_ubyte2_e32 v152, v53
	v_cvt_f32_ubyte3_e32 v154, v53
	s_lshl_b32 s30, s82, 12
	s_add_u32 s28, s26, s30
	s_addc_u32 s29, s27, 0
	global_load_dwordx2 v[52:53], v162, s[28:29]
	v_cvt_f32_ubyte0_e32 v141, v54
	v_cvt_f32_ubyte1_e32 v143, v54
	v_cvt_f32_ubyte2_e32 v145, v54
	v_cvt_f32_ubyte3_e32 v147, v54
	v_cvt_f32_ubyte0_e32 v149, v55
	v_cvt_f32_ubyte1_e32 v151, v55
	v_cvt_f32_ubyte2_e32 v153, v55
	v_cvt_f32_ubyte3_e32 v155, v55
	s_lshl_b32 s30, s83, 12
	s_add_u32 s28, s26, s30
	s_addc_u32 s29, s27, 0
	global_load_dwordx2 v[54:55], v162, s[28:29]
	v_mul_f32_e32 v190, v124, v108
	v_mul_f32_e32 v191, v125, v108
	v_mul_f32_e32 v192, v140, v108
	v_mul_f32_e32 v193, v141, v108
	v_fmac_f32_e32 v190, v126, v109
	v_fmac_f32_e32 v191, v127, v109
	v_fmac_f32_e32 v192, v142, v109
	v_fmac_f32_e32 v193, v143, v109
	v_fmac_f32_e32 v190, v128, v110
	v_fmac_f32_e32 v191, v129, v110
	v_fmac_f32_e32 v192, v144, v110
	v_fmac_f32_e32 v193, v145, v110
	v_fmac_f32_e32 v190, v130, v111
	v_fmac_f32_e32 v191, v131, v111
	v_fmac_f32_e32 v192, v146, v111
	v_fmac_f32_e32 v193, v147, v111
	v_fmac_f32_e32 v190, v132, v112
	v_fmac_f32_e32 v191, v133, v112
	v_fmac_f32_e32 v192, v148, v112
	v_fmac_f32_e32 v193, v149, v112
	v_fmac_f32_e32 v190, v134, v113
	v_fmac_f32_e32 v191, v135, v113
	v_fmac_f32_e32 v192, v150, v113
	v_fmac_f32_e32 v193, v151, v113
	v_fmac_f32_e32 v190, v136, v114
	v_fmac_f32_e32 v191, v137, v114
	v_fmac_f32_e32 v192, v152, v114
	v_fmac_f32_e32 v193, v153, v114
	v_fmac_f32_e32 v190, v138, v115
	v_fmac_f32_e32 v191, v139, v115
	v_fmac_f32_e32 v192, v154, v115
	v_fmac_f32_e32 v193, v155, v115
	s_waitcnt vmcnt(29)
	v_cvt_f32_ubyte0_e32 v124, v56
	v_cvt_f32_ubyte1_e32 v126, v56
	v_cvt_f32_ubyte2_e32 v128, v56
	v_cvt_f32_ubyte3_e32 v130, v56
	v_cvt_f32_ubyte0_e32 v132, v57
	v_cvt_f32_ubyte1_e32 v134, v57
	v_cvt_f32_ubyte2_e32 v136, v57
	v_cvt_f32_ubyte3_e32 v138, v57
	s_waitcnt lgkmcnt(0)
	s_load_dwordx16 s[68:83], s[38:39], 0x0 glc
	s_lshl_b32 s30, s84, 12
	s_add_u32 s28, s26, s30
	s_addc_u32 s29, s27, 0
	global_load_dwordx2 v[56:57], v162, s[28:29]
	v_cvt_f32_ubyte0_e32 v125, v58
	v_cvt_f32_ubyte1_e32 v127, v58
	v_cvt_f32_ubyte2_e32 v129, v58
	v_cvt_f32_ubyte3_e32 v131, v58
	v_cvt_f32_ubyte0_e32 v133, v59
	v_cvt_f32_ubyte1_e32 v135, v59
	v_cvt_f32_ubyte2_e32 v137, v59
	v_cvt_f32_ubyte3_e32 v139, v59
	s_lshl_b32 s30, s85, 12
	s_add_u32 s28, s26, s30
	s_addc_u32 s29, s27, 0
	global_load_dwordx2 v[58:59], v162, s[28:29]
	v_cvt_f32_ubyte0_e32 v140, v60
	v_cvt_f32_ubyte1_e32 v142, v60
	v_cvt_f32_ubyte2_e32 v144, v60
	v_cvt_f32_ubyte3_e32 v146, v60
	v_cvt_f32_ubyte0_e32 v148, v61
	v_cvt_f32_ubyte1_e32 v150, v61
	v_cvt_f32_ubyte2_e32 v152, v61
	v_cvt_f32_ubyte3_e32 v154, v61
	s_lshl_b32 s30, s86, 12
	s_add_u32 s28, s26, s30
	s_addc_u32 s29, s27, 0
	global_load_dwordx2 v[60:61], v162, s[28:29]
	v_cvt_f32_ubyte0_e32 v141, v62
	v_cvt_f32_ubyte1_e32 v143, v62
	v_cvt_f32_ubyte2_e32 v145, v62
	v_cvt_f32_ubyte3_e32 v147, v62
	v_cvt_f32_ubyte0_e32 v149, v63
	v_cvt_f32_ubyte1_e32 v151, v63
	v_cvt_f32_ubyte2_e32 v153, v63
	v_cvt_f32_ubyte3_e32 v155, v63
	s_lshl_b32 s30, s87, 12
	s_add_u32 s28, s26, s30
	s_addc_u32 s29, s27, 0
	global_load_dwordx2 v[62:63], v162, s[28:29]
	v_mul_f32_e32 v194, v124, v108
	v_mul_f32_e32 v195, v125, v108
	v_mul_f32_e32 v196, v140, v108
	v_mul_f32_e32 v197, v141, v108
	v_fmac_f32_e32 v194, v126, v109
	v_fmac_f32_e32 v195, v127, v109
	v_fmac_f32_e32 v196, v142, v109
	v_fmac_f32_e32 v197, v143, v109
	v_fmac_f32_e32 v194, v128, v110
	v_fmac_f32_e32 v195, v129, v110
	v_fmac_f32_e32 v196, v144, v110
	v_fmac_f32_e32 v197, v145, v110
	v_fmac_f32_e32 v194, v130, v111
	v_fmac_f32_e32 v195, v131, v111
	v_fmac_f32_e32 v196, v146, v111
	v_fmac_f32_e32 v197, v147, v111
	v_fmac_f32_e32 v194, v132, v112
	v_fmac_f32_e32 v195, v133, v112
	v_fmac_f32_e32 v196, v148, v112
	v_fmac_f32_e32 v197, v149, v112
	v_fmac_f32_e32 v194, v134, v113
	v_fmac_f32_e32 v195, v135, v113
	v_fmac_f32_e32 v196, v150, v113
	v_fmac_f32_e32 v197, v151, v113
	v_fmac_f32_e32 v194, v136, v114
	v_fmac_f32_e32 v195, v137, v114
	v_fmac_f32_e32 v196, v152, v114
	v_fmac_f32_e32 v197, v153, v114
	v_fmac_f32_e32 v194, v138, v115
	v_fmac_f32_e32 v195, v139, v115
	v_fmac_f32_e32 v196, v154, v115
	v_fmac_f32_e32 v197, v155, v115
	s_waitcnt vmcnt(29)
	v_cvt_f32_ubyte0_e32 v124, v64
	v_cvt_f32_ubyte1_e32 v126, v64
	v_cvt_f32_ubyte2_e32 v128, v64
	v_cvt_f32_ubyte3_e32 v130, v64
	v_cvt_f32_ubyte0_e32 v132, v65
	v_cvt_f32_ubyte1_e32 v134, v65
	v_cvt_f32_ubyte2_e32 v136, v65
	v_cvt_f32_ubyte3_e32 v138, v65
	s_lshl_b32 s30, s88, 12
	s_add_u32 s28, s26, s30
	s_addc_u32 s29, s27, 0
	global_load_dwordx2 v[64:65], v162, s[28:29]
	v_cvt_f32_ubyte0_e32 v125, v66
	v_cvt_f32_ubyte1_e32 v127, v66
	v_cvt_f32_ubyte2_e32 v129, v66
	v_cvt_f32_ubyte3_e32 v131, v66
	v_cvt_f32_ubyte0_e32 v133, v67
	v_cvt_f32_ubyte1_e32 v135, v67
	v_cvt_f32_ubyte2_e32 v137, v67
	v_cvt_f32_ubyte3_e32 v139, v67
	s_lshl_b32 s30, s89, 12
	s_add_u32 s28, s26, s30
	s_addc_u32 s29, s27, 0
	global_load_dwordx2 v[66:67], v162, s[28:29]
	v_cvt_f32_ubyte0_e32 v140, v68
	v_cvt_f32_ubyte1_e32 v142, v68
	v_cvt_f32_ubyte2_e32 v144, v68
	v_cvt_f32_ubyte3_e32 v146, v68
	v_cvt_f32_ubyte0_e32 v148, v69
	v_cvt_f32_ubyte1_e32 v150, v69
	v_cvt_f32_ubyte2_e32 v152, v69
	v_cvt_f32_ubyte3_e32 v154, v69
	s_lshl_b32 s30, s90, 12
	s_add_u32 s28, s26, s30
	s_addc_u32 s29, s27, 0
	global_load_dwordx2 v[68:69], v162, s[28:29]
	v_cvt_f32_ubyte0_e32 v141, v70
	v_cvt_f32_ubyte1_e32 v143, v70
	v_cvt_f32_ubyte2_e32 v145, v70
	v_cvt_f32_ubyte3_e32 v147, v70
	v_cvt_f32_ubyte0_e32 v149, v71
	v_cvt_f32_ubyte1_e32 v151, v71
	v_cvt_f32_ubyte2_e32 v153, v71
	v_cvt_f32_ubyte3_e32 v155, v71
	s_lshl_b32 s30, s91, 12
	s_add_u32 s28, s26, s30
	s_addc_u32 s29, s27, 0
	global_load_dwordx2 v[70:71], v162, s[28:29]
	v_mul_f32_e32 v198, v124, v108
	v_mul_f32_e32 v199, v125, v108
	v_mul_f32_e32 v200, v140, v108
	v_mul_f32_e32 v201, v141, v108
	v_fmac_f32_e32 v198, v126, v109
	v_fmac_f32_e32 v199, v127, v109
	v_fmac_f32_e32 v200, v142, v109
	v_fmac_f32_e32 v201, v143, v109
	v_fmac_f32_e32 v198, v128, v110
	v_fmac_f32_e32 v199, v129, v110
	v_fmac_f32_e32 v200, v144, v110
	v_fmac_f32_e32 v201, v145, v110
	v_fmac_f32_e32 v198, v130, v111
	v_fmac_f32_e32 v199, v131, v111
	v_fmac_f32_e32 v200, v146, v111
	v_fmac_f32_e32 v201, v147, v111
	v_fmac_f32_e32 v198, v132, v112
	v_fmac_f32_e32 v199, v133, v112
	v_fmac_f32_e32 v200, v148, v112
	v_fmac_f32_e32 v201, v149, v112
	v_fmac_f32_e32 v198, v134, v113
	v_fmac_f32_e32 v199, v135, v113
	v_fmac_f32_e32 v200, v150, v113
	v_fmac_f32_e32 v201, v151, v113
	v_fmac_f32_e32 v198, v136, v114
	v_fmac_f32_e32 v199, v137, v114
	v_fmac_f32_e32 v200, v152, v114
	v_fmac_f32_e32 v201, v153, v114
	v_fmac_f32_e32 v198, v138, v115
	v_fmac_f32_e32 v199, v139, v115
	v_fmac_f32_e32 v200, v154, v115
	v_fmac_f32_e32 v201, v155, v115
	s_waitcnt vmcnt(29)
	v_cvt_f32_ubyte0_e32 v124, v72
	v_cvt_f32_ubyte1_e32 v126, v72
	v_cvt_f32_ubyte2_e32 v128, v72
	v_cvt_f32_ubyte3_e32 v130, v72
	v_cvt_f32_ubyte0_e32 v132, v73
	v_cvt_f32_ubyte1_e32 v134, v73
	v_cvt_f32_ubyte2_e32 v136, v73
	v_cvt_f32_ubyte3_e32 v138, v73
	s_lshl_b32 s30, s92, 12
	s_add_u32 s28, s26, s30
	s_addc_u32 s29, s27, 0
	global_load_dwordx2 v[72:73], v162, s[28:29]
	v_cvt_f32_ubyte0_e32 v125, v74
	v_cvt_f32_ubyte1_e32 v127, v74
	v_cvt_f32_ubyte2_e32 v129, v74
	v_cvt_f32_ubyte3_e32 v131, v74
	v_cvt_f32_ubyte0_e32 v133, v75
	v_cvt_f32_ubyte1_e32 v135, v75
	v_cvt_f32_ubyte2_e32 v137, v75
	v_cvt_f32_ubyte3_e32 v139, v75
	s_lshl_b32 s30, s93, 12
	s_add_u32 s28, s26, s30
	s_addc_u32 s29, s27, 0
	global_load_dwordx2 v[74:75], v162, s[28:29]
	v_cvt_f32_ubyte0_e32 v140, v76
	v_cvt_f32_ubyte1_e32 v142, v76
	v_cvt_f32_ubyte2_e32 v144, v76
	v_cvt_f32_ubyte3_e32 v146, v76
	v_cvt_f32_ubyte0_e32 v148, v77
	v_cvt_f32_ubyte1_e32 v150, v77
	v_cvt_f32_ubyte2_e32 v152, v77
	v_cvt_f32_ubyte3_e32 v154, v77
	s_lshl_b32 s30, s94, 12
	s_add_u32 s28, s26, s30
	s_addc_u32 s29, s27, 0
	global_load_dwordx2 v[76:77], v162, s[28:29]
	v_cvt_f32_ubyte0_e32 v141, v78
	v_cvt_f32_ubyte1_e32 v143, v78
	v_cvt_f32_ubyte2_e32 v145, v78
	v_cvt_f32_ubyte3_e32 v147, v78
	v_cvt_f32_ubyte0_e32 v149, v79
	v_cvt_f32_ubyte1_e32 v151, v79
	v_cvt_f32_ubyte2_e32 v153, v79
	v_cvt_f32_ubyte3_e32 v155, v79
	s_lshl_b32 s30, s95, 12
	s_add_u32 s28, s26, s30
	s_addc_u32 s29, s27, 0
	global_load_dwordx2 v[78:79], v162, s[28:29]
	v_mul_f32_e32 v202, v124, v108
	v_mul_f32_e32 v203, v125, v108
	v_mul_f32_e32 v204, v140, v108
	v_mul_f32_e32 v205, v141, v108
	v_fmac_f32_e32 v202, v126, v109
	v_fmac_f32_e32 v203, v127, v109
	v_fmac_f32_e32 v204, v142, v109
	v_fmac_f32_e32 v205, v143, v109
	v_fmac_f32_e32 v202, v128, v110
	v_fmac_f32_e32 v203, v129, v110
	v_fmac_f32_e32 v204, v144, v110
	v_fmac_f32_e32 v205, v145, v110
	v_fmac_f32_e32 v202, v130, v111
	v_fmac_f32_e32 v203, v131, v111
	v_fmac_f32_e32 v204, v146, v111
	v_fmac_f32_e32 v205, v147, v111
	v_fmac_f32_e32 v202, v132, v112
	v_fmac_f32_e32 v203, v133, v112
	v_fmac_f32_e32 v204, v148, v112
	v_fmac_f32_e32 v205, v149, v112
	v_fmac_f32_e32 v202, v134, v113
	v_fmac_f32_e32 v203, v135, v113
	v_fmac_f32_e32 v204, v150, v113
	v_fmac_f32_e32 v205, v151, v113
	v_fmac_f32_e32 v202, v136, v114
	v_fmac_f32_e32 v203, v137, v114
	v_fmac_f32_e32 v204, v152, v114
	v_fmac_f32_e32 v205, v153, v114
	v_fmac_f32_e32 v202, v138, v115
	v_fmac_f32_e32 v203, v139, v115
	v_fmac_f32_e32 v204, v154, v115
	v_fmac_f32_e32 v205, v155, v115
	s_waitcnt vmcnt(29)
	v_cvt_f32_ubyte0_e32 v124, v80
	v_cvt_f32_ubyte1_e32 v126, v80
	v_cvt_f32_ubyte2_e32 v128, v80
	v_cvt_f32_ubyte3_e32 v130, v80
	v_cvt_f32_ubyte0_e32 v132, v81
	v_cvt_f32_ubyte1_e32 v134, v81
	v_cvt_f32_ubyte2_e32 v136, v81
	v_cvt_f32_ubyte3_e32 v138, v81
	s_lshl_b32 s30, s96, 12
	s_add_u32 s28, s26, s30
	s_addc_u32 s29, s27, 0
	global_load_dwordx2 v[80:81], v162, s[28:29]
	v_cvt_f32_ubyte0_e32 v125, v82
	v_cvt_f32_ubyte1_e32 v127, v82
	v_cvt_f32_ubyte2_e32 v129, v82
	v_cvt_f32_ubyte3_e32 v131, v82
	v_cvt_f32_ubyte0_e32 v133, v83
	v_cvt_f32_ubyte1_e32 v135, v83
	v_cvt_f32_ubyte2_e32 v137, v83
	v_cvt_f32_ubyte3_e32 v139, v83
	s_lshl_b32 s30, s97, 12
	s_add_u32 s28, s26, s30
	s_addc_u32 s29, s27, 0
	global_load_dwordx2 v[82:83], v162, s[28:29]
	v_cvt_f32_ubyte0_e32 v140, v84
	v_cvt_f32_ubyte1_e32 v142, v84
	v_cvt_f32_ubyte2_e32 v144, v84
	v_cvt_f32_ubyte3_e32 v146, v84
	v_cvt_f32_ubyte0_e32 v148, v85
	v_cvt_f32_ubyte1_e32 v150, v85
	v_cvt_f32_ubyte2_e32 v152, v85
	v_cvt_f32_ubyte3_e32 v154, v85
	s_lshl_b32 s30, s98, 12
	s_add_u32 s28, s26, s30
	s_addc_u32 s29, s27, 0
	global_load_dwordx2 v[84:85], v162, s[28:29]
	v_cvt_f32_ubyte0_e32 v141, v86
	v_cvt_f32_ubyte1_e32 v143, v86
	v_cvt_f32_ubyte2_e32 v145, v86
	v_cvt_f32_ubyte3_e32 v147, v86
	v_cvt_f32_ubyte0_e32 v149, v87
	v_cvt_f32_ubyte1_e32 v151, v87
	v_cvt_f32_ubyte2_e32 v153, v87
	v_cvt_f32_ubyte3_e32 v155, v87
	s_lshl_b32 s30, s99, 12
	s_add_u32 s28, s26, s30
	s_addc_u32 s29, s27, 0
	global_load_dwordx2 v[86:87], v162, s[28:29]
	v_mul_f32_e32 v206, v124, v108
	v_mul_f32_e32 v207, v125, v108
	v_mul_f32_e32 v208, v140, v108
	v_mul_f32_e32 v209, v141, v108
	v_fmac_f32_e32 v206, v126, v109
	v_fmac_f32_e32 v207, v127, v109
	v_fmac_f32_e32 v208, v142, v109
	v_fmac_f32_e32 v209, v143, v109
	v_fmac_f32_e32 v206, v128, v110
	v_fmac_f32_e32 v207, v129, v110
	v_fmac_f32_e32 v208, v144, v110
	v_fmac_f32_e32 v209, v145, v110
	v_fmac_f32_e32 v206, v130, v111
	v_fmac_f32_e32 v207, v131, v111
	v_fmac_f32_e32 v208, v146, v111
	v_fmac_f32_e32 v209, v147, v111
	v_fmac_f32_e32 v206, v132, v112
	v_fmac_f32_e32 v207, v133, v112
	v_fmac_f32_e32 v208, v148, v112
	v_fmac_f32_e32 v209, v149, v112
	v_fmac_f32_e32 v206, v134, v113
	v_fmac_f32_e32 v207, v135, v113
	v_fmac_f32_e32 v208, v150, v113
	v_fmac_f32_e32 v209, v151, v113
	v_fmac_f32_e32 v206, v136, v114
	v_fmac_f32_e32 v207, v137, v114
	v_fmac_f32_e32 v208, v152, v114
	v_fmac_f32_e32 v209, v153, v114
	v_fmac_f32_e32 v206, v138, v115
	v_fmac_f32_e32 v207, v139, v115
	v_fmac_f32_e32 v208, v154, v115
	v_fmac_f32_e32 v209, v155, v115
	v_permlane32_swap_b32_e32 v178, v194
	v_permlane32_swap_b32_e32 v179, v195
	v_permlane32_swap_b32_e32 v180, v196
	v_permlane32_swap_b32_e32 v181, v197
	v_permlane32_swap_b32_e32 v182, v198
	v_permlane32_swap_b32_e32 v183, v199
	v_permlane32_swap_b32_e32 v184, v200
	v_permlane32_swap_b32_e32 v185, v201
	v_permlane32_swap_b32_e32 v186, v202
	v_permlane32_swap_b32_e32 v187, v203
	v_permlane32_swap_b32_e32 v188, v204
	v_permlane32_swap_b32_e32 v189, v205
	v_permlane32_swap_b32_e32 v190, v206
	v_permlane32_swap_b32_e32 v191, v207
	v_permlane32_swap_b32_e32 v192, v208
	v_permlane32_swap_b32_e32 v193, v209
	v_add_f32_e32 v178, v178, v194
	v_add_f32_e32 v179, v179, v195
	v_add_f32_e32 v180, v180, v196
	v_add_f32_e32 v181, v181, v197
	v_add_f32_e32 v182, v182, v198
	v_add_f32_e32 v183, v183, v199
	v_add_f32_e32 v184, v184, v200
	v_add_f32_e32 v185, v185, v201
	v_add_f32_e32 v186, v186, v202
	v_add_f32_e32 v187, v187, v203
	v_add_f32_e32 v188, v188, v204
	v_add_f32_e32 v189, v189, v205
	v_add_f32_e32 v190, v190, v206
	v_add_f32_e32 v191, v191, v207
	v_add_f32_e32 v192, v192, v208
	v_add_f32_e32 v193, v193, v209
	v_permlane16_swap_b32_e32 v178, v186
	v_permlane16_swap_b32_e32 v179, v187
	v_permlane16_swap_b32_e32 v180, v188
	v_permlane16_swap_b32_e32 v181, v189
	v_permlane16_swap_b32_e32 v182, v190
	v_permlane16_swap_b32_e32 v183, v191
	v_permlane16_swap_b32_e32 v184, v192
	v_permlane16_swap_b32_e32 v185, v193
	v_add_f32_e32 v178, v178, v186
	v_add_f32_e32 v179, v179, v187
	v_add_f32_e32 v180, v180, v188
	v_add_f32_e32 v181, v181, v189
	v_add_f32_e32 v182, v182, v190
	v_add_f32_e32 v183, v183, v191
	v_add_f32_e32 v184, v184, v192
	v_add_f32_e32 v185, v185, v193
	v_cndmask_b32_e64 v2, v178, v182, s[8:9]
	v_cndmask_b32_e64 v3, v179, v183, s[8:9]
	v_cndmask_b32_e64 v4, v180, v184, s[8:9]
	v_cndmask_b32_e64 v5, v181, v185, s[8:9]
	v_cndmask_b32_e64 v6, v182, v178, s[8:9]
	v_cndmask_b32_e64 v7, v183, v179, s[8:9]
	v_cndmask_b32_e64 v8, v184, v180, s[8:9]
	v_cndmask_b32_e64 v9, v185, v181, s[8:9]
	v_add_f32_dpp v6, v2, v6 row_ror:8 row_mask:0xf bank_mask:0xf
	v_add_f32_dpp v7, v3, v7 row_ror:8 row_mask:0xf bank_mask:0xf
	v_add_f32_dpp v8, v4, v8 row_ror:8 row_mask:0xf bank_mask:0xf
	v_add_f32_dpp v9, v5, v9 row_ror:8 row_mask:0xf bank_mask:0xf
	v_cndmask_b32_e64 v2, v6, v8, s[10:11]
	v_cndmask_b32_e64 v3, v7, v9, s[10:11]
	v_cndmask_b32_e64 v4, v8, v6, s[10:11]
	v_cndmask_b32_e64 v5, v9, v7, s[10:11]
	v_add_f32_dpp v4, v2, v4 row_half_mirror row_mask:0xf bank_mask:0xf
	v_add_f32_dpp v5, v3, v5 row_half_mirror row_mask:0xf bank_mask:0xf
	v_cndmask_b32_e64 v2, v4, v5, s[14:15]
	v_cndmask_b32_e64 v3, v5, v4, s[14:15]
	s_nop 0
	v_add_f32_dpp v3, v2, v3 quad_perm:[2,3,0,1] row_mask:0xf bank_mask:0xf
	s_nop 1
	v_add_f32_dpp v11, v3, v3 quad_perm:[1,0,3,2] row_mask:0xf bank_mask:0xf
	s_mov_b64 exec, s[2:3]
	global_store_dword v[22:23], v11, off offset:256
	s_mov_b64 exec, -1
	s_waitcnt vmcnt(29)
	v_cvt_f32_ubyte0_e32 v124, v24
	v_cvt_f32_ubyte1_e32 v126, v24
	v_cvt_f32_ubyte2_e32 v128, v24
	v_cvt_f32_ubyte3_e32 v130, v24
	v_cvt_f32_ubyte0_e32 v132, v25
	v_cvt_f32_ubyte1_e32 v134, v25
	v_cvt_f32_ubyte2_e32 v136, v25
	v_cvt_f32_ubyte3_e32 v138, v25
	v_cvt_f32_ubyte0_e32 v125, v26
	v_cvt_f32_ubyte1_e32 v127, v26
	v_cvt_f32_ubyte2_e32 v129, v26
	v_cvt_f32_ubyte3_e32 v131, v26
	v_cvt_f32_ubyte0_e32 v133, v27
	v_cvt_f32_ubyte1_e32 v135, v27
	v_cvt_f32_ubyte2_e32 v137, v27
	v_cvt_f32_ubyte3_e32 v139, v27
	v_cvt_f32_ubyte0_e32 v140, v28
	v_cvt_f32_ubyte1_e32 v142, v28
	v_cvt_f32_ubyte2_e32 v144, v28
	v_cvt_f32_ubyte3_e32 v146, v28
	v_cvt_f32_ubyte0_e32 v148, v29
	v_cvt_f32_ubyte1_e32 v150, v29
	v_cvt_f32_ubyte2_e32 v152, v29
	v_cvt_f32_ubyte3_e32 v154, v29
	v_cvt_f32_ubyte0_e32 v141, v30
	v_cvt_f32_ubyte1_e32 v143, v30
	v_cvt_f32_ubyte2_e32 v145, v30
	v_cvt_f32_ubyte3_e32 v147, v30
	v_cvt_f32_ubyte0_e32 v149, v31
	v_cvt_f32_ubyte1_e32 v151, v31
	v_cvt_f32_ubyte2_e32 v153, v31
	v_cvt_f32_ubyte3_e32 v155, v31
	v_mul_f32_e32 v178, v124, v108
	v_mul_f32_e32 v179, v125, v108
	v_mul_f32_e32 v180, v140, v108
	v_mul_f32_e32 v181, v141, v108
	v_fmac_f32_e32 v178, v126, v109
	v_fmac_f32_e32 v179, v127, v109
	v_fmac_f32_e32 v180, v142, v109
	v_fmac_f32_e32 v181, v143, v109
	v_fmac_f32_e32 v178, v128, v110
	v_fmac_f32_e32 v179, v129, v110
	v_fmac_f32_e32 v180, v144, v110
	v_fmac_f32_e32 v181, v145, v110
	v_fmac_f32_e32 v178, v130, v111
	v_fmac_f32_e32 v179, v131, v111
	v_fmac_f32_e32 v180, v146, v111
	v_fmac_f32_e32 v181, v147, v111
	v_fmac_f32_e32 v178, v132, v112
	v_fmac_f32_e32 v179, v133, v112
	v_fmac_f32_e32 v180, v148, v112
	v_fmac_f32_e32 v181, v149, v112
	v_fmac_f32_e32 v178, v134, v113
	v_fmac_f32_e32 v179, v135, v113
	v_fmac_f32_e32 v180, v150, v113
	v_fmac_f32_e32 v181, v151, v113
	v_fmac_f32_e32 v178, v136, v114
	v_fmac_f32_e32 v179, v137, v114
	v_fmac_f32_e32 v180, v152, v114
	v_fmac_f32_e32 v181, v153, v114
	v_fmac_f32_e32 v178, v138, v115
	v_fmac_f32_e32 v179, v139, v115
	v_fmac_f32_e32 v180, v154, v115
	v_fmac_f32_e32 v181, v155, v115
	s_waitcnt vmcnt(25)
	v_cvt_f32_ubyte0_e32 v124, v32
	v_cvt_f32_ubyte1_e32 v126, v32
	v_cvt_f32_ubyte2_e32 v128, v32
	v_cvt_f32_ubyte3_e32 v130, v32
	v_cvt_f32_ubyte0_e32 v132, v33
	v_cvt_f32_ubyte1_e32 v134, v33
	v_cvt_f32_ubyte2_e32 v136, v33
	v_cvt_f32_ubyte3_e32 v138, v33
	v_cvt_f32_ubyte0_e32 v125, v34
	v_cvt_f32_ubyte1_e32 v127, v34
	v_cvt_f32_ubyte2_e32 v129, v34
	v_cvt_f32_ubyte3_e32 v131, v34
	v_cvt_f32_ubyte0_e32 v133, v35
	v_cvt_f32_ubyte1_e32 v135, v35
	v_cvt_f32_ubyte2_e32 v137, v35
	v_cvt_f32_ubyte3_e32 v139, v35
	v_cvt_f32_ubyte0_e32 v140, v36
	v_cvt_f32_ubyte1_e32 v142, v36
	v_cvt_f32_ubyte2_e32 v144, v36
	v_cvt_f32_ubyte3_e32 v146, v36
	v_cvt_f32_ubyte0_e32 v148, v37
	v_cvt_f32_ubyte1_e32 v150, v37
	v_cvt_f32_ubyte2_e32 v152, v37
	v_cvt_f32_ubyte3_e32 v154, v37
	v_cvt_f32_ubyte0_e32 v141, v38
	v_cvt_f32_ubyte1_e32 v143, v38
	v_cvt_f32_ubyte2_e32 v145, v38
	v_cvt_f32_ubyte3_e32 v147, v38
	v_cvt_f32_ubyte0_e32 v149, v39
	v_cvt_f32_ubyte1_e32 v151, v39
	v_cvt_f32_ubyte2_e32 v153, v39
	v_cvt_f32_ubyte3_e32 v155, v39
	v_mul_f32_e32 v182, v124, v108
	v_mul_f32_e32 v183, v125, v108
	v_mul_f32_e32 v184, v140, v108
	v_mul_f32_e32 v185, v141, v108
	v_fmac_f32_e32 v182, v126, v109
	v_fmac_f32_e32 v183, v127, v109
	v_fmac_f32_e32 v184, v142, v109
	v_fmac_f32_e32 v185, v143, v109
	v_fmac_f32_e32 v182, v128, v110
	v_fmac_f32_e32 v183, v129, v110
	v_fmac_f32_e32 v184, v144, v110
	v_fmac_f32_e32 v185, v145, v110
	v_fmac_f32_e32 v182, v130, v111
	v_fmac_f32_e32 v183, v131, v111
	v_fmac_f32_e32 v184, v146, v111
	v_fmac_f32_e32 v185, v147, v111
	v_fmac_f32_e32 v182, v132, v112
	v_fmac_f32_e32 v183, v133, v112
	v_fmac_f32_e32 v184, v148, v112
	v_fmac_f32_e32 v185, v149, v112
	v_fmac_f32_e32 v182, v134, v113
	v_fmac_f32_e32 v183, v135, v113
	v_fmac_f32_e32 v184, v150, v113
	v_fmac_f32_e32 v185, v151, v113
	v_fmac_f32_e32 v182, v136, v114
	v_fmac_f32_e32 v183, v137, v114
	v_fmac_f32_e32 v184, v152, v114
	v_fmac_f32_e32 v185, v153, v114
	v_fmac_f32_e32 v182, v138, v115
	v_fmac_f32_e32 v183, v139, v115
	v_fmac_f32_e32 v184, v154, v115
	v_fmac_f32_e32 v185, v155, v115
	s_waitcnt vmcnt(21)
	v_cvt_f32_ubyte0_e32 v124, v40
	v_cvt_f32_ubyte1_e32 v126, v40
	v_cvt_f32_ubyte2_e32 v128, v40
	v_cvt_f32_ubyte3_e32 v130, v40
	v_cvt_f32_ubyte0_e32 v132, v41
	v_cvt_f32_ubyte1_e32 v134, v41
	v_cvt_f32_ubyte2_e32 v136, v41
	v_cvt_f32_ubyte3_e32 v138, v41
	v_cvt_f32_ubyte0_e32 v125, v42
	v_cvt_f32_ubyte1_e32 v127, v42
	v_cvt_f32_ubyte2_e32 v129, v42
	v_cvt_f32_ubyte3_e32 v131, v42
	v_cvt_f32_ubyte0_e32 v133, v43
	v_cvt_f32_ubyte1_e32 v135, v43
	v_cvt_f32_ubyte2_e32 v137, v43
	v_cvt_f32_ubyte3_e32 v139, v43
	v_cvt_f32_ubyte0_e32 v140, v44
	v_cvt_f32_ubyte1_e32 v142, v44
	v_cvt_f32_ubyte2_e32 v144, v44
	v_cvt_f32_ubyte3_e32 v146, v44
	v_cvt_f32_ubyte0_e32 v148, v45
	v_cvt_f32_ubyte1_e32 v150, v45
	v_cvt_f32_ubyte2_e32 v152, v45
	v_cvt_f32_ubyte3_e32 v154, v45
	v_cvt_f32_ubyte0_e32 v141, v46
	v_cvt_f32_ubyte1_e32 v143, v46
	v_cvt_f32_ubyte2_e32 v145, v46
	v_cvt_f32_ubyte3_e32 v147, v46
	v_cvt_f32_ubyte0_e32 v149, v47
	v_cvt_f32_ubyte1_e32 v151, v47
	v_cvt_f32_ubyte2_e32 v153, v47
	v_cvt_f32_ubyte3_e32 v155, v47
	v_mul_f32_e32 v186, v124, v108
	v_mul_f32_e32 v187, v125, v108
	v_mul_f32_e32 v188, v140, v108
	v_mul_f32_e32 v189, v141, v108
	v_fmac_f32_e32 v186, v126, v109
	v_fmac_f32_e32 v187, v127, v109
	v_fmac_f32_e32 v188, v142, v109
	v_fmac_f32_e32 v189, v143, v109
	v_fmac_f32_e32 v186, v128, v110
	v_fmac_f32_e32 v187, v129, v110
	v_fmac_f32_e32 v188, v144, v110
	v_fmac_f32_e32 v189, v145, v110
	v_fmac_f32_e32 v186, v130, v111
	v_fmac_f32_e32 v187, v131, v111
	v_fmac_f32_e32 v188, v146, v111
	v_fmac_f32_e32 v189, v147, v111
	v_fmac_f32_e32 v186, v132, v112
	v_fmac_f32_e32 v187, v133, v112
	v_fmac_f32_e32 v188, v148, v112
	v_fmac_f32_e32 v189, v149, v112
	v_fmac_f32_e32 v186, v134, v113
	v_fmac_f32_e32 v187, v135, v113
	v_fmac_f32_e32 v188, v150, v113
	v_fmac_f32_e32 v189, v151, v113
	v_fmac_f32_e32 v186, v136, v114
	v_fmac_f32_e32 v187, v137, v114
	v_fmac_f32_e32 v188, v152, v114
	v_fmac_f32_e32 v189, v153, v114
	v_fmac_f32_e32 v186, v138, v115
	v_fmac_f32_e32 v187, v139, v115
	v_fmac_f32_e32 v188, v154, v115
	v_fmac_f32_e32 v189, v155, v115
	s_waitcnt vmcnt(17)
	v_cvt_f32_ubyte0_e32 v124, v48
	v_cvt_f32_ubyte1_e32 v126, v48
	v_cvt_f32_ubyte2_e32 v128, v48
	v_cvt_f32_ubyte3_e32 v130, v48
	v_cvt_f32_ubyte0_e32 v132, v49
	v_cvt_f32_ubyte1_e32 v134, v49
	v_cvt_f32_ubyte2_e32 v136, v49
	v_cvt_f32_ubyte3_e32 v138, v49
	v_cvt_f32_ubyte0_e32 v125, v50
	v_cvt_f32_ubyte1_e32 v127, v50
	v_cvt_f32_ubyte2_e32 v129, v50
	v_cvt_f32_ubyte3_e32 v131, v50
	v_cvt_f32_ubyte0_e32 v133, v51
	v_cvt_f32_ubyte1_e32 v135, v51
	v_cvt_f32_ubyte2_e32 v137, v51
	v_cvt_f32_ubyte3_e32 v139, v51
	v_cvt_f32_ubyte0_e32 v140, v52
	v_cvt_f32_ubyte1_e32 v142, v52
	v_cvt_f32_ubyte2_e32 v144, v52
	v_cvt_f32_ubyte3_e32 v146, v52
	v_cvt_f32_ubyte0_e32 v148, v53
	v_cvt_f32_ubyte1_e32 v150, v53
	v_cvt_f32_ubyte2_e32 v152, v53
	v_cvt_f32_ubyte3_e32 v154, v53
	v_cvt_f32_ubyte0_e32 v141, v54
	v_cvt_f32_ubyte1_e32 v143, v54
	v_cvt_f32_ubyte2_e32 v145, v54
	v_cvt_f32_ubyte3_e32 v147, v54
	v_cvt_f32_ubyte0_e32 v149, v55
	v_cvt_f32_ubyte1_e32 v151, v55
	v_cvt_f32_ubyte2_e32 v153, v55
	v_cvt_f32_ubyte3_e32 v155, v55
	v_mul_f32_e32 v190, v124, v108
	v_mul_f32_e32 v191, v125, v108
	v_mul_f32_e32 v192, v140, v108
	v_mul_f32_e32 v193, v141, v108
	v_fmac_f32_e32 v190, v126, v109
	v_fmac_f32_e32 v191, v127, v109
	v_fmac_f32_e32 v192, v142, v109
	v_fmac_f32_e32 v193, v143, v109
	v_fmac_f32_e32 v190, v128, v110
	v_fmac_f32_e32 v191, v129, v110
	v_fmac_f32_e32 v192, v144, v110
	v_fmac_f32_e32 v193, v145, v110
	v_fmac_f32_e32 v190, v130, v111
	v_fmac_f32_e32 v191, v131, v111
	v_fmac_f32_e32 v192, v146, v111
	v_fmac_f32_e32 v193, v147, v111
	v_fmac_f32_e32 v190, v132, v112
	v_fmac_f32_e32 v191, v133, v112
	v_fmac_f32_e32 v192, v148, v112
	v_fmac_f32_e32 v193, v149, v112
	v_fmac_f32_e32 v190, v134, v113
	v_fmac_f32_e32 v191, v135, v113
	v_fmac_f32_e32 v192, v150, v113
	v_fmac_f32_e32 v193, v151, v113
	v_fmac_f32_e32 v190, v136, v114
	v_fmac_f32_e32 v191, v137, v114
	v_fmac_f32_e32 v192, v152, v114
	v_fmac_f32_e32 v193, v153, v114
	v_fmac_f32_e32 v190, v138, v115
	v_fmac_f32_e32 v191, v139, v115
	v_fmac_f32_e32 v192, v154, v115
	v_fmac_f32_e32 v193, v155, v115
	s_waitcnt vmcnt(13)
	v_cvt_f32_ubyte0_e32 v124, v56
	v_cvt_f32_ubyte1_e32 v126, v56
	v_cvt_f32_ubyte2_e32 v128, v56
	v_cvt_f32_ubyte3_e32 v130, v56
	v_cvt_f32_ubyte0_e32 v132, v57
	v_cvt_f32_ubyte1_e32 v134, v57
	v_cvt_f32_ubyte2_e32 v136, v57
	v_cvt_f32_ubyte3_e32 v138, v57
	v_cvt_f32_ubyte0_e32 v125, v58
	v_cvt_f32_ubyte1_e32 v127, v58
	v_cvt_f32_ubyte2_e32 v129, v58
	v_cvt_f32_ubyte3_e32 v131, v58
	v_cvt_f32_ubyte0_e32 v133, v59
	v_cvt_f32_ubyte1_e32 v135, v59
	v_cvt_f32_ubyte2_e32 v137, v59
	v_cvt_f32_ubyte3_e32 v139, v59
	v_cvt_f32_ubyte0_e32 v140, v60
	v_cvt_f32_ubyte1_e32 v142, v60
	v_cvt_f32_ubyte2_e32 v144, v60
	v_cvt_f32_ubyte3_e32 v146, v60
	v_cvt_f32_ubyte0_e32 v148, v61
	v_cvt_f32_ubyte1_e32 v150, v61
	v_cvt_f32_ubyte2_e32 v152, v61
	v_cvt_f32_ubyte3_e32 v154, v61
	v_cvt_f32_ubyte0_e32 v141, v62
	v_cvt_f32_ubyte1_e32 v143, v62
	v_cvt_f32_ubyte2_e32 v145, v62
	v_cvt_f32_ubyte3_e32 v147, v62
	v_cvt_f32_ubyte0_e32 v149, v63
	v_cvt_f32_ubyte1_e32 v151, v63
	v_cvt_f32_ubyte2_e32 v153, v63
	v_cvt_f32_ubyte3_e32 v155, v63
	v_mul_f32_e32 v194, v124, v108
	v_mul_f32_e32 v195, v125, v108
	v_mul_f32_e32 v196, v140, v108
	v_mul_f32_e32 v197, v141, v108
	v_fmac_f32_e32 v194, v126, v109
	v_fmac_f32_e32 v195, v127, v109
	v_fmac_f32_e32 v196, v142, v109
	v_fmac_f32_e32 v197, v143, v109
	v_fmac_f32_e32 v194, v128, v110
	v_fmac_f32_e32 v195, v129, v110
	v_fmac_f32_e32 v196, v144, v110
	v_fmac_f32_e32 v197, v145, v110
	v_fmac_f32_e32 v194, v130, v111
	v_fmac_f32_e32 v195, v131, v111
	v_fmac_f32_e32 v196, v146, v111
	v_fmac_f32_e32 v197, v147, v111
	v_fmac_f32_e32 v194, v132, v112
	v_fmac_f32_e32 v195, v133, v112
	v_fmac_f32_e32 v196, v148, v112
	v_fmac_f32_e32 v197, v149, v112
	v_fmac_f32_e32 v194, v134, v113
	v_fmac_f32_e32 v195, v135, v113
	v_fmac_f32_e32 v196, v150, v113
	v_fmac_f32_e32 v197, v151, v113
	v_fmac_f32_e32 v194, v136, v114
	v_fmac_f32_e32 v195, v137, v114
	v_fmac_f32_e32 v196, v152, v114
	v_fmac_f32_e32 v197, v153, v114
	v_fmac_f32_e32 v194, v138, v115
	v_fmac_f32_e32 v195, v139, v115
	v_fmac_f32_e32 v196, v154, v115
	v_fmac_f32_e32 v197, v155, v115
	s_waitcnt vmcnt(9)
	v_cvt_f32_ubyte0_e32 v124, v64
	v_cvt_f32_ubyte1_e32 v126, v64
	v_cvt_f32_ubyte2_e32 v128, v64
	v_cvt_f32_ubyte3_e32 v130, v64
	v_cvt_f32_ubyte0_e32 v132, v65
	v_cvt_f32_ubyte1_e32 v134, v65
	v_cvt_f32_ubyte2_e32 v136, v65
	v_cvt_f32_ubyte3_e32 v138, v65
	v_cvt_f32_ubyte0_e32 v125, v66
	v_cvt_f32_ubyte1_e32 v127, v66
	v_cvt_f32_ubyte2_e32 v129, v66
	v_cvt_f32_ubyte3_e32 v131, v66
	v_cvt_f32_ubyte0_e32 v133, v67
	v_cvt_f32_ubyte1_e32 v135, v67
	v_cvt_f32_ubyte2_e32 v137, v67
	v_cvt_f32_ubyte3_e32 v139, v67
	v_cvt_f32_ubyte0_e32 v140, v68
	v_cvt_f32_ubyte1_e32 v142, v68
	v_cvt_f32_ubyte2_e32 v144, v68
	v_cvt_f32_ubyte3_e32 v146, v68
	v_cvt_f32_ubyte0_e32 v148, v69
	v_cvt_f32_ubyte1_e32 v150, v69
	v_cvt_f32_ubyte2_e32 v152, v69
	v_cvt_f32_ubyte3_e32 v154, v69
	v_cvt_f32_ubyte0_e32 v141, v70
	v_cvt_f32_ubyte1_e32 v143, v70
	v_cvt_f32_ubyte2_e32 v145, v70
	v_cvt_f32_ubyte3_e32 v147, v70
	v_cvt_f32_ubyte0_e32 v149, v71
	v_cvt_f32_ubyte1_e32 v151, v71
	v_cvt_f32_ubyte2_e32 v153, v71
	v_cvt_f32_ubyte3_e32 v155, v71
	v_mul_f32_e32 v198, v124, v108
	v_mul_f32_e32 v199, v125, v108
	v_mul_f32_e32 v200, v140, v108
	v_mul_f32_e32 v201, v141, v108
	v_fmac_f32_e32 v198, v126, v109
	v_fmac_f32_e32 v199, v127, v109
	v_fmac_f32_e32 v200, v142, v109
	v_fmac_f32_e32 v201, v143, v109
	v_fmac_f32_e32 v198, v128, v110
	v_fmac_f32_e32 v199, v129, v110
	v_fmac_f32_e32 v200, v144, v110
	v_fmac_f32_e32 v201, v145, v110
	v_fmac_f32_e32 v198, v130, v111
	v_fmac_f32_e32 v199, v131, v111
	v_fmac_f32_e32 v200, v146, v111
	v_fmac_f32_e32 v201, v147, v111
	v_fmac_f32_e32 v198, v132, v112
	v_fmac_f32_e32 v199, v133, v112
	v_fmac_f32_e32 v200, v148, v112
	v_fmac_f32_e32 v201, v149, v112
	v_fmac_f32_e32 v198, v134, v113
	v_fmac_f32_e32 v199, v135, v113
	v_fmac_f32_e32 v200, v150, v113
	v_fmac_f32_e32 v201, v151, v113
	v_fmac_f32_e32 v198, v136, v114
	v_fmac_f32_e32 v199, v137, v114
	v_fmac_f32_e32 v200, v152, v114
	v_fmac_f32_e32 v201, v153, v114
	v_fmac_f32_e32 v198, v138, v115
	v_fmac_f32_e32 v199, v139, v115
	v_fmac_f32_e32 v200, v154, v115
	v_fmac_f32_e32 v201, v155, v115
	s_waitcnt vmcnt(5)
	v_cvt_f32_ubyte0_e32 v124, v72
	v_cvt_f32_ubyte1_e32 v126, v72
	v_cvt_f32_ubyte2_e32 v128, v72
	v_cvt_f32_ubyte3_e32 v130, v72
	v_cvt_f32_ubyte0_e32 v132, v73
	v_cvt_f32_ubyte1_e32 v134, v73
	v_cvt_f32_ubyte2_e32 v136, v73
	v_cvt_f32_ubyte3_e32 v138, v73
	v_cvt_f32_ubyte0_e32 v125, v74
	v_cvt_f32_ubyte1_e32 v127, v74
	v_cvt_f32_ubyte2_e32 v129, v74
	v_cvt_f32_ubyte3_e32 v131, v74
	v_cvt_f32_ubyte0_e32 v133, v75
	v_cvt_f32_ubyte1_e32 v135, v75
	v_cvt_f32_ubyte2_e32 v137, v75
	v_cvt_f32_ubyte3_e32 v139, v75
	v_cvt_f32_ubyte0_e32 v140, v76
	v_cvt_f32_ubyte1_e32 v142, v76
	v_cvt_f32_ubyte2_e32 v144, v76
	v_cvt_f32_ubyte3_e32 v146, v76
	v_cvt_f32_ubyte0_e32 v148, v77
	v_cvt_f32_ubyte1_e32 v150, v77
	v_cvt_f32_ubyte2_e32 v152, v77
	v_cvt_f32_ubyte3_e32 v154, v77
	v_cvt_f32_ubyte0_e32 v141, v78
	v_cvt_f32_ubyte1_e32 v143, v78
	v_cvt_f32_ubyte2_e32 v145, v78
	v_cvt_f32_ubyte3_e32 v147, v78
	v_cvt_f32_ubyte0_e32 v149, v79
	v_cvt_f32_ubyte1_e32 v151, v79
	v_cvt_f32_ubyte2_e32 v153, v79
	v_cvt_f32_ubyte3_e32 v155, v79
	v_mul_f32_e32 v202, v124, v108
	v_mul_f32_e32 v203, v125, v108
	v_mul_f32_e32 v204, v140, v108
	v_mul_f32_e32 v205, v141, v108
	v_fmac_f32_e32 v202, v126, v109
	v_fmac_f32_e32 v203, v127, v109
	v_fmac_f32_e32 v204, v142, v109
	v_fmac_f32_e32 v205, v143, v109
	v_fmac_f32_e32 v202, v128, v110
	v_fmac_f32_e32 v203, v129, v110
	v_fmac_f32_e32 v204, v144, v110
	v_fmac_f32_e32 v205, v145, v110
	v_fmac_f32_e32 v202, v130, v111
	v_fmac_f32_e32 v203, v131, v111
	v_fmac_f32_e32 v204, v146, v111
	v_fmac_f32_e32 v205, v147, v111
	v_fmac_f32_e32 v202, v132, v112
	v_fmac_f32_e32 v203, v133, v112
	v_fmac_f32_e32 v204, v148, v112
	v_fmac_f32_e32 v205, v149, v112
	v_fmac_f32_e32 v202, v134, v113
	v_fmac_f32_e32 v203, v135, v113
	v_fmac_f32_e32 v204, v150, v113
	v_fmac_f32_e32 v205, v151, v113
	v_fmac_f32_e32 v202, v136, v114
	v_fmac_f32_e32 v203, v137, v114
	v_fmac_f32_e32 v204, v152, v114
	v_fmac_f32_e32 v205, v153, v114
	v_fmac_f32_e32 v202, v138, v115
	v_fmac_f32_e32 v203, v139, v115
	v_fmac_f32_e32 v204, v154, v115
	v_fmac_f32_e32 v205, v155, v115
	s_waitcnt vmcnt(1)
	v_cvt_f32_ubyte0_e32 v124, v80
	v_cvt_f32_ubyte1_e32 v126, v80
	v_cvt_f32_ubyte2_e32 v128, v80
	v_cvt_f32_ubyte3_e32 v130, v80
	v_cvt_f32_ubyte0_e32 v132, v81
	v_cvt_f32_ubyte1_e32 v134, v81
	v_cvt_f32_ubyte2_e32 v136, v81
	v_cvt_f32_ubyte3_e32 v138, v81
	v_cvt_f32_ubyte0_e32 v125, v82
	v_cvt_f32_ubyte1_e32 v127, v82
	v_cvt_f32_ubyte2_e32 v129, v82
	v_cvt_f32_ubyte3_e32 v131, v82
	v_cvt_f32_ubyte0_e32 v133, v83
	v_cvt_f32_ubyte1_e32 v135, v83
	v_cvt_f32_ubyte2_e32 v137, v83
	v_cvt_f32_ubyte3_e32 v139, v83
	v_cvt_f32_ubyte0_e32 v140, v84
	v_cvt_f32_ubyte1_e32 v142, v84
	v_cvt_f32_ubyte2_e32 v144, v84
	v_cvt_f32_ubyte3_e32 v146, v84
	v_cvt_f32_ubyte0_e32 v148, v85
	v_cvt_f32_ubyte1_e32 v150, v85
	v_cvt_f32_ubyte2_e32 v152, v85
	v_cvt_f32_ubyte3_e32 v154, v85
	v_cvt_f32_ubyte0_e32 v141, v86
	v_cvt_f32_ubyte1_e32 v143, v86
	v_cvt_f32_ubyte2_e32 v145, v86
	v_cvt_f32_ubyte3_e32 v147, v86
	v_cvt_f32_ubyte0_e32 v149, v87
	v_cvt_f32_ubyte1_e32 v151, v87
	v_cvt_f32_ubyte2_e32 v153, v87
	v_cvt_f32_ubyte3_e32 v155, v87
	v_mul_f32_e32 v206, v124, v108
	v_mul_f32_e32 v207, v125, v108
	v_mul_f32_e32 v208, v140, v108
	v_mul_f32_e32 v209, v141, v108
	v_fmac_f32_e32 v206, v126, v109
	v_fmac_f32_e32 v207, v127, v109
	v_fmac_f32_e32 v208, v142, v109
	v_fmac_f32_e32 v209, v143, v109
	v_fmac_f32_e32 v206, v128, v110
	v_fmac_f32_e32 v207, v129, v110
	v_fmac_f32_e32 v208, v144, v110
	v_fmac_f32_e32 v209, v145, v110
	v_fmac_f32_e32 v206, v130, v111
	v_fmac_f32_e32 v207, v131, v111
	v_fmac_f32_e32 v208, v146, v111
	v_fmac_f32_e32 v209, v147, v111
	v_fmac_f32_e32 v206, v132, v112
	v_fmac_f32_e32 v207, v133, v112
	v_fmac_f32_e32 v208, v148, v112
	v_fmac_f32_e32 v209, v149, v112
	v_fmac_f32_e32 v206, v134, v113
	v_fmac_f32_e32 v207, v135, v113
	v_fmac_f32_e32 v208, v150, v113
	v_fmac_f32_e32 v209, v151, v113
	v_fmac_f32_e32 v206, v136, v114
	v_fmac_f32_e32 v207, v137, v114
	v_fmac_f32_e32 v208, v152, v114
	v_fmac_f32_e32 v209, v153, v114
	v_fmac_f32_e32 v206, v138, v115
	v_fmac_f32_e32 v207, v139, v115
	v_fmac_f32_e32 v208, v154, v115
	v_fmac_f32_e32 v209, v155, v115
	s_waitcnt lgkmcnt(0)
	s_load_dwordx16 s[84:99], s[38:39], 0x40 glc
	s_lshl_b32 s30, s68, 12
	s_add_u32 s28, s26, s30
	s_addc_u32 s29, s27, 0
	global_load_dwordx2 v[24:25], v162, s[28:29]
	s_lshl_b32 s30, s69, 12
	s_add_u32 s28, s26, s30
	s_addc_u32 s29, s27, 0
	global_load_dwordx2 v[26:27], v162, s[28:29]
	s_lshl_b32 s30, s70, 12
	s_add_u32 s28, s26, s30
	s_addc_u32 s29, s27, 0
	global_load_dwordx2 v[28:29], v162, s[28:29]
	s_lshl_b32 s30, s71, 12
	s_add_u32 s28, s26, s30
	s_addc_u32 s29, s27, 0
	global_load_dwordx2 v[30:31], v162, s[28:29]
	s_lshl_b32 s30, s72, 12
	s_add_u32 s28, s26, s30
	s_addc_u32 s29, s27, 0
	global_load_dwordx2 v[32:33], v162, s[28:29]
	s_lshl_b32 s30, s73, 12
	s_add_u32 s28, s26, s30
	s_addc_u32 s29, s27, 0
	global_load_dwordx2 v[34:35], v162, s[28:29]
	s_lshl_b32 s30, s74, 12
	s_add_u32 s28, s26, s30
	s_addc_u32 s29, s27, 0
	global_load_dwordx2 v[36:37], v162, s[28:29]
	s_lshl_b32 s30, s75, 12
	s_add_u32 s28, s26, s30
	s_addc_u32 s29, s27, 0
	global_load_dwordx2 v[38:39], v162, s[28:29]
	s_lshl_b32 s30, s76, 12
	s_add_u32 s28, s26, s30
	s_addc_u32 s29, s27, 0
	global_load_dwordx2 v[40:41], v162, s[28:29]
	s_lshl_b32 s30, s77, 12
	s_add_u32 s28, s26, s30
	s_addc_u32 s29, s27, 0
	global_load_dwordx2 v[42:43], v162, s[28:29]
	s_lshl_b32 s30, s78, 12
	s_add_u32 s28, s26, s30
	s_addc_u32 s29, s27, 0
	global_load_dwordx2 v[44:45], v162, s[28:29]
	s_lshl_b32 s30, s79, 12
	s_add_u32 s28, s26, s30
	s_addc_u32 s29, s27, 0
	global_load_dwordx2 v[46:47], v162, s[28:29]
	s_lshl_b32 s30, s80, 12
	s_add_u32 s28, s26, s30
	s_addc_u32 s29, s27, 0
	global_load_dwordx2 v[48:49], v162, s[28:29]
	s_lshl_b32 s30, s81, 12
	s_add_u32 s28, s26, s30
	s_addc_u32 s29, s27, 0
	global_load_dwordx2 v[50:51], v162, s[28:29]
	s_lshl_b32 s30, s82, 12
	s_add_u32 s28, s26, s30
	s_addc_u32 s29, s27, 0
	global_load_dwordx2 v[52:53], v162, s[28:29]
	s_lshl_b32 s30, s83, 12
	s_add_u32 s28, s26, s30
	s_addc_u32 s29, s27, 0
	global_load_dwordx2 v[54:55], v162, s[28:29]
	s_waitcnt lgkmcnt(0)
	s_load_dwordx16 s[68:83], s[38:39], 0x80 glc
	s_lshl_b32 s30, s84, 12
	s_add_u32 s28, s26, s30
	s_addc_u32 s29, s27, 0
	global_load_dwordx2 v[56:57], v162, s[28:29]
	s_lshl_b32 s30, s85, 12
	s_add_u32 s28, s26, s30
	s_addc_u32 s29, s27, 0
	global_load_dwordx2 v[58:59], v162, s[28:29]
	s_lshl_b32 s30, s86, 12
	s_add_u32 s28, s26, s30
	s_addc_u32 s29, s27, 0
	global_load_dwordx2 v[60:61], v162, s[28:29]
	s_lshl_b32 s30, s87, 12
	s_add_u32 s28, s26, s30
	s_addc_u32 s29, s27, 0
	global_load_dwordx2 v[62:63], v162, s[28:29]
	s_lshl_b32 s30, s88, 12
	s_add_u32 s28, s26, s30
	s_addc_u32 s29, s27, 0
	global_load_dwordx2 v[64:65], v162, s[28:29]
	s_lshl_b32 s30, s89, 12
	s_add_u32 s28, s26, s30
	s_addc_u32 s29, s27, 0
	global_load_dwordx2 v[66:67], v162, s[28:29]
	s_lshl_b32 s30, s90, 12
	s_add_u32 s28, s26, s30
	s_addc_u32 s29, s27, 0
	global_load_dwordx2 v[68:69], v162, s[28:29]
	s_lshl_b32 s30, s91, 12
	s_add_u32 s28, s26, s30
	s_addc_u32 s29, s27, 0
	global_load_dwordx2 v[70:71], v162, s[28:29]
	s_lshl_b32 s30, s92, 12
	s_add_u32 s28, s26, s30
	s_addc_u32 s29, s27, 0
	global_load_dwordx2 v[72:73], v162, s[28:29]
	s_lshl_b32 s30, s93, 12
	s_add_u32 s28, s26, s30
	s_addc_u32 s29, s27, 0
	global_load_dwordx2 v[74:75], v162, s[28:29]
	s_lshl_b32 s30, s94, 12
	s_add_u32 s28, s26, s30
	s_addc_u32 s29, s27, 0
	global_load_dwordx2 v[76:77], v162, s[28:29]
	s_lshl_b32 s30, s95, 12
	s_add_u32 s28, s26, s30
	s_addc_u32 s29, s27, 0
	global_load_dwordx2 v[78:79], v162, s[28:29]
	s_lshl_b32 s30, s96, 12
	s_add_u32 s28, s26, s30
	s_addc_u32 s29, s27, 0
	global_load_dwordx2 v[80:81], v162, s[28:29]
	s_lshl_b32 s30, s97, 12
	s_add_u32 s28, s26, s30
	s_addc_u32 s29, s27, 0
	global_load_dwordx2 v[82:83], v162, s[28:29]
	s_lshl_b32 s30, s98, 12
	s_add_u32 s28, s26, s30
	s_addc_u32 s29, s27, 0
	global_load_dwordx2 v[84:85], v162, s[28:29]
	s_lshl_b32 s30, s99, 12
	s_add_u32 s28, s26, s30
	s_addc_u32 s29, s27, 0
	global_load_dwordx2 v[86:87], v162, s[28:29]
	v_permlane32_swap_b32_e32 v178, v194
	v_permlane32_swap_b32_e32 v179, v195
	v_permlane32_swap_b32_e32 v180, v196
	v_permlane32_swap_b32_e32 v181, v197
	v_permlane32_swap_b32_e32 v182, v198
	v_permlane32_swap_b32_e32 v183, v199
	v_permlane32_swap_b32_e32 v184, v200
	v_permlane32_swap_b32_e32 v185, v201
	v_permlane32_swap_b32_e32 v186, v202
	v_permlane32_swap_b32_e32 v187, v203
	v_permlane32_swap_b32_e32 v188, v204
	v_permlane32_swap_b32_e32 v189, v205
	v_permlane32_swap_b32_e32 v190, v206
	v_permlane32_swap_b32_e32 v191, v207
	v_permlane32_swap_b32_e32 v192, v208
	v_permlane32_swap_b32_e32 v193, v209
	v_add_f32_e32 v178, v178, v194
	v_add_f32_e32 v179, v179, v195
	v_add_f32_e32 v180, v180, v196
	v_add_f32_e32 v181, v181, v197
	v_add_f32_e32 v182, v182, v198
	v_add_f32_e32 v183, v183, v199
	v_add_f32_e32 v184, v184, v200
	v_add_f32_e32 v185, v185, v201
	v_add_f32_e32 v186, v186, v202
	v_add_f32_e32 v187, v187, v203
	v_add_f32_e32 v188, v188, v204
	v_add_f32_e32 v189, v189, v205
	v_add_f32_e32 v190, v190, v206
	v_add_f32_e32 v191, v191, v207
	v_add_f32_e32 v192, v192, v208
	v_add_f32_e32 v193, v193, v209
	v_permlane16_swap_b32_e32 v178, v186
	v_permlane16_swap_b32_e32 v179, v187
	v_permlane16_swap_b32_e32 v180, v188
	v_permlane16_swap_b32_e32 v181, v189
	v_permlane16_swap_b32_e32 v182, v190
	v_permlane16_swap_b32_e32 v183, v191
	v_permlane16_swap_b32_e32 v184, v192
	v_permlane16_swap_b32_e32 v185, v193
	v_add_f32_e32 v178, v178, v186
	v_add_f32_e32 v179, v179, v187
	v_add_f32_e32 v180, v180, v188
	v_add_f32_e32 v181, v181, v189
	v_add_f32_e32 v182, v182, v190
	v_add_f32_e32 v183, v183, v191
	v_add_f32_e32 v184, v184, v192
	v_add_f32_e32 v185, v185, v193
	v_cndmask_b32_e64 v2, v178, v182, s[8:9]
	v_cndmask_b32_e64 v3, v179, v183, s[8:9]
	v_cndmask_b32_e64 v4, v180, v184, s[8:9]
	v_cndmask_b32_e64 v5, v181, v185, s[8:9]
	v_cndmask_b32_e64 v6, v182, v178, s[8:9]
	v_cndmask_b32_e64 v7, v183, v179, s[8:9]
	v_cndmask_b32_e64 v8, v184, v180, s[8:9]
	v_cndmask_b32_e64 v9, v185, v181, s[8:9]
	v_add_f32_dpp v6, v2, v6 row_ror:8 row_mask:0xf bank_mask:0xf
	v_add_f32_dpp v7, v3, v7 row_ror:8 row_mask:0xf bank_mask:0xf
	v_add_f32_dpp v8, v4, v8 row_ror:8 row_mask:0xf bank_mask:0xf
	v_add_f32_dpp v9, v5, v9 row_ror:8 row_mask:0xf bank_mask:0xf
	v_cndmask_b32_e64 v2, v6, v8, s[10:11]
	v_cndmask_b32_e64 v3, v7, v9, s[10:11]
	v_cndmask_b32_e64 v4, v8, v6, s[10:11]
	v_cndmask_b32_e64 v5, v9, v7, s[10:11]
	v_add_f32_dpp v4, v2, v4 row_half_mirror row_mask:0xf bank_mask:0xf
	v_add_f32_dpp v5, v3, v5 row_half_mirror row_mask:0xf bank_mask:0xf
	v_cndmask_b32_e64 v2, v4, v5, s[14:15]
	v_cndmask_b32_e64 v3, v5, v4, s[14:15]
	s_nop 0
	v_add_f32_dpp v3, v2, v3 quad_perm:[2,3,0,1] row_mask:0xf bank_mask:0xf
	s_nop 1
	v_add_f32_dpp v11, v3, v3 quad_perm:[1,0,3,2] row_mask:0xf bank_mask:0xf
	s_mov_b64 exec, s[2:3]
	global_store_dword v[22:23], v11, off offset:384
	s_mov_b64 exec, -1
	s_add_i32 s16, s16, 1
	s_cmp_lt_i32 s16, s17
	s_cbranch_scc1 .Lpa_tok
	s_waitcnt vmcnt(0)
	s_waitcnt vmcnt(0)
	v_cmp_eq_u32_e32 vcc, 0, v0
	s_waitcnt vmcnt(0) lgkmcnt(0)
	s_barrier
	s_and_saveexec_b64 s[2:3], vcc
	s_cbranch_execz .Lgbb_1444
	v_readlane_b32 s4, v237, 5
	s_waitcnt vmcnt(0) expcnt(0) lgkmcnt(0)
	s_nop 0
	v_mov_b32_e32 v1, s4
	ds_read_b32 v3, v1
	ds_read_b32 v1, v1 offset:4
	s_waitcnt lgkmcnt(1)
	v_cmp_ne_u32_e32 vcc, 0, v3
	s_branch .Lgbb_1412
	v_readlane_b32 s4, v237, 2
	v_readlane_b32 s5, v237, 3
	s_load_dwordx2 s[8:9], s[6:7], 0x4
	s_lshl_b64 s[4:5], s[4:5], 2
	v_readlane_b32 s6, v237, 0
	s_add_u32 s4, s6, s4
	v_readlane_b32 s6, v237, 1
	s_addc_u32 s5, s6, s5
	s_add_u32 s6, s4, 0x1000
	s_addc_u32 s7, s5, 0
	s_waitcnt lgkmcnt(0)
	s_mul_i32 s20, s8, s38
	s_add_u32 s8, s4, 0x1100
	s_mul_i32 s20, s20, s9
	s_addc_u32 s9, s5, 0
	s_add_u32 s10, s4, 0x1200
	s_addc_u32 s11, s5, 0
	s_add_u32 s12, s4, 0x1300
	s_addc_u32 s13, s5, 0
	s_mov_b32 s21, 1
	v_mov_b32_e32 v17, 0
	s_branch .Lgbb_1400

.Lerfa1_1476:
	s_andn2_saveexec_b64 s[34:35], s[34:35]
	v_mul_f32_e32 v12, v11, v11
	v_fmamk_f32 v13, v12, 0xba1345e1, v250
	v_fmaak_f32 v13, v12, v13, 0xbcdac9b8
	v_fmaak_f32 v13, v12, v13, 0x3de703be
	v_fmaak_f32 v13, v12, v13, 0xbec09330
	v_fmaak_f32 v12, v12, v13, 0x3e0375d0
	v_fma_f32 v12, |v11|, v12, |v11|
	s_or_b64 exec, exec, s[34:35]
	v_bfi_b32 v11, s50, v12, v11
	v_mul_f32_e32 v10, 0.5, v10
	v_add_f32_e32 v11, 1.0, v11
	v_mul_f32_e32 v10, v10, v11
	v_mul_f32_e32 v10, v164, v10
	v_mul_f32_e32 v10, v249, v10
	v_mov_b32_e32 v247, v10
	v_add_f32_e32 v16, v246, v247
	s_nop 1
	v_add_f32_dpp v17, v16, v16 quad_perm:[1,0,3,2] row_mask:0xf bank_mask:0xf
	s_nop 1
	v_add_f32_dpp v16, v17, v17 quad_perm:[2,3,0,1] row_mask:0xf bank_mask:0xf
	s_nop 1
	v_add_f32_dpp v17, v16, v16 row_half_mirror row_mask:0xf bank_mask:0xf
	s_nop 1
	v_add_f32_dpp v16, v17, v17 row_ror:8 row_mask:0xf bank_mask:0xf
	v_mov_b32_e32 v17, v16
	s_nop 1
	v_permlane16_swap_b32_e32 v16, v17
	v_add_f32_e32 v16, v16, v17
	v_mov_b32_e32 v17, v16
	s_nop 1
	v_permlane32_swap_b32_e32 v16, v17
	v_add_f32_e32 v16, v16, v17
	v_mul_f32_e32 v248, 0xc3000000, v16
	v_mov_b32_e32 v242, v116
	v_mov_b32_e32 v243, v117
	v_mov_b32_e32 v244, v118
	v_mov_b32_e32 v245, v119
	v_mov_b32_e32 v120, v122
	v_mov_b32_e32 v121, v123
	s_lshl_b32 s30, s16, 14
	v_lshl_add_u64 v[20:21], v[214:215], 0, s[30:31]
	s_add_i32 s18, s16, 1
	s_min_i32 s18, s18, s24
	s_lshl_b32 s30, s16, 9
	s_add_u32 s36, s22, s30
	s_addc_u32 s37, s23, 0
	s_lshl_b32 s30, s18, 9
	s_add_u32 s38, s22, s30
	s_addc_u32 s39, s23, 0
	s_lshl_b32 s30, s18, 13
	v_lshl_add_u64 v[160:161], v[172:173], 0, s[30:31]
	global_load_dwordx4 v[116:119], v[160:161], off
	s_lshl_b32 s30, s18, 9
	v_lshl_add_u64 v[160:161], v[174:175], 0, s[30:31]
	global_load_dword v122, v[160:161], off
	global_load_dword v123, v[160:161], off offset:256
	v_lshl_add_u64 v[160:161], v[176:177], 0, s[30:31]
	global_load_dword v216, v[160:161], off
	global_load_dword v217, v[160:161], off offset:256
	v_lshl_add_u64 v[160:161], v[210:211], 0, s[30:31]
	global_load_dword v218, v[160:161], off
	global_load_dword v226, v[160:161], off offset:256
	v_lshl_add_u64 v[160:161], v[160:161], 0, s[100:101]
	global_load_dword v219, v[160:161], off
	global_load_dword v227, v[160:161], off offset:256
	v_lshl_add_u64 v[160:161], v[160:161], 0, s[100:101]
	global_load_dword v220, v[160:161], off
	global_load_dword v228, v[160:161], off offset:256
	v_lshl_add_u64 v[160:161], v[160:161], 0, s[100:101]
	global_load_dword v221, v[160:161], off
	global_load_dword v229, v[160:161], off offset:256
	v_lshl_add_u64 v[160:161], v[160:161], 0, s[100:101]
	global_load_dword v222, v[160:161], off
	global_load_dword v230, v[160:161], off offset:256
	v_lshl_add_u64 v[160:161], v[160:161], 0, s[100:101]
	global_load_dword v223, v[160:161], off
	global_load_dword v231, v[160:161], off offset:256
	v_lshl_add_u64 v[160:161], v[160:161], 0, s[100:101]
	global_load_dword v224, v[160:161], off
	global_load_dword v232, v[160:161], off offset:256
	v_lshl_add_u64 v[160:161], v[160:161], 0, s[100:101]
	global_load_dword v225, v[160:161], off
	global_load_dword v233, v[160:161], off offset:256
	s_lshl_b32 s30, s18, 7
	v_lshl_add_u64 v[160:161], v[212:213], 0, s[30:31]
	global_load_dword v234, v[160:161], off
	s_lshl_b32 s30, s18, 2
	s_add_u32 s28, s66, s30
	s_addc_u32 s29, s67, 0
	global_load_dword v235, v19, s[28:29]
	v_mov_b32_e32 v178, 0
	v_mov_b32_e32 v179, 0
	v_mov_b32_e32 v180, 0
	v_mov_b32_e32 v181, 0
	v_mov_b32_e32 v182, 0
	v_mov_b32_e32 v183, 0
	v_mov_b32_e32 v184, 0
	v_mov_b32_e32 v185, 0
	s_waitcnt vmcnt(51)
	v_readlane_b32 s25, v246, 0
	v_cvt_f32_ubyte0_e32 v124, v24
	v_cvt_f32_ubyte1_e32 v125, v24
	v_cvt_f32_ubyte2_e32 v126, v24
	v_cvt_f32_ubyte3_e32 v127, v24
	v_cvt_f32_ubyte0_e32 v128, v25
	v_cvt_f32_ubyte1_e32 v129, v25
	v_cvt_f32_ubyte2_e32 v130, v25
	v_cvt_f32_ubyte3_e32 v131, v25
	s_waitcnt lgkmcnt(0)
	s_load_dwordx16 s[84:99], s[36:37], 0xc0 glc
	s_lshl_b32 s30, s68, 12
	s_add_u32 s28, s26, s30
	s_addc_u32 s29, s27, 0
	global_load_dwordx2 v[24:25], v162, s[28:29]
	v_fmac_f32_e32 v178, s25, v124
	v_fmac_f32_e32 v179, s25, v125
	v_fmac_f32_e32 v180, s25, v126
	v_fmac_f32_e32 v181, s25, v127
	v_fmac_f32_e32 v182, s25, v128
	v_fmac_f32_e32 v183, s25, v129
	v_fmac_f32_e32 v184, s25, v130
	v_fmac_f32_e32 v185, s25, v131
	v_readlane_b32 s25, v246, 1
	v_cvt_f32_ubyte0_e32 v132, v26
	v_cvt_f32_ubyte1_e32 v133, v26
	v_cvt_f32_ubyte2_e32 v134, v26
	v_cvt_f32_ubyte3_e32 v135, v26
	v_cvt_f32_ubyte0_e32 v136, v27
	v_cvt_f32_ubyte1_e32 v137, v27
	v_cvt_f32_ubyte2_e32 v138, v27
	v_cvt_f32_ubyte3_e32 v139, v27
	s_lshl_b32 s30, s69, 12
	s_add_u32 s28, s26, s30
	s_addc_u32 s29, s27, 0
	global_load_dwordx2 v[26:27], v162, s[28:29]
	v_fmac_f32_e32 v178, s25, v132
	v_fmac_f32_e32 v179, s25, v133
	v_fmac_f32_e32 v180, s25, v134
	v_fmac_f32_e32 v181, s25, v135
	v_fmac_f32_e32 v182, s25, v136
	v_fmac_f32_e32 v183, s25, v137
	v_fmac_f32_e32 v184, s25, v138
	v_fmac_f32_e32 v185, s25, v139
	v_readlane_b32 s25, v246, 2
	v_cvt_f32_ubyte0_e32 v124, v28
	v_cvt_f32_ubyte1_e32 v125, v28
	v_cvt_f32_ubyte2_e32 v126, v28
	v_cvt_f32_ubyte3_e32 v127, v28
	v_cvt_f32_ubyte0_e32 v128, v29
	v_cvt_f32_ubyte1_e32 v129, v29
	v_cvt_f32_ubyte2_e32 v130, v29
	v_cvt_f32_ubyte3_e32 v131, v29
	s_lshl_b32 s30, s70, 12
	s_add_u32 s28, s26, s30
	s_addc_u32 s29, s27, 0
	global_load_dwordx2 v[28:29], v162, s[28:29]
	v_fmac_f32_e32 v178, s25, v124
	v_fmac_f32_e32 v179, s25, v125
	v_fmac_f32_e32 v180, s25, v126
	v_fmac_f32_e32 v181, s25, v127
	v_fmac_f32_e32 v182, s25, v128
	v_fmac_f32_e32 v183, s25, v129
	v_fmac_f32_e32 v184, s25, v130
	v_fmac_f32_e32 v185, s25, v131
	v_readlane_b32 s25, v246, 3
	v_cvt_f32_ubyte0_e32 v132, v30
	v_cvt_f32_ubyte1_e32 v133, v30
	v_cvt_f32_ubyte2_e32 v134, v30
	v_cvt_f32_ubyte3_e32 v135, v30
	v_cvt_f32_ubyte0_e32 v136, v31
	v_cvt_f32_ubyte1_e32 v137, v31
	v_cvt_f32_ubyte2_e32 v138, v31
	v_cvt_f32_ubyte3_e32 v139, v31
	s_lshl_b32 s30, s71, 12
	s_add_u32 s28, s26, s30
	s_addc_u32 s29, s27, 0
	global_load_dwordx2 v[30:31], v162, s[28:29]
	v_fmac_f32_e32 v178, s25, v132
	v_fmac_f32_e32 v179, s25, v133
	v_fmac_f32_e32 v180, s25, v134
	v_fmac_f32_e32 v181, s25, v135
	v_fmac_f32_e32 v182, s25, v136
	v_fmac_f32_e32 v183, s25, v137
	v_fmac_f32_e32 v184, s25, v138
	v_fmac_f32_e32 v185, s25, v139
	s_waitcnt vmcnt(51)
	v_readlane_b32 s25, v246, 4
	v_cvt_f32_ubyte0_e32 v124, v32
	v_cvt_f32_ubyte1_e32 v125, v32
	v_cvt_f32_ubyte2_e32 v126, v32
	v_cvt_f32_ubyte3_e32 v127, v32
	v_cvt_f32_ubyte0_e32 v128, v33
	v_cvt_f32_ubyte1_e32 v129, v33
	v_cvt_f32_ubyte2_e32 v130, v33
	v_cvt_f32_ubyte3_e32 v131, v33
	s_lshl_b32 s30, s72, 12
	s_add_u32 s28, s26, s30
	s_addc_u32 s29, s27, 0
	global_load_dwordx2 v[32:33], v162, s[28:29]
	v_fmac_f32_e32 v178, s25, v124
	v_fmac_f32_e32 v179, s25, v125
	v_fmac_f32_e32 v180, s25, v126
	v_fmac_f32_e32 v181, s25, v127
	v_fmac_f32_e32 v182, s25, v128
	v_fmac_f32_e32 v183, s25, v129
	v_fmac_f32_e32 v184, s25, v130
	v_fmac_f32_e32 v185, s25, v131
	v_readlane_b32 s25, v246, 5
	v_cvt_f32_ubyte0_e32 v132, v34
	v_cvt_f32_ubyte1_e32 v133, v34
	v_cvt_f32_ubyte2_e32 v134, v34
	v_cvt_f32_ubyte3_e32 v135, v34
	v_cvt_f32_ubyte0_e32 v136, v35
	v_cvt_f32_ubyte1_e32 v137, v35
	v_cvt_f32_ubyte2_e32 v138, v35
	v_cvt_f32_ubyte3_e32 v139, v35
	s_lshl_b32 s30, s73, 12
	s_add_u32 s28, s26, s30
	s_addc_u32 s29, s27, 0
	global_load_dwordx2 v[34:35], v162, s[28:29]
	v_fmac_f32_e32 v178, s25, v132
	v_fmac_f32_e32 v179, s25, v133
	v_fmac_f32_e32 v180, s25, v134
	v_fmac_f32_e32 v181, s25, v135
	v_fmac_f32_e32 v182, s25, v136
	v_fmac_f32_e32 v183, s25, v137
	v_fmac_f32_e32 v184, s25, v138
	v_fmac_f32_e32 v185, s25, v139
	v_readlane_b32 s25, v246, 6
	v_cvt_f32_ubyte0_e32 v124, v36
	v_cvt_f32_ubyte1_e32 v125, v36
	v_cvt_f32_ubyte2_e32 v126, v36
	v_cvt_f32_ubyte3_e32 v127, v36
	v_cvt_f32_ubyte0_e32 v128, v37
	v_cvt_f32_ubyte1_e32 v129, v37
	v_cvt_f32_ubyte2_e32 v130, v37
	v_cvt_f32_ubyte3_e32 v131, v37
	s_lshl_b32 s30, s74, 12
	s_add_u32 s28, s26, s30
	s_addc_u32 s29, s27, 0
	global_load_dwordx2 v[36:37], v162, s[28:29]
	v_fmac_f32_e32 v178, s25, v124
	v_fmac_f32_e32 v179, s25, v125
	v_fmac_f32_e32 v180, s25, v126
	v_fmac_f32_e32 v181, s25, v127
	v_fmac_f32_e32 v182, s25, v128
	v_fmac_f32_e32 v183, s25, v129
	v_fmac_f32_e32 v184, s25, v130
	v_fmac_f32_e32 v185, s25, v131
	v_readlane_b32 s25, v246, 7
	v_cvt_f32_ubyte0_e32 v132, v38
	v_cvt_f32_ubyte1_e32 v133, v38
	v_cvt_f32_ubyte2_e32 v134, v38
	v_cvt_f32_ubyte3_e32 v135, v38
	v_cvt_f32_ubyte0_e32 v136, v39
	v_cvt_f32_ubyte1_e32 v137, v39
	v_cvt_f32_ubyte2_e32 v138, v39
	v_cvt_f32_ubyte3_e32 v139, v39
	s_lshl_b32 s30, s75, 12
	s_add_u32 s28, s26, s30
	s_addc_u32 s29, s27, 0
	global_load_dwordx2 v[38:39], v162, s[28:29]
	v_fmac_f32_e32 v178, s25, v132
	v_fmac_f32_e32 v179, s25, v133
	v_fmac_f32_e32 v180, s25, v134
	v_fmac_f32_e32 v181, s25, v135
	v_fmac_f32_e32 v182, s25, v136
	v_fmac_f32_e32 v183, s25, v137
	v_fmac_f32_e32 v184, s25, v138
	v_fmac_f32_e32 v185, s25, v139
	s_waitcnt vmcnt(51)
	v_readlane_b32 s25, v246, 8
	v_cvt_f32_ubyte0_e32 v124, v40
	v_cvt_f32_ubyte1_e32 v125, v40
	v_cvt_f32_ubyte2_e32 v126, v40
	v_cvt_f32_ubyte3_e32 v127, v40
	v_cvt_f32_ubyte0_e32 v128, v41
	v_cvt_f32_ubyte1_e32 v129, v41
	v_cvt_f32_ubyte2_e32 v130, v41
	v_cvt_f32_ubyte3_e32 v131, v41
	s_lshl_b32 s30, s76, 12
	s_add_u32 s28, s26, s30
	s_addc_u32 s29, s27, 0
	global_load_dwordx2 v[40:41], v162, s[28:29]
	v_fmac_f32_e32 v178, s25, v124
	v_fmac_f32_e32 v179, s25, v125
	v_fmac_f32_e32 v180, s25, v126
	v_fmac_f32_e32 v181, s25, v127
	v_fmac_f32_e32 v182, s25, v128
	v_fmac_f32_e32 v183, s25, v129
	v_fmac_f32_e32 v184, s25, v130
	v_fmac_f32_e32 v185, s25, v131
	v_readlane_b32 s25, v246, 9
	v_cvt_f32_ubyte0_e32 v132, v42
	v_cvt_f32_ubyte1_e32 v133, v42
	v_cvt_f32_ubyte2_e32 v134, v42
	v_cvt_f32_ubyte3_e32 v135, v42
	v_cvt_f32_ubyte0_e32 v136, v43
	v_cvt_f32_ubyte1_e32 v137, v43
	v_cvt_f32_ubyte2_e32 v138, v43
	v_cvt_f32_ubyte3_e32 v139, v43
	s_lshl_b32 s30, s77, 12
	s_add_u32 s28, s26, s30
	s_addc_u32 s29, s27, 0
	global_load_dwordx2 v[42:43], v162, s[28:29]
	v_fmac_f32_e32 v178, s25, v132
	v_fmac_f32_e32 v179, s25, v133
	v_fmac_f32_e32 v180, s25, v134
	v_fmac_f32_e32 v181, s25, v135
	v_fmac_f32_e32 v182, s25, v136
	v_fmac_f32_e32 v183, s25, v137
	v_fmac_f32_e32 v184, s25, v138
	v_fmac_f32_e32 v185, s25, v139
	v_readlane_b32 s25, v246, 10
	v_cvt_f32_ubyte0_e32 v124, v44
	v_cvt_f32_ubyte1_e32 v125, v44
	v_cvt_f32_ubyte2_e32 v126, v44
	v_cvt_f32_ubyte3_e32 v127, v44
	v_cvt_f32_ubyte0_e32 v128, v45
	v_cvt_f32_ubyte1_e32 v129, v45
	v_cvt_f32_ubyte2_e32 v130, v45
	v_cvt_f32_ubyte3_e32 v131, v45
	s_lshl_b32 s30, s78, 12
	s_add_u32 s28, s26, s30
	s_addc_u32 s29, s27, 0
	global_load_dwordx2 v[44:45], v162, s[28:29]
	v_fmac_f32_e32 v178, s25, v124
	v_fmac_f32_e32 v179, s25, v125
	v_fmac_f32_e32 v180, s25, v126
	v_fmac_f32_e32 v181, s25, v127
	v_fmac_f32_e32 v182, s25, v128
	v_fmac_f32_e32 v183, s25, v129
	v_fmac_f32_e32 v184, s25, v130
	v_fmac_f32_e32 v185, s25, v131
	v_readlane_b32 s25, v246, 11
	v_cvt_f32_ubyte0_e32 v132, v46
	v_cvt_f32_ubyte1_e32 v133, v46
	v_cvt_f32_ubyte2_e32 v134, v46
	v_cvt_f32_ubyte3_e32 v135, v46
	v_cvt_f32_ubyte0_e32 v136, v47
	v_cvt_f32_ubyte1_e32 v137, v47
	v_cvt_f32_ubyte2_e32 v138, v47
	v_cvt_f32_ubyte3_e32 v139, v47
	s_lshl_b32 s30, s79, 12
	s_add_u32 s28, s26, s30
	s_addc_u32 s29, s27, 0
	global_load_dwordx2 v[46:47], v162, s[28:29]
	v_fmac_f32_e32 v178, s25, v132
	v_fmac_f32_e32 v179, s25, v133
	v_fmac_f32_e32 v180, s25, v134
	v_fmac_f32_e32 v181, s25, v135
	v_fmac_f32_e32 v182, s25, v136
	v_fmac_f32_e32 v183, s25, v137
	v_fmac_f32_e32 v184, s25, v138
	v_fmac_f32_e32 v185, s25, v139
	s_waitcnt vmcnt(51)
	v_readlane_b32 s25, v246, 12
	v_cvt_f32_ubyte0_e32 v124, v48
	v_cvt_f32_ubyte1_e32 v125, v48
	v_cvt_f32_ubyte2_e32 v126, v48
	v_cvt_f32_ubyte3_e32 v127, v48
	v_cvt_f32_ubyte0_e32 v128, v49
	v_cvt_f32_ubyte1_e32 v129, v49
	v_cvt_f32_ubyte2_e32 v130, v49
	v_cvt_f32_ubyte3_e32 v131, v49
	s_lshl_b32 s30, s80, 12
	s_add_u32 s28, s26, s30
	s_addc_u32 s29, s27, 0
	global_load_dwordx2 v[48:49], v162, s[28:29]
	v_fmac_f32_e32 v178, s25, v124
	v_fmac_f32_e32 v179, s25, v125
	v_fmac_f32_e32 v180, s25, v126
	v_fmac_f32_e32 v181, s25, v127
	v_fmac_f32_e32 v182, s25, v128
	v_fmac_f32_e32 v183, s25, v129
	v_fmac_f32_e32 v184, s25, v130
	v_fmac_f32_e32 v185, s25, v131
	v_readlane_b32 s25, v246, 13
	v_cvt_f32_ubyte0_e32 v132, v50
	v_cvt_f32_ubyte1_e32 v133, v50
	v_cvt_f32_ubyte2_e32 v134, v50
	v_cvt_f32_ubyte3_e32 v135, v50
	v_cvt_f32_ubyte0_e32 v136, v51
	v_cvt_f32_ubyte1_e32 v137, v51
	v_cvt_f32_ubyte2_e32 v138, v51
	v_cvt_f32_ubyte3_e32 v139, v51
	s_lshl_b32 s30, s81, 12
	s_add_u32 s28, s26, s30
	s_addc_u32 s29, s27, 0
	global_load_dwordx2 v[50:51], v162, s[28:29]
	v_fmac_f32_e32 v178, s25, v132
	v_fmac_f32_e32 v179, s25, v133
	v_fmac_f32_e32 v180, s25, v134
	v_fmac_f32_e32 v181, s25, v135
	v_fmac_f32_e32 v182, s25, v136
	v_fmac_f32_e32 v183, s25, v137
	v_fmac_f32_e32 v184, s25, v138
	v_fmac_f32_e32 v185, s25, v139
	v_readlane_b32 s25, v246, 14
	v_cvt_f32_ubyte0_e32 v124, v52
	v_cvt_f32_ubyte1_e32 v125, v52
	v_cvt_f32_ubyte2_e32 v126, v52
	v_cvt_f32_ubyte3_e32 v127, v52
	v_cvt_f32_ubyte0_e32 v128, v53
	v_cvt_f32_ubyte1_e32 v129, v53
	v_cvt_f32_ubyte2_e32 v130, v53
	v_cvt_f32_ubyte3_e32 v131, v53
	s_lshl_b32 s30, s82, 12
	s_add_u32 s28, s26, s30
	s_addc_u32 s29, s27, 0
	global_load_dwordx2 v[52:53], v162, s[28:29]
	v_fmac_f32_e32 v178, s25, v124
	v_fmac_f32_e32 v179, s25, v125
	v_fmac_f32_e32 v180, s25, v126
	v_fmac_f32_e32 v181, s25, v127
	v_fmac_f32_e32 v182, s25, v128
	v_fmac_f32_e32 v183, s25, v129
	v_fmac_f32_e32 v184, s25, v130
	v_fmac_f32_e32 v185, s25, v131
	v_readlane_b32 s25, v246, 15
	v_cvt_f32_ubyte0_e32 v132, v54
	v_cvt_f32_ubyte1_e32 v133, v54
	v_cvt_f32_ubyte2_e32 v134, v54
	v_cvt_f32_ubyte3_e32 v135, v54
	v_cvt_f32_ubyte0_e32 v136, v55
	v_cvt_f32_ubyte1_e32 v137, v55
	v_cvt_f32_ubyte2_e32 v138, v55
	v_cvt_f32_ubyte3_e32 v139, v55
	s_lshl_b32 s30, s83, 12
	s_add_u32 s28, s26, s30
	s_addc_u32 s29, s27, 0
	global_load_dwordx2 v[54:55], v162, s[28:29]
	v_fmac_f32_e32 v178, s25, v132
	v_fmac_f32_e32 v179, s25, v133
	v_fmac_f32_e32 v180, s25, v134
	v_fmac_f32_e32 v181, s25, v135
	v_fmac_f32_e32 v182, s25, v136
	v_fmac_f32_e32 v183, s25, v137
	v_fmac_f32_e32 v184, s25, v138
	v_fmac_f32_e32 v185, s25, v139
	s_waitcnt vmcnt(51)
	v_readlane_b32 s25, v246, 16
	v_cvt_f32_ubyte0_e32 v124, v56
	v_cvt_f32_ubyte1_e32 v125, v56
	v_cvt_f32_ubyte2_e32 v126, v56
	v_cvt_f32_ubyte3_e32 v127, v56
	v_cvt_f32_ubyte0_e32 v128, v57
	v_cvt_f32_ubyte1_e32 v129, v57
	v_cvt_f32_ubyte2_e32 v130, v57
	v_cvt_f32_ubyte3_e32 v131, v57
	s_waitcnt lgkmcnt(0)
	s_load_dwordx16 s[68:83], s[36:37], 0x100 glc
	s_lshl_b32 s30, s84, 12
	s_add_u32 s28, s26, s30
	s_addc_u32 s29, s27, 0
	global_load_dwordx2 v[56:57], v162, s[28:29]
	v_fmac_f32_e32 v178, s25, v124
	v_fmac_f32_e32 v179, s25, v125
	v_fmac_f32_e32 v180, s25, v126
	v_fmac_f32_e32 v181, s25, v127
	v_fmac_f32_e32 v182, s25, v128
	v_fmac_f32_e32 v183, s25, v129
	v_fmac_f32_e32 v184, s25, v130
	v_fmac_f32_e32 v185, s25, v131
	v_readlane_b32 s25, v246, 17
	v_cvt_f32_ubyte0_e32 v132, v58
	v_cvt_f32_ubyte1_e32 v133, v58
	v_cvt_f32_ubyte2_e32 v134, v58
	v_cvt_f32_ubyte3_e32 v135, v58
	v_cvt_f32_ubyte0_e32 v136, v59
	v_cvt_f32_ubyte1_e32 v137, v59
	v_cvt_f32_ubyte2_e32 v138, v59
	v_cvt_f32_ubyte3_e32 v139, v59
	s_lshl_b32 s30, s85, 12
	s_add_u32 s28, s26, s30
	s_addc_u32 s29, s27, 0
	global_load_dwordx2 v[58:59], v162, s[28:29]
	v_fmac_f32_e32 v178, s25, v132
	v_fmac_f32_e32 v179, s25, v133
	v_fmac_f32_e32 v180, s25, v134
	v_fmac_f32_e32 v181, s25, v135
	v_fmac_f32_e32 v182, s25, v136
	v_fmac_f32_e32 v183, s25, v137
	v_fmac_f32_e32 v184, s25, v138
	v_fmac_f32_e32 v185, s25, v139
	v_readlane_b32 s25, v246, 18
	v_cvt_f32_ubyte0_e32 v124, v60
	v_cvt_f32_ubyte1_e32 v125, v60
	v_cvt_f32_ubyte2_e32 v126, v60
	v_cvt_f32_ubyte3_e32 v127, v60
	v_cvt_f32_ubyte0_e32 v128, v61
	v_cvt_f32_ubyte1_e32 v129, v61
	v_cvt_f32_ubyte2_e32 v130, v61
	v_cvt_f32_ubyte3_e32 v131, v61
	s_lshl_b32 s30, s86, 12
	s_add_u32 s28, s26, s30
	s_addc_u32 s29, s27, 0
	global_load_dwordx2 v[60:61], v162, s[28:29]
	v_fmac_f32_e32 v178, s25, v124
	v_fmac_f32_e32 v179, s25, v125
	v_fmac_f32_e32 v180, s25, v126
	v_fmac_f32_e32 v181, s25, v127
	v_fmac_f32_e32 v182, s25, v128
	v_fmac_f32_e32 v183, s25, v129
	v_fmac_f32_e32 v184, s25, v130
	v_fmac_f32_e32 v185, s25, v131
	v_readlane_b32 s25, v246, 19
	v_cvt_f32_ubyte0_e32 v132, v62
	v_cvt_f32_ubyte1_e32 v133, v62
	v_cvt_f32_ubyte2_e32 v134, v62
	v_cvt_f32_ubyte3_e32 v135, v62
	v_cvt_f32_ubyte0_e32 v136, v63
	v_cvt_f32_ubyte1_e32 v137, v63
	v_cvt_f32_ubyte2_e32 v138, v63
	v_cvt_f32_ubyte3_e32 v139, v63
	s_lshl_b32 s30, s87, 12
	s_add_u32 s28, s26, s30
	s_addc_u32 s29, s27, 0
	global_load_dwordx2 v[62:63], v162, s[28:29]
	v_fmac_f32_e32 v178, s25, v132
	v_fmac_f32_e32 v179, s25, v133
	v_fmac_f32_e32 v180, s25, v134
	v_fmac_f32_e32 v181, s25, v135
	v_fmac_f32_e32 v182, s25, v136
	v_fmac_f32_e32 v183, s25, v137
	v_fmac_f32_e32 v184, s25, v138
	v_fmac_f32_e32 v185, s25, v139
	s_waitcnt vmcnt(51)
	v_readlane_b32 s25, v246, 20
	v_cvt_f32_ubyte0_e32 v124, v64
	v_cvt_f32_ubyte1_e32 v125, v64
	v_cvt_f32_ubyte2_e32 v126, v64
	v_cvt_f32_ubyte3_e32 v127, v64
	v_cvt_f32_ubyte0_e32 v128, v65
	v_cvt_f32_ubyte1_e32 v129, v65
	v_cvt_f32_ubyte2_e32 v130, v65
	v_cvt_f32_ubyte3_e32 v131, v65
	s_lshl_b32 s30, s88, 12
	s_add_u32 s28, s26, s30
	s_addc_u32 s29, s27, 0
	global_load_dwordx2 v[64:65], v162, s[28:29]
	v_fmac_f32_e32 v178, s25, v124
	v_fmac_f32_e32 v179, s25, v125
	v_fmac_f32_e32 v180, s25, v126
	v_fmac_f32_e32 v181, s25, v127
	v_fmac_f32_e32 v182, s25, v128
	v_fmac_f32_e32 v183, s25, v129
	v_fmac_f32_e32 v184, s25, v130
	v_fmac_f32_e32 v185, s25, v131
	v_readlane_b32 s25, v246, 21
	v_cvt_f32_ubyte0_e32 v132, v66
	v_cvt_f32_ubyte1_e32 v133, v66
	v_cvt_f32_ubyte2_e32 v134, v66
	v_cvt_f32_ubyte3_e32 v135, v66
	v_cvt_f32_ubyte0_e32 v136, v67
	v_cvt_f32_ubyte1_e32 v137, v67
	v_cvt_f32_ubyte2_e32 v138, v67
	v_cvt_f32_ubyte3_e32 v139, v67
	s_lshl_b32 s30, s89, 12
	s_add_u32 s28, s26, s30
	s_addc_u32 s29, s27, 0
	global_load_dwordx2 v[66:67], v162, s[28:29]
	v_fmac_f32_e32 v178, s25, v132
	v_fmac_f32_e32 v179, s25, v133
	v_fmac_f32_e32 v180, s25, v134
	v_fmac_f32_e32 v181, s25, v135
	v_fmac_f32_e32 v182, s25, v136
	v_fmac_f32_e32 v183, s25, v137
	v_fmac_f32_e32 v184, s25, v138
	v_fmac_f32_e32 v185, s25, v139
	v_readlane_b32 s25, v246, 22
	v_cvt_f32_ubyte0_e32 v124, v68
	v_cvt_f32_ubyte1_e32 v125, v68
	v_cvt_f32_ubyte2_e32 v126, v68
	v_cvt_f32_ubyte3_e32 v127, v68
	v_cvt_f32_ubyte0_e32 v128, v69
	v_cvt_f32_ubyte1_e32 v129, v69
	v_cvt_f32_ubyte2_e32 v130, v69
	v_cvt_f32_ubyte3_e32 v131, v69
	s_lshl_b32 s30, s90, 12
	s_add_u32 s28, s26, s30
	s_addc_u32 s29, s27, 0
	global_load_dwordx2 v[68:69], v162, s[28:29]
	v_fmac_f32_e32 v178, s25, v124
	v_fmac_f32_e32 v179, s25, v125
	v_fmac_f32_e32 v180, s25, v126
	v_fmac_f32_e32 v181, s25, v127
	v_fmac_f32_e32 v182, s25, v128
	v_fmac_f32_e32 v183, s25, v129
	v_fmac_f32_e32 v184, s25, v130
	v_fmac_f32_e32 v185, s25, v131
	v_readlane_b32 s25, v246, 23
	v_cvt_f32_ubyte0_e32 v132, v70
	v_cvt_f32_ubyte1_e32 v133, v70
	v_cvt_f32_ubyte2_e32 v134, v70
	v_cvt_f32_ubyte3_e32 v135, v70
	v_cvt_f32_ubyte0_e32 v136, v71
	v_cvt_f32_ubyte1_e32 v137, v71
	v_cvt_f32_ubyte2_e32 v138, v71
	v_cvt_f32_ubyte3_e32 v139, v71
	s_lshl_b32 s30, s91, 12
	s_add_u32 s28, s26, s30
	s_addc_u32 s29, s27, 0
	global_load_dwordx2 v[70:71], v162, s[28:29]
	v_fmac_f32_e32 v178, s25, v132
	v_fmac_f32_e32 v179, s25, v133
	v_fmac_f32_e32 v180, s25, v134
	v_fmac_f32_e32 v181, s25, v135
	v_fmac_f32_e32 v182, s25, v136
	v_fmac_f32_e32 v183, s25, v137
	v_fmac_f32_e32 v184, s25, v138
	v_fmac_f32_e32 v185, s25, v139
	s_waitcnt vmcnt(51)
	v_readlane_b32 s25, v246, 24
	v_cvt_f32_ubyte0_e32 v124, v72
	v_cvt_f32_ubyte1_e32 v125, v72
	v_cvt_f32_ubyte2_e32 v126, v72
	v_cvt_f32_ubyte3_e32 v127, v72
	v_cvt_f32_ubyte0_e32 v128, v73
	v_cvt_f32_ubyte1_e32 v129, v73
	v_cvt_f32_ubyte2_e32 v130, v73
	v_cvt_f32_ubyte3_e32 v131, v73
	s_lshl_b32 s30, s92, 12
	s_add_u32 s28, s26, s30
	s_addc_u32 s29, s27, 0
	global_load_dwordx2 v[72:73], v162, s[28:29]
	v_fmac_f32_e32 v178, s25, v124
	v_fmac_f32_e32 v179, s25, v125
	v_fmac_f32_e32 v180, s25, v126
	v_fmac_f32_e32 v181, s25, v127
	v_fmac_f32_e32 v182, s25, v128
	v_fmac_f32_e32 v183, s25, v129
	v_fmac_f32_e32 v184, s25, v130
	v_fmac_f32_e32 v185, s25, v131
	v_readlane_b32 s25, v246, 25
	v_cvt_f32_ubyte0_e32 v132, v74
	v_cvt_f32_ubyte1_e32 v133, v74
	v_cvt_f32_ubyte2_e32 v134, v74
	v_cvt_f32_ubyte3_e32 v135, v74
	v_cvt_f32_ubyte0_e32 v136, v75
	v_cvt_f32_ubyte1_e32 v137, v75
	v_cvt_f32_ubyte2_e32 v138, v75
	v_cvt_f32_ubyte3_e32 v139, v75
	s_lshl_b32 s30, s93, 12
	s_add_u32 s28, s26, s30
	s_addc_u32 s29, s27, 0
	global_load_dwordx2 v[74:75], v162, s[28:29]
	v_fmac_f32_e32 v178, s25, v132
	v_fmac_f32_e32 v179, s25, v133
	v_fmac_f32_e32 v180, s25, v134
	v_fmac_f32_e32 v181, s25, v135
	v_fmac_f32_e32 v182, s25, v136
	v_fmac_f32_e32 v183, s25, v137
	v_fmac_f32_e32 v184, s25, v138
	v_fmac_f32_e32 v185, s25, v139
	v_readlane_b32 s25, v246, 26
	v_cvt_f32_ubyte0_e32 v124, v76
	v_cvt_f32_ubyte1_e32 v125, v76
	v_cvt_f32_ubyte2_e32 v126, v76
	v_cvt_f32_ubyte3_e32 v127, v76
	v_cvt_f32_ubyte0_e32 v128, v77
	v_cvt_f32_ubyte1_e32 v129, v77
	v_cvt_f32_ubyte2_e32 v130, v77
	v_cvt_f32_ubyte3_e32 v131, v77
	s_lshl_b32 s30, s94, 12
	s_add_u32 s28, s26, s30
	s_addc_u32 s29, s27, 0
	global_load_dwordx2 v[76:77], v162, s[28:29]
	v_fmac_f32_e32 v178, s25, v124
	v_fmac_f32_e32 v179, s25, v125
	v_fmac_f32_e32 v180, s25, v126
	v_fmac_f32_e32 v181, s25, v127
	v_fmac_f32_e32 v182, s25, v128
	v_fmac_f32_e32 v183, s25, v129
	v_fmac_f32_e32 v184, s25, v130
	v_fmac_f32_e32 v185, s25, v131
	v_readlane_b32 s25, v246, 27
	v_cvt_f32_ubyte0_e32 v132, v78
	v_cvt_f32_ubyte1_e32 v133, v78
	v_cvt_f32_ubyte2_e32 v134, v78
	v_cvt_f32_ubyte3_e32 v135, v78
	v_cvt_f32_ubyte0_e32 v136, v79
	v_cvt_f32_ubyte1_e32 v137, v79
	v_cvt_f32_ubyte2_e32 v138, v79
	v_cvt_f32_ubyte3_e32 v139, v79
	s_lshl_b32 s30, s95, 12
	s_add_u32 s28, s26, s30
	s_addc_u32 s29, s27, 0
	global_load_dwordx2 v[78:79], v162, s[28:29]
	v_fmac_f32_e32 v178, s25, v132
	v_fmac_f32_e32 v179, s25, v133
	v_fmac_f32_e32 v180, s25, v134
	v_fmac_f32_e32 v181, s25, v135
	v_fmac_f32_e32 v182, s25, v136
	v_fmac_f32_e32 v183, s25, v137
	v_fmac_f32_e32 v184, s25, v138
	v_fmac_f32_e32 v185, s25, v139
	s_waitcnt vmcnt(51)
	v_readlane_b32 s25, v246, 28
	v_cvt_f32_ubyte0_e32 v124, v80
	v_cvt_f32_ubyte1_e32 v125, v80
	v_cvt_f32_ubyte2_e32 v126, v80
	v_cvt_f32_ubyte3_e32 v127, v80
	v_cvt_f32_ubyte0_e32 v128, v81
	v_cvt_f32_ubyte1_e32 v129, v81
	v_cvt_f32_ubyte2_e32 v130, v81
	v_cvt_f32_ubyte3_e32 v131, v81
	s_lshl_b32 s30, s96, 12
	s_add_u32 s28, s26, s30
	s_addc_u32 s29, s27, 0
	global_load_dwordx2 v[80:81], v162, s[28:29]
	v_fmac_f32_e32 v178, s25, v124
	v_fmac_f32_e32 v179, s25, v125
	v_fmac_f32_e32 v180, s25, v126
	v_fmac_f32_e32 v181, s25, v127
	v_fmac_f32_e32 v182, s25, v128
	v_fmac_f32_e32 v183, s25, v129
	v_fmac_f32_e32 v184, s25, v130
	v_fmac_f32_e32 v185, s25, v131
	v_readlane_b32 s25, v246, 29
	v_cvt_f32_ubyte0_e32 v132, v82
	v_cvt_f32_ubyte1_e32 v133, v82
	v_cvt_f32_ubyte2_e32 v134, v82
	v_cvt_f32_ubyte3_e32 v135, v82
	v_cvt_f32_ubyte0_e32 v136, v83
	v_cvt_f32_ubyte1_e32 v137, v83
	v_cvt_f32_ubyte2_e32 v138, v83
	v_cvt_f32_ubyte3_e32 v139, v83
	s_lshl_b32 s30, s97, 12
	s_add_u32 s28, s26, s30
	s_addc_u32 s29, s27, 0
	global_load_dwordx2 v[82:83], v162, s[28:29]
	v_fmac_f32_e32 v178, s25, v132
	v_fmac_f32_e32 v179, s25, v133
	v_fmac_f32_e32 v180, s25, v134
	v_fmac_f32_e32 v181, s25, v135
	v_fmac_f32_e32 v182, s25, v136
	v_fmac_f32_e32 v183, s25, v137
	v_fmac_f32_e32 v184, s25, v138
	v_fmac_f32_e32 v185, s25, v139
	v_readlane_b32 s25, v246, 30
	v_cvt_f32_ubyte0_e32 v124, v84
	v_cvt_f32_ubyte1_e32 v125, v84
	v_cvt_f32_ubyte2_e32 v126, v84
	v_cvt_f32_ubyte3_e32 v127, v84
	v_cvt_f32_ubyte0_e32 v128, v85
	v_cvt_f32_ubyte1_e32 v129, v85
	v_cvt_f32_ubyte2_e32 v130, v85
	v_cvt_f32_ubyte3_e32 v131, v85
	s_lshl_b32 s30, s98, 12
	s_add_u32 s28, s26, s30
	s_addc_u32 s29, s27, 0
	global_load_dwordx2 v[84:85], v162, s[28:29]
	v_fmac_f32_e32 v178, s25, v124
	v_fmac_f32_e32 v179, s25, v125
	v_fmac_f32_e32 v180, s25, v126
	v_fmac_f32_e32 v181, s25, v127
	v_fmac_f32_e32 v182, s25, v128
	v_fmac_f32_e32 v183, s25, v129
	v_fmac_f32_e32 v184, s25, v130
	v_fmac_f32_e32 v185, s25, v131
	v_readlane_b32 s25, v246, 31
	v_cvt_f32_ubyte0_e32 v132, v86
	v_cvt_f32_ubyte1_e32 v133, v86
	v_cvt_f32_ubyte2_e32 v134, v86
	v_cvt_f32_ubyte3_e32 v135, v86
	v_cvt_f32_ubyte0_e32 v136, v87
	v_cvt_f32_ubyte1_e32 v137, v87
	v_cvt_f32_ubyte2_e32 v138, v87
	v_cvt_f32_ubyte3_e32 v139, v87
	s_lshl_b32 s30, s99, 12
	s_add_u32 s28, s26, s30
	s_addc_u32 s29, s27, 0
	global_load_dwordx2 v[86:87], v162, s[28:29]
	v_fmac_f32_e32 v178, s25, v132
	v_fmac_f32_e32 v179, s25, v133
	v_fmac_f32_e32 v180, s25, v134
	v_fmac_f32_e32 v181, s25, v135
	v_fmac_f32_e32 v182, s25, v136
	v_fmac_f32_e32 v183, s25, v137
	v_fmac_f32_e32 v184, s25, v138
	v_fmac_f32_e32 v185, s25, v139
	s_waitcnt vmcnt(28)
	v_readlane_b32 s25, v246, 32
	v_cvt_f32_ubyte0_e32 v124, v24
	v_cvt_f32_ubyte1_e32 v125, v24
	v_cvt_f32_ubyte2_e32 v126, v24
	v_cvt_f32_ubyte3_e32 v127, v24
	v_cvt_f32_ubyte0_e32 v128, v25
	v_cvt_f32_ubyte1_e32 v129, v25
	v_cvt_f32_ubyte2_e32 v130, v25
	v_cvt_f32_ubyte3_e32 v131, v25
	s_waitcnt lgkmcnt(0)
	s_load_dwordx16 s[84:99], s[36:37], 0x140 glc
	s_lshl_b32 s30, s68, 12
	s_add_u32 s28, s26, s30
	s_addc_u32 s29, s27, 0
	global_load_dwordx2 v[24:25], v162, s[28:29]
	v_fmac_f32_e32 v178, s25, v124
	v_fmac_f32_e32 v179, s25, v125
	v_fmac_f32_e32 v180, s25, v126
	v_fmac_f32_e32 v181, s25, v127
	v_fmac_f32_e32 v182, s25, v128
	v_fmac_f32_e32 v183, s25, v129
	v_fmac_f32_e32 v184, s25, v130
	v_fmac_f32_e32 v185, s25, v131
	v_readlane_b32 s25, v246, 33
	v_cvt_f32_ubyte0_e32 v132, v26
	v_cvt_f32_ubyte1_e32 v133, v26
	v_cvt_f32_ubyte2_e32 v134, v26
	v_cvt_f32_ubyte3_e32 v135, v26
	v_cvt_f32_ubyte0_e32 v136, v27
	v_cvt_f32_ubyte1_e32 v137, v27
	v_cvt_f32_ubyte2_e32 v138, v27
	v_cvt_f32_ubyte3_e32 v139, v27
	s_lshl_b32 s30, s69, 12
	s_add_u32 s28, s26, s30
	s_addc_u32 s29, s27, 0
	global_load_dwordx2 v[26:27], v162, s[28:29]
	v_fmac_f32_e32 v178, s25, v132
	v_fmac_f32_e32 v179, s25, v133
	v_fmac_f32_e32 v180, s25, v134
	v_fmac_f32_e32 v181, s25, v135
	v_fmac_f32_e32 v182, s25, v136
	v_fmac_f32_e32 v183, s25, v137
	v_fmac_f32_e32 v184, s25, v138
	v_fmac_f32_e32 v185, s25, v139
	v_readlane_b32 s25, v246, 34
	v_cvt_f32_ubyte0_e32 v124, v28
	v_cvt_f32_ubyte1_e32 v125, v28
	v_cvt_f32_ubyte2_e32 v126, v28
	v_cvt_f32_ubyte3_e32 v127, v28
	v_cvt_f32_ubyte0_e32 v128, v29
	v_cvt_f32_ubyte1_e32 v129, v29
	v_cvt_f32_ubyte2_e32 v130, v29
	v_cvt_f32_ubyte3_e32 v131, v29
	s_lshl_b32 s30, s70, 12
	s_add_u32 s28, s26, s30
	s_addc_u32 s29, s27, 0
	global_load_dwordx2 v[28:29], v162, s[28:29]
	v_fmac_f32_e32 v178, s25, v124
	v_fmac_f32_e32 v179, s25, v125
	v_fmac_f32_e32 v180, s25, v126
	v_fmac_f32_e32 v181, s25, v127
	v_fmac_f32_e32 v182, s25, v128
	v_fmac_f32_e32 v183, s25, v129
	v_fmac_f32_e32 v184, s25, v130
	v_fmac_f32_e32 v185, s25, v131
	v_readlane_b32 s25, v246, 35
	v_cvt_f32_ubyte0_e32 v132, v30
	v_cvt_f32_ubyte1_e32 v133, v30
	v_cvt_f32_ubyte2_e32 v134, v30
	v_cvt_f32_ubyte3_e32 v135, v30
	v_cvt_f32_ubyte0_e32 v136, v31
	v_cvt_f32_ubyte1_e32 v137, v31
	v_cvt_f32_ubyte2_e32 v138, v31
	v_cvt_f32_ubyte3_e32 v139, v31
	s_lshl_b32 s30, s71, 12
	s_add_u32 s28, s26, s30
	s_addc_u32 s29, s27, 0
	global_load_dwordx2 v[30:31], v162, s[28:29]
	v_fmac_f32_e32 v178, s25, v132
	v_fmac_f32_e32 v179, s25, v133
	v_fmac_f32_e32 v180, s25, v134
	v_fmac_f32_e32 v181, s25, v135
	v_fmac_f32_e32 v182, s25, v136
	v_fmac_f32_e32 v183, s25, v137
	v_fmac_f32_e32 v184, s25, v138
	v_fmac_f32_e32 v185, s25, v139
	s_waitcnt vmcnt(28)
	v_readlane_b32 s25, v246, 36
	v_cvt_f32_ubyte0_e32 v124, v32
	v_cvt_f32_ubyte1_e32 v125, v32
	v_cvt_f32_ubyte2_e32 v126, v32
	v_cvt_f32_ubyte3_e32 v127, v32
	v_cvt_f32_ubyte0_e32 v128, v33
	v_cvt_f32_ubyte1_e32 v129, v33
	v_cvt_f32_ubyte2_e32 v130, v33
	v_cvt_f32_ubyte3_e32 v131, v33
	s_lshl_b32 s30, s72, 12
	s_add_u32 s28, s26, s30
	s_addc_u32 s29, s27, 0
	global_load_dwordx2 v[32:33], v162, s[28:29]
	v_fmac_f32_e32 v178, s25, v124
	v_fmac_f32_e32 v179, s25, v125
	v_fmac_f32_e32 v180, s25, v126
	v_fmac_f32_e32 v181, s25, v127
	v_fmac_f32_e32 v182, s25, v128
	v_fmac_f32_e32 v183, s25, v129
	v_fmac_f32_e32 v184, s25, v130
	v_fmac_f32_e32 v185, s25, v131
	v_readlane_b32 s25, v246, 37
	v_cvt_f32_ubyte0_e32 v132, v34
	v_cvt_f32_ubyte1_e32 v133, v34
	v_cvt_f32_ubyte2_e32 v134, v34
	v_cvt_f32_ubyte3_e32 v135, v34
	v_cvt_f32_ubyte0_e32 v136, v35
	v_cvt_f32_ubyte1_e32 v137, v35
	v_cvt_f32_ubyte2_e32 v138, v35
	v_cvt_f32_ubyte3_e32 v139, v35
	s_lshl_b32 s30, s73, 12
	s_add_u32 s28, s26, s30
	s_addc_u32 s29, s27, 0
	global_load_dwordx2 v[34:35], v162, s[28:29]
	v_fmac_f32_e32 v178, s25, v132
	v_fmac_f32_e32 v179, s25, v133
	v_fmac_f32_e32 v180, s25, v134
	v_fmac_f32_e32 v181, s25, v135
	v_fmac_f32_e32 v182, s25, v136
	v_fmac_f32_e32 v183, s25, v137
	v_fmac_f32_e32 v184, s25, v138
	v_fmac_f32_e32 v185, s25, v139
	v_readlane_b32 s25, v246, 38
	v_cvt_f32_ubyte0_e32 v124, v36
	v_cvt_f32_ubyte1_e32 v125, v36
	v_cvt_f32_ubyte2_e32 v126, v36
	v_cvt_f32_ubyte3_e32 v127, v36
	v_cvt_f32_ubyte0_e32 v128, v37
	v_cvt_f32_ubyte1_e32 v129, v37
	v_cvt_f32_ubyte2_e32 v130, v37
	v_cvt_f32_ubyte3_e32 v131, v37
	s_lshl_b32 s30, s74, 12
	s_add_u32 s28, s26, s30
	s_addc_u32 s29, s27, 0
	global_load_dwordx2 v[36:37], v162, s[28:29]
	v_fmac_f32_e32 v178, s25, v124
	v_fmac_f32_e32 v179, s25, v125
	v_fmac_f32_e32 v180, s25, v126
	v_fmac_f32_e32 v181, s25, v127
	v_fmac_f32_e32 v182, s25, v128
	v_fmac_f32_e32 v183, s25, v129
	v_fmac_f32_e32 v184, s25, v130
	v_fmac_f32_e32 v185, s25, v131
	v_readlane_b32 s25, v246, 39
	v_cvt_f32_ubyte0_e32 v132, v38
	v_cvt_f32_ubyte1_e32 v133, v38
	v_cvt_f32_ubyte2_e32 v134, v38
	v_cvt_f32_ubyte3_e32 v135, v38
	v_cvt_f32_ubyte0_e32 v136, v39
	v_cvt_f32_ubyte1_e32 v137, v39
	v_cvt_f32_ubyte2_e32 v138, v39
	v_cvt_f32_ubyte3_e32 v139, v39
	s_lshl_b32 s30, s75, 12
	s_add_u32 s28, s26, s30
	s_addc_u32 s29, s27, 0
	global_load_dwordx2 v[38:39], v162, s[28:29]
	v_fmac_f32_e32 v178, s25, v132
	v_fmac_f32_e32 v179, s25, v133
	v_fmac_f32_e32 v180, s25, v134
	v_fmac_f32_e32 v181, s25, v135
	v_fmac_f32_e32 v182, s25, v136
	v_fmac_f32_e32 v183, s25, v137
	v_fmac_f32_e32 v184, s25, v138
	v_fmac_f32_e32 v185, s25, v139
	s_waitcnt vmcnt(28)
	v_readlane_b32 s25, v246, 40
	v_cvt_f32_ubyte0_e32 v124, v40
	v_cvt_f32_ubyte1_e32 v125, v40
	v_cvt_f32_ubyte2_e32 v126, v40
	v_cvt_f32_ubyte3_e32 v127, v40
	v_cvt_f32_ubyte0_e32 v128, v41
	v_cvt_f32_ubyte1_e32 v129, v41
	v_cvt_f32_ubyte2_e32 v130, v41
	v_cvt_f32_ubyte3_e32 v131, v41
	s_lshl_b32 s30, s76, 12
	s_add_u32 s28, s26, s30
	s_addc_u32 s29, s27, 0
	global_load_dwordx2 v[40:41], v162, s[28:29]
	v_fmac_f32_e32 v178, s25, v124
	v_fmac_f32_e32 v179, s25, v125
	v_fmac_f32_e32 v180, s25, v126
	v_fmac_f32_e32 v181, s25, v127
	v_fmac_f32_e32 v182, s25, v128
	v_fmac_f32_e32 v183, s25, v129
	v_fmac_f32_e32 v184, s25, v130
	v_fmac_f32_e32 v185, s25, v131
	v_readlane_b32 s25, v246, 41
	v_cvt_f32_ubyte0_e32 v132, v42
	v_cvt_f32_ubyte1_e32 v133, v42
	v_cvt_f32_ubyte2_e32 v134, v42
	v_cvt_f32_ubyte3_e32 v135, v42
	v_cvt_f32_ubyte0_e32 v136, v43
	v_cvt_f32_ubyte1_e32 v137, v43
	v_cvt_f32_ubyte2_e32 v138, v43
	v_cvt_f32_ubyte3_e32 v139, v43
	s_lshl_b32 s30, s77, 12
	s_add_u32 s28, s26, s30
	s_addc_u32 s29, s27, 0
	global_load_dwordx2 v[42:43], v162, s[28:29]
	v_fmac_f32_e32 v178, s25, v132
	v_fmac_f32_e32 v179, s25, v133
	v_fmac_f32_e32 v180, s25, v134
	v_fmac_f32_e32 v181, s25, v135
	v_fmac_f32_e32 v182, s25, v136
	v_fmac_f32_e32 v183, s25, v137
	v_fmac_f32_e32 v184, s25, v138
	v_fmac_f32_e32 v185, s25, v139
	v_readlane_b32 s25, v246, 42
	v_cvt_f32_ubyte0_e32 v124, v44
	v_cvt_f32_ubyte1_e32 v125, v44
	v_cvt_f32_ubyte2_e32 v126, v44
	v_cvt_f32_ubyte3_e32 v127, v44
	v_cvt_f32_ubyte0_e32 v128, v45
	v_cvt_f32_ubyte1_e32 v129, v45
	v_cvt_f32_ubyte2_e32 v130, v45
	v_cvt_f32_ubyte3_e32 v131, v45
	s_lshl_b32 s30, s78, 12
	s_add_u32 s28, s26, s30
	s_addc_u32 s29, s27, 0
	global_load_dwordx2 v[44:45], v162, s[28:29]
	v_fmac_f32_e32 v178, s25, v124
	v_fmac_f32_e32 v179, s25, v125
	v_fmac_f32_e32 v180, s25, v126
	v_fmac_f32_e32 v181, s25, v127
	v_fmac_f32_e32 v182, s25, v128
	v_fmac_f32_e32 v183, s25, v129
	v_fmac_f32_e32 v184, s25, v130
	v_fmac_f32_e32 v185, s25, v131
	v_readlane_b32 s25, v246, 43
	v_cvt_f32_ubyte0_e32 v132, v46
	v_cvt_f32_ubyte1_e32 v133, v46
	v_cvt_f32_ubyte2_e32 v134, v46
	v_cvt_f32_ubyte3_e32 v135, v46
	v_cvt_f32_ubyte0_e32 v136, v47
	v_cvt_f32_ubyte1_e32 v137, v47
	v_cvt_f32_ubyte2_e32 v138, v47
	v_cvt_f32_ubyte3_e32 v139, v47
	s_lshl_b32 s30, s79, 12
	s_add_u32 s28, s26, s30
	s_addc_u32 s29, s27, 0
	global_load_dwordx2 v[46:47], v162, s[28:29]
	v_fmac_f32_e32 v178, s25, v132
	v_fmac_f32_e32 v179, s25, v133
	v_fmac_f32_e32 v180, s25, v134
	v_fmac_f32_e32 v181, s25, v135
	v_fmac_f32_e32 v182, s25, v136
	v_fmac_f32_e32 v183, s25, v137
	v_fmac_f32_e32 v184, s25, v138
	v_fmac_f32_e32 v185, s25, v139
	s_waitcnt vmcnt(28)
	v_readlane_b32 s25, v246, 44
	v_cvt_f32_ubyte0_e32 v124, v48
	v_cvt_f32_ubyte1_e32 v125, v48
	v_cvt_f32_ubyte2_e32 v126, v48
	v_cvt_f32_ubyte3_e32 v127, v48
	v_cvt_f32_ubyte0_e32 v128, v49
	v_cvt_f32_ubyte1_e32 v129, v49
	v_cvt_f32_ubyte2_e32 v130, v49
	v_cvt_f32_ubyte3_e32 v131, v49
	s_lshl_b32 s30, s80, 12
	s_add_u32 s28, s26, s30
	s_addc_u32 s29, s27, 0
	global_load_dwordx2 v[48:49], v162, s[28:29]
	v_fmac_f32_e32 v178, s25, v124
	v_fmac_f32_e32 v179, s25, v125
	v_fmac_f32_e32 v180, s25, v126
	v_fmac_f32_e32 v181, s25, v127
	v_fmac_f32_e32 v182, s25, v128
	v_fmac_f32_e32 v183, s25, v129
	v_fmac_f32_e32 v184, s25, v130
	v_fmac_f32_e32 v185, s25, v131
	v_readlane_b32 s25, v246, 45
	v_cvt_f32_ubyte0_e32 v132, v50
	v_cvt_f32_ubyte1_e32 v133, v50
	v_cvt_f32_ubyte2_e32 v134, v50
	v_cvt_f32_ubyte3_e32 v135, v50
	v_cvt_f32_ubyte0_e32 v136, v51
	v_cvt_f32_ubyte1_e32 v137, v51
	v_cvt_f32_ubyte2_e32 v138, v51
	v_cvt_f32_ubyte3_e32 v139, v51
	s_lshl_b32 s30, s81, 12
	s_add_u32 s28, s26, s30
	s_addc_u32 s29, s27, 0
	global_load_dwordx2 v[50:51], v162, s[28:29]
	v_fmac_f32_e32 v178, s25, v132
	v_fmac_f32_e32 v179, s25, v133
	v_fmac_f32_e32 v180, s25, v134
	v_fmac_f32_e32 v181, s25, v135
	v_fmac_f32_e32 v182, s25, v136
	v_fmac_f32_e32 v183, s25, v137
	v_fmac_f32_e32 v184, s25, v138
	v_fmac_f32_e32 v185, s25, v139
	v_readlane_b32 s25, v246, 46
	v_cvt_f32_ubyte0_e32 v124, v52
	v_cvt_f32_ubyte1_e32 v125, v52
	v_cvt_f32_ubyte2_e32 v126, v52
	v_cvt_f32_ubyte3_e32 v127, v52
	v_cvt_f32_ubyte0_e32 v128, v53
	v_cvt_f32_ubyte1_e32 v129, v53
	v_cvt_f32_ubyte2_e32 v130, v53
	v_cvt_f32_ubyte3_e32 v131, v53
	s_lshl_b32 s30, s82, 12
	s_add_u32 s28, s26, s30
	s_addc_u32 s29, s27, 0
	global_load_dwordx2 v[52:53], v162, s[28:29]
	v_fmac_f32_e32 v178, s25, v124
	v_fmac_f32_e32 v179, s25, v125
	v_fmac_f32_e32 v180, s25, v126
	v_fmac_f32_e32 v181, s25, v127
	v_fmac_f32_e32 v182, s25, v128
	v_fmac_f32_e32 v183, s25, v129
	v_fmac_f32_e32 v184, s25, v130
	v_fmac_f32_e32 v185, s25, v131
	v_readlane_b32 s25, v246, 47
	v_cvt_f32_ubyte0_e32 v132, v54
	v_cvt_f32_ubyte1_e32 v133, v54
	v_cvt_f32_ubyte2_e32 v134, v54
	v_cvt_f32_ubyte3_e32 v135, v54
	v_cvt_f32_ubyte0_e32 v136, v55
	v_cvt_f32_ubyte1_e32 v137, v55
	v_cvt_f32_ubyte2_e32 v138, v55
	v_cvt_f32_ubyte3_e32 v139, v55
	s_lshl_b32 s30, s83, 12
	s_add_u32 s28, s26, s30
	s_addc_u32 s29, s27, 0
	global_load_dwordx2 v[54:55], v162, s[28:29]
	v_fmac_f32_e32 v178, s25, v132
	v_fmac_f32_e32 v179, s25, v133
	v_fmac_f32_e32 v180, s25, v134
	v_fmac_f32_e32 v181, s25, v135
	v_fmac_f32_e32 v182, s25, v136
	v_fmac_f32_e32 v183, s25, v137
	v_fmac_f32_e32 v184, s25, v138
	v_fmac_f32_e32 v185, s25, v139
	s_waitcnt vmcnt(28)
	v_readlane_b32 s25, v246, 48
	v_cvt_f32_ubyte0_e32 v124, v56
	v_cvt_f32_ubyte1_e32 v125, v56
	v_cvt_f32_ubyte2_e32 v126, v56
	v_cvt_f32_ubyte3_e32 v127, v56
	v_cvt_f32_ubyte0_e32 v128, v57
	v_cvt_f32_ubyte1_e32 v129, v57
	v_cvt_f32_ubyte2_e32 v130, v57
	v_cvt_f32_ubyte3_e32 v131, v57
	s_waitcnt lgkmcnt(0)
	s_load_dwordx16 s[68:83], s[36:37], 0x180 glc
	s_lshl_b32 s30, s84, 12
	s_add_u32 s28, s26, s30
	s_addc_u32 s29, s27, 0
	global_load_dwordx2 v[56:57], v162, s[28:29]
	v_fmac_f32_e32 v178, s25, v124
	v_fmac_f32_e32 v179, s25, v125
	v_fmac_f32_e32 v180, s25, v126
	v_fmac_f32_e32 v181, s25, v127
	v_fmac_f32_e32 v182, s25, v128
	v_fmac_f32_e32 v183, s25, v129
	v_fmac_f32_e32 v184, s25, v130
	v_fmac_f32_e32 v185, s25, v131
	v_readlane_b32 s25, v246, 49
	v_cvt_f32_ubyte0_e32 v132, v58
	v_cvt_f32_ubyte1_e32 v133, v58
	v_cvt_f32_ubyte2_e32 v134, v58
	v_cvt_f32_ubyte3_e32 v135, v58
	v_cvt_f32_ubyte0_e32 v136, v59
	v_cvt_f32_ubyte1_e32 v137, v59
	v_cvt_f32_ubyte2_e32 v138, v59
	v_cvt_f32_ubyte3_e32 v139, v59
	s_lshl_b32 s30, s85, 12
	s_add_u32 s28, s26, s30
	s_addc_u32 s29, s27, 0
	global_load_dwordx2 v[58:59], v162, s[28:29]
	v_fmac_f32_e32 v178, s25, v132
	v_fmac_f32_e32 v179, s25, v133
	v_fmac_f32_e32 v180, s25, v134
	v_fmac_f32_e32 v181, s25, v135
	v_fmac_f32_e32 v182, s25, v136
	v_fmac_f32_e32 v183, s25, v137
	v_fmac_f32_e32 v184, s25, v138
	v_fmac_f32_e32 v185, s25, v139
	v_readlane_b32 s25, v246, 50
	v_cvt_f32_ubyte0_e32 v124, v60
	v_cvt_f32_ubyte1_e32 v125, v60
	v_cvt_f32_ubyte2_e32 v126, v60
	v_cvt_f32_ubyte3_e32 v127, v60
	v_cvt_f32_ubyte0_e32 v128, v61
	v_cvt_f32_ubyte1_e32 v129, v61
	v_cvt_f32_ubyte2_e32 v130, v61
	v_cvt_f32_ubyte3_e32 v131, v61
	s_lshl_b32 s30, s86, 12
	s_add_u32 s28, s26, s30
	s_addc_u32 s29, s27, 0
	global_load_dwordx2 v[60:61], v162, s[28:29]
	v_fmac_f32_e32 v178, s25, v124
	v_fmac_f32_e32 v179, s25, v125
	v_fmac_f32_e32 v180, s25, v126
	v_fmac_f32_e32 v181, s25, v127
	v_fmac_f32_e32 v182, s25, v128
	v_fmac_f32_e32 v183, s25, v129
	v_fmac_f32_e32 v184, s25, v130
	v_fmac_f32_e32 v185, s25, v131
	v_readlane_b32 s25, v246, 51
	v_cvt_f32_ubyte0_e32 v132, v62
	v_cvt_f32_ubyte1_e32 v133, v62
	v_cvt_f32_ubyte2_e32 v134, v62
	v_cvt_f32_ubyte3_e32 v135, v62
	v_cvt_f32_ubyte0_e32 v136, v63
	v_cvt_f32_ubyte1_e32 v137, v63
	v_cvt_f32_ubyte2_e32 v138, v63
	v_cvt_f32_ubyte3_e32 v139, v63
	s_lshl_b32 s30, s87, 12
	s_add_u32 s28, s26, s30
	s_addc_u32 s29, s27, 0
	global_load_dwordx2 v[62:63], v162, s[28:29]
	v_fmac_f32_e32 v178, s25, v132
	v_fmac_f32_e32 v179, s25, v133
	v_fmac_f32_e32 v180, s25, v134
	v_fmac_f32_e32 v181, s25, v135
	v_fmac_f32_e32 v182, s25, v136
	v_fmac_f32_e32 v183, s25, v137
	v_fmac_f32_e32 v184, s25, v138
	v_fmac_f32_e32 v185, s25, v139
	s_waitcnt vmcnt(28)
	v_readlane_b32 s25, v246, 52
	v_cvt_f32_ubyte0_e32 v124, v64
	v_cvt_f32_ubyte1_e32 v125, v64
	v_cvt_f32_ubyte2_e32 v126, v64
	v_cvt_f32_ubyte3_e32 v127, v64
	v_cvt_f32_ubyte0_e32 v128, v65
	v_cvt_f32_ubyte1_e32 v129, v65
	v_cvt_f32_ubyte2_e32 v130, v65
	v_cvt_f32_ubyte3_e32 v131, v65
	s_lshl_b32 s30, s88, 12
	s_add_u32 s28, s26, s30
	s_addc_u32 s29, s27, 0
	global_load_dwordx2 v[64:65], v162, s[28:29]
	v_fmac_f32_e32 v178, s25, v124
	v_fmac_f32_e32 v179, s25, v125
	v_fmac_f32_e32 v180, s25, v126
	v_fmac_f32_e32 v181, s25, v127
	v_fmac_f32_e32 v182, s25, v128
	v_fmac_f32_e32 v183, s25, v129
	v_fmac_f32_e32 v184, s25, v130
	v_fmac_f32_e32 v185, s25, v131
	v_readlane_b32 s25, v246, 53
	v_cvt_f32_ubyte0_e32 v132, v66
	v_cvt_f32_ubyte1_e32 v133, v66
	v_cvt_f32_ubyte2_e32 v134, v66
	v_cvt_f32_ubyte3_e32 v135, v66
	v_cvt_f32_ubyte0_e32 v136, v67
	v_cvt_f32_ubyte1_e32 v137, v67
	v_cvt_f32_ubyte2_e32 v138, v67
	v_cvt_f32_ubyte3_e32 v139, v67
	s_lshl_b32 s30, s89, 12
	s_add_u32 s28, s26, s30
	s_addc_u32 s29, s27, 0
	global_load_dwordx2 v[66:67], v162, s[28:29]
	v_fmac_f32_e32 v178, s25, v132
	v_fmac_f32_e32 v179, s25, v133
	v_fmac_f32_e32 v180, s25, v134
	v_fmac_f32_e32 v181, s25, v135
	v_fmac_f32_e32 v182, s25, v136
	v_fmac_f32_e32 v183, s25, v137
	v_fmac_f32_e32 v184, s25, v138
	v_fmac_f32_e32 v185, s25, v139
	v_readlane_b32 s25, v246, 54
	v_cvt_f32_ubyte0_e32 v124, v68
	v_cvt_f32_ubyte1_e32 v125, v68
	v_cvt_f32_ubyte2_e32 v126, v68
	v_cvt_f32_ubyte3_e32 v127, v68
	v_cvt_f32_ubyte0_e32 v128, v69
	v_cvt_f32_ubyte1_e32 v129, v69
	v_cvt_f32_ubyte2_e32 v130, v69
	v_cvt_f32_ubyte3_e32 v131, v69
	s_lshl_b32 s30, s90, 12
	s_add_u32 s28, s26, s30
	s_addc_u32 s29, s27, 0
	global_load_dwordx2 v[68:69], v162, s[28:29]
	v_fmac_f32_e32 v178, s25, v124
	v_fmac_f32_e32 v179, s25, v125
	v_fmac_f32_e32 v180, s25, v126
	v_fmac_f32_e32 v181, s25, v127
	v_fmac_f32_e32 v182, s25, v128
	v_fmac_f32_e32 v183, s25, v129
	v_fmac_f32_e32 v184, s25, v130
	v_fmac_f32_e32 v185, s25, v131
	v_readlane_b32 s25, v246, 55
	v_cvt_f32_ubyte0_e32 v132, v70
	v_cvt_f32_ubyte1_e32 v133, v70
	v_cvt_f32_ubyte2_e32 v134, v70
	v_cvt_f32_ubyte3_e32 v135, v70
	v_cvt_f32_ubyte0_e32 v136, v71
	v_cvt_f32_ubyte1_e32 v137, v71
	v_cvt_f32_ubyte2_e32 v138, v71
	v_cvt_f32_ubyte3_e32 v139, v71
	s_lshl_b32 s30, s91, 12
	s_add_u32 s28, s26, s30
	s_addc_u32 s29, s27, 0
	global_load_dwordx2 v[70:71], v162, s[28:29]
	v_fmac_f32_e32 v178, s25, v132
	v_fmac_f32_e32 v179, s25, v133
	v_fmac_f32_e32 v180, s25, v134
	v_fmac_f32_e32 v181, s25, v135
	v_fmac_f32_e32 v182, s25, v136
	v_fmac_f32_e32 v183, s25, v137
	v_fmac_f32_e32 v184, s25, v138
	v_fmac_f32_e32 v185, s25, v139
	s_waitcnt vmcnt(28)
	v_readlane_b32 s25, v246, 56
	v_cvt_f32_ubyte0_e32 v124, v72
	v_cvt_f32_ubyte1_e32 v125, v72
	v_cvt_f32_ubyte2_e32 v126, v72
	v_cvt_f32_ubyte3_e32 v127, v72
	v_cvt_f32_ubyte0_e32 v128, v73
	v_cvt_f32_ubyte1_e32 v129, v73
	v_cvt_f32_ubyte2_e32 v130, v73
	v_cvt_f32_ubyte3_e32 v131, v73
	s_lshl_b32 s30, s92, 12
	s_add_u32 s28, s26, s30
	s_addc_u32 s29, s27, 0
	global_load_dwordx2 v[72:73], v162, s[28:29]
	v_fmac_f32_e32 v178, s25, v124
	v_fmac_f32_e32 v179, s25, v125
	v_fmac_f32_e32 v180, s25, v126
	v_fmac_f32_e32 v181, s25, v127
	v_fmac_f32_e32 v182, s25, v128
	v_fmac_f32_e32 v183, s25, v129
	v_fmac_f32_e32 v184, s25, v130
	v_fmac_f32_e32 v185, s25, v131
	v_readlane_b32 s25, v246, 57
	v_cvt_f32_ubyte0_e32 v132, v74
	v_cvt_f32_ubyte1_e32 v133, v74
	v_cvt_f32_ubyte2_e32 v134, v74
	v_cvt_f32_ubyte3_e32 v135, v74
	v_cvt_f32_ubyte0_e32 v136, v75
	v_cvt_f32_ubyte1_e32 v137, v75
	v_cvt_f32_ubyte2_e32 v138, v75
	v_cvt_f32_ubyte3_e32 v139, v75
	s_lshl_b32 s30, s93, 12
	s_add_u32 s28, s26, s30
	s_addc_u32 s29, s27, 0
	global_load_dwordx2 v[74:75], v162, s[28:29]
	v_fmac_f32_e32 v178, s25, v132
	v_fmac_f32_e32 v179, s25, v133
	v_fmac_f32_e32 v180, s25, v134
	v_fmac_f32_e32 v181, s25, v135
	v_fmac_f32_e32 v182, s25, v136
	v_fmac_f32_e32 v183, s25, v137
	v_fmac_f32_e32 v184, s25, v138
	v_fmac_f32_e32 v185, s25, v139
	v_readlane_b32 s25, v246, 58
	v_cvt_f32_ubyte0_e32 v124, v76
	v_cvt_f32_ubyte1_e32 v125, v76
	v_cvt_f32_ubyte2_e32 v126, v76
	v_cvt_f32_ubyte3_e32 v127, v76
	v_cvt_f32_ubyte0_e32 v128, v77
	v_cvt_f32_ubyte1_e32 v129, v77
	v_cvt_f32_ubyte2_e32 v130, v77
	v_cvt_f32_ubyte3_e32 v131, v77
	s_lshl_b32 s30, s94, 12
	s_add_u32 s28, s26, s30
	s_addc_u32 s29, s27, 0
	global_load_dwordx2 v[76:77], v162, s[28:29]
	v_fmac_f32_e32 v178, s25, v124
	v_fmac_f32_e32 v179, s25, v125
	v_fmac_f32_e32 v180, s25, v126
	v_fmac_f32_e32 v181, s25, v127
	v_fmac_f32_e32 v182, s25, v128
	v_fmac_f32_e32 v183, s25, v129
	v_fmac_f32_e32 v184, s25, v130
	v_fmac_f32_e32 v185, s25, v131
	v_readlane_b32 s25, v246, 59
	v_cvt_f32_ubyte0_e32 v132, v78
	v_cvt_f32_ubyte1_e32 v133, v78
	v_cvt_f32_ubyte2_e32 v134, v78
	v_cvt_f32_ubyte3_e32 v135, v78
	v_cvt_f32_ubyte0_e32 v136, v79
	v_cvt_f32_ubyte1_e32 v137, v79
	v_cvt_f32_ubyte2_e32 v138, v79
	v_cvt_f32_ubyte3_e32 v139, v79
	s_lshl_b32 s30, s95, 12
	s_add_u32 s28, s26, s30
	s_addc_u32 s29, s27, 0
	global_load_dwordx2 v[78:79], v162, s[28:29]
	v_fmac_f32_e32 v178, s25, v132
	v_fmac_f32_e32 v179, s25, v133
	v_fmac_f32_e32 v180, s25, v134
	v_fmac_f32_e32 v181, s25, v135
	v_fmac_f32_e32 v182, s25, v136
	v_fmac_f32_e32 v183, s25, v137
	v_fmac_f32_e32 v184, s25, v138
	v_fmac_f32_e32 v185, s25, v139
	s_waitcnt vmcnt(28)
	v_readlane_b32 s25, v246, 60
	v_cvt_f32_ubyte0_e32 v124, v80
	v_cvt_f32_ubyte1_e32 v125, v80
	v_cvt_f32_ubyte2_e32 v126, v80
	v_cvt_f32_ubyte3_e32 v127, v80
	v_cvt_f32_ubyte0_e32 v128, v81
	v_cvt_f32_ubyte1_e32 v129, v81
	v_cvt_f32_ubyte2_e32 v130, v81
	v_cvt_f32_ubyte3_e32 v131, v81
	s_lshl_b32 s30, s96, 12
	s_add_u32 s28, s26, s30
	s_addc_u32 s29, s27, 0
	global_load_dwordx2 v[80:81], v162, s[28:29]
	v_fmac_f32_e32 v178, s25, v124
	v_fmac_f32_e32 v179, s25, v125
	v_fmac_f32_e32 v180, s25, v126
	v_fmac_f32_e32 v181, s25, v127
	v_fmac_f32_e32 v182, s25, v128
	v_fmac_f32_e32 v183, s25, v129
	v_fmac_f32_e32 v184, s25, v130
	v_fmac_f32_e32 v185, s25, v131
	v_readlane_b32 s25, v246, 61
	v_cvt_f32_ubyte0_e32 v132, v82
	v_cvt_f32_ubyte1_e32 v133, v82
	v_cvt_f32_ubyte2_e32 v134, v82
	v_cvt_f32_ubyte3_e32 v135, v82
	v_cvt_f32_ubyte0_e32 v136, v83
	v_cvt_f32_ubyte1_e32 v137, v83
	v_cvt_f32_ubyte2_e32 v138, v83
	v_cvt_f32_ubyte3_e32 v139, v83
	s_lshl_b32 s30, s97, 12
	s_add_u32 s28, s26, s30
	s_addc_u32 s29, s27, 0
	global_load_dwordx2 v[82:83], v162, s[28:29]
	v_fmac_f32_e32 v178, s25, v132
	v_fmac_f32_e32 v179, s25, v133
	v_fmac_f32_e32 v180, s25, v134
	v_fmac_f32_e32 v181, s25, v135
	v_fmac_f32_e32 v182, s25, v136
	v_fmac_f32_e32 v183, s25, v137
	v_fmac_f32_e32 v184, s25, v138
	v_fmac_f32_e32 v185, s25, v139
	v_readlane_b32 s25, v246, 62
	v_cvt_f32_ubyte0_e32 v124, v84
	v_cvt_f32_ubyte1_e32 v125, v84
	v_cvt_f32_ubyte2_e32 v126, v84
	v_cvt_f32_ubyte3_e32 v127, v84
	v_cvt_f32_ubyte0_e32 v128, v85
	v_cvt_f32_ubyte1_e32 v129, v85
	v_cvt_f32_ubyte2_e32 v130, v85
	v_cvt_f32_ubyte3_e32 v131, v85
	s_lshl_b32 s30, s98, 12
	s_add_u32 s28, s26, s30
	s_addc_u32 s29, s27, 0
	global_load_dwordx2 v[84:85], v162, s[28:29]
	v_fmac_f32_e32 v178, s25, v124
	v_fmac_f32_e32 v179, s25, v125
	v_fmac_f32_e32 v180, s25, v126
	v_fmac_f32_e32 v181, s25, v127
	v_fmac_f32_e32 v182, s25, v128
	v_fmac_f32_e32 v183, s25, v129
	v_fmac_f32_e32 v184, s25, v130
	v_fmac_f32_e32 v185, s25, v131
	v_readlane_b32 s25, v246, 63
	v_cvt_f32_ubyte0_e32 v132, v86
	v_cvt_f32_ubyte1_e32 v133, v86
	v_cvt_f32_ubyte2_e32 v134, v86
	v_cvt_f32_ubyte3_e32 v135, v86
	v_cvt_f32_ubyte0_e32 v136, v87
	v_cvt_f32_ubyte1_e32 v137, v87
	v_cvt_f32_ubyte2_e32 v138, v87
	v_cvt_f32_ubyte3_e32 v139, v87
	s_lshl_b32 s30, s99, 12
	s_add_u32 s28, s26, s30
	s_addc_u32 s29, s27, 0
	global_load_dwordx2 v[86:87], v162, s[28:29]
	v_fmac_f32_e32 v178, s25, v132
	v_fmac_f32_e32 v179, s25, v133
	v_fmac_f32_e32 v180, s25, v134
	v_fmac_f32_e32 v181, s25, v135
	v_fmac_f32_e32 v182, s25, v136
	v_fmac_f32_e32 v183, s25, v137
	v_fmac_f32_e32 v184, s25, v138
	v_fmac_f32_e32 v185, s25, v139
	s_waitcnt vmcnt(28)
	v_readlane_b32 s25, v247, 0
	v_cvt_f32_ubyte0_e32 v124, v24
	v_cvt_f32_ubyte1_e32 v125, v24
	v_cvt_f32_ubyte2_e32 v126, v24
	v_cvt_f32_ubyte3_e32 v127, v24
	v_cvt_f32_ubyte0_e32 v128, v25
	v_cvt_f32_ubyte1_e32 v129, v25
	v_cvt_f32_ubyte2_e32 v130, v25
	v_cvt_f32_ubyte3_e32 v131, v25
	s_waitcnt lgkmcnt(0)
	s_load_dwordx16 s[84:99], s[36:37], 0x1c0 glc
	s_lshl_b32 s30, s68, 12
	s_add_u32 s28, s26, s30
	s_addc_u32 s29, s27, 0
	global_load_dwordx2 v[24:25], v162, s[28:29]
	v_lshlrev_b32_e32 v16, 2, v122
	v_lshlrev_b32_e32 v17, 2, v123
	global_load_dword v238, v16, s[64:65]
	global_load_dword v240, v16, s[60:61]
	global_load_dword v239, v17, s[64:65]
	global_load_dword v241, v17, s[60:61]
	v_fmac_f32_e32 v178, s25, v124
	v_fmac_f32_e32 v179, s25, v125
	v_fmac_f32_e32 v180, s25, v126
	v_fmac_f32_e32 v181, s25, v127
	v_fmac_f32_e32 v182, s25, v128
	v_fmac_f32_e32 v183, s25, v129
	v_fmac_f32_e32 v184, s25, v130
	v_fmac_f32_e32 v185, s25, v131
	v_readlane_b32 s25, v247, 1
	v_cvt_f32_ubyte0_e32 v132, v26
	v_cvt_f32_ubyte1_e32 v133, v26
	v_cvt_f32_ubyte2_e32 v134, v26
	v_cvt_f32_ubyte3_e32 v135, v26
	v_cvt_f32_ubyte0_e32 v136, v27
	v_cvt_f32_ubyte1_e32 v137, v27
	v_cvt_f32_ubyte2_e32 v138, v27
	v_cvt_f32_ubyte3_e32 v139, v27
	s_lshl_b32 s30, s69, 12
	s_add_u32 s28, s26, s30
	s_addc_u32 s29, s27, 0
	global_load_dwordx2 v[26:27], v162, s[28:29]
	v_fmac_f32_e32 v178, s25, v132
	v_fmac_f32_e32 v179, s25, v133
	v_fmac_f32_e32 v180, s25, v134
	v_fmac_f32_e32 v181, s25, v135
	v_fmac_f32_e32 v182, s25, v136
	v_fmac_f32_e32 v183, s25, v137
	v_fmac_f32_e32 v184, s25, v138
	v_fmac_f32_e32 v185, s25, v139
	v_readlane_b32 s25, v247, 2
	v_cvt_f32_ubyte0_e32 v124, v28
	v_cvt_f32_ubyte1_e32 v125, v28
	v_cvt_f32_ubyte2_e32 v126, v28
	v_cvt_f32_ubyte3_e32 v127, v28
	v_cvt_f32_ubyte0_e32 v128, v29
	v_cvt_f32_ubyte1_e32 v129, v29
	v_cvt_f32_ubyte2_e32 v130, v29
	v_cvt_f32_ubyte3_e32 v131, v29
	s_lshl_b32 s30, s70, 12
	s_add_u32 s28, s26, s30
	s_addc_u32 s29, s27, 0
	global_load_dwordx2 v[28:29], v162, s[28:29]
	v_fmac_f32_e32 v178, s25, v124
	v_fmac_f32_e32 v179, s25, v125
	v_fmac_f32_e32 v180, s25, v126
	v_fmac_f32_e32 v181, s25, v127
	v_fmac_f32_e32 v182, s25, v128
	v_fmac_f32_e32 v183, s25, v129
	v_fmac_f32_e32 v184, s25, v130
	v_fmac_f32_e32 v185, s25, v131
	v_readlane_b32 s25, v247, 3
	v_cvt_f32_ubyte0_e32 v132, v30
	v_cvt_f32_ubyte1_e32 v133, v30
	v_cvt_f32_ubyte2_e32 v134, v30
	v_cvt_f32_ubyte3_e32 v135, v30
	v_cvt_f32_ubyte0_e32 v136, v31
	v_cvt_f32_ubyte1_e32 v137, v31
	v_cvt_f32_ubyte2_e32 v138, v31
	v_cvt_f32_ubyte3_e32 v139, v31
	s_lshl_b32 s30, s71, 12
	s_add_u32 s28, s26, s30
	s_addc_u32 s29, s27, 0
	global_load_dwordx2 v[30:31], v162, s[28:29]
	v_fmac_f32_e32 v178, s25, v132
	v_fmac_f32_e32 v179, s25, v133
	v_fmac_f32_e32 v180, s25, v134
	v_fmac_f32_e32 v181, s25, v135
	v_fmac_f32_e32 v182, s25, v136
	v_fmac_f32_e32 v183, s25, v137
	v_fmac_f32_e32 v184, s25, v138
	v_fmac_f32_e32 v185, s25, v139
	s_waitcnt vmcnt(32)
	v_readlane_b32 s25, v247, 4
	v_cvt_f32_ubyte0_e32 v124, v32
	v_cvt_f32_ubyte1_e32 v125, v32
	v_cvt_f32_ubyte2_e32 v126, v32
	v_cvt_f32_ubyte3_e32 v127, v32
	v_cvt_f32_ubyte0_e32 v128, v33
	v_cvt_f32_ubyte1_e32 v129, v33
	v_cvt_f32_ubyte2_e32 v130, v33
	v_cvt_f32_ubyte3_e32 v131, v33
	s_lshl_b32 s30, s72, 12
	s_add_u32 s28, s26, s30
	s_addc_u32 s29, s27, 0
	global_load_dwordx2 v[32:33], v162, s[28:29]
	v_fmac_f32_e32 v178, s25, v124
	v_fmac_f32_e32 v179, s25, v125
	v_fmac_f32_e32 v180, s25, v126
	v_fmac_f32_e32 v181, s25, v127
	v_fmac_f32_e32 v182, s25, v128
	v_fmac_f32_e32 v183, s25, v129
	v_fmac_f32_e32 v184, s25, v130
	v_fmac_f32_e32 v185, s25, v131
	v_readlane_b32 s25, v247, 5
	v_cvt_f32_ubyte0_e32 v132, v34
	v_cvt_f32_ubyte1_e32 v133, v34
	v_cvt_f32_ubyte2_e32 v134, v34
	v_cvt_f32_ubyte3_e32 v135, v34
	v_cvt_f32_ubyte0_e32 v136, v35
	v_cvt_f32_ubyte1_e32 v137, v35
	v_cvt_f32_ubyte2_e32 v138, v35
	v_cvt_f32_ubyte3_e32 v139, v35
	s_lshl_b32 s30, s73, 12
	s_add_u32 s28, s26, s30
	s_addc_u32 s29, s27, 0
	global_load_dwordx2 v[34:35], v162, s[28:29]
	v_fmac_f32_e32 v178, s25, v132
	v_fmac_f32_e32 v179, s25, v133
	v_fmac_f32_e32 v180, s25, v134
	v_fmac_f32_e32 v181, s25, v135
	v_fmac_f32_e32 v182, s25, v136
	v_fmac_f32_e32 v183, s25, v137
	v_fmac_f32_e32 v184, s25, v138
	v_fmac_f32_e32 v185, s25, v139
	v_readlane_b32 s25, v247, 6
	v_cvt_f32_ubyte0_e32 v124, v36
	v_cvt_f32_ubyte1_e32 v125, v36
	v_cvt_f32_ubyte2_e32 v126, v36
	v_cvt_f32_ubyte3_e32 v127, v36
	v_cvt_f32_ubyte0_e32 v128, v37
	v_cvt_f32_ubyte1_e32 v129, v37
	v_cvt_f32_ubyte2_e32 v130, v37
	v_cvt_f32_ubyte3_e32 v131, v37
	s_lshl_b32 s30, s74, 12
	s_add_u32 s28, s26, s30
	s_addc_u32 s29, s27, 0
	global_load_dwordx2 v[36:37], v162, s[28:29]
	v_fmac_f32_e32 v178, s25, v124
	v_fmac_f32_e32 v179, s25, v125
	v_fmac_f32_e32 v180, s25, v126
	v_fmac_f32_e32 v181, s25, v127
	v_fmac_f32_e32 v182, s25, v128
	v_fmac_f32_e32 v183, s25, v129
	v_fmac_f32_e32 v184, s25, v130
	v_fmac_f32_e32 v185, s25, v131
	v_readlane_b32 s25, v247, 7
	v_cvt_f32_ubyte0_e32 v132, v38
	v_cvt_f32_ubyte1_e32 v133, v38
	v_cvt_f32_ubyte2_e32 v134, v38
	v_cvt_f32_ubyte3_e32 v135, v38
	v_cvt_f32_ubyte0_e32 v136, v39
	v_cvt_f32_ubyte1_e32 v137, v39
	v_cvt_f32_ubyte2_e32 v138, v39
	v_cvt_f32_ubyte3_e32 v139, v39
	s_lshl_b32 s30, s75, 12
	s_add_u32 s28, s26, s30
	s_addc_u32 s29, s27, 0
	global_load_dwordx2 v[38:39], v162, s[28:29]
	v_fmac_f32_e32 v178, s25, v132
	v_fmac_f32_e32 v179, s25, v133
	v_fmac_f32_e32 v180, s25, v134
	v_fmac_f32_e32 v181, s25, v135
	v_fmac_f32_e32 v182, s25, v136
	v_fmac_f32_e32 v183, s25, v137
	v_fmac_f32_e32 v184, s25, v138
	v_fmac_f32_e32 v185, s25, v139
	s_waitcnt vmcnt(32)
	v_readlane_b32 s25, v247, 8
	v_cvt_f32_ubyte0_e32 v124, v40
	v_cvt_f32_ubyte1_e32 v125, v40
	v_cvt_f32_ubyte2_e32 v126, v40
	v_cvt_f32_ubyte3_e32 v127, v40
	v_cvt_f32_ubyte0_e32 v128, v41
	v_cvt_f32_ubyte1_e32 v129, v41
	v_cvt_f32_ubyte2_e32 v130, v41
	v_cvt_f32_ubyte3_e32 v131, v41
	s_lshl_b32 s30, s76, 12
	s_add_u32 s28, s26, s30
	s_addc_u32 s29, s27, 0
	global_load_dwordx2 v[40:41], v162, s[28:29]
	v_fmac_f32_e32 v178, s25, v124
	v_fmac_f32_e32 v179, s25, v125
	v_fmac_f32_e32 v180, s25, v126
	v_fmac_f32_e32 v181, s25, v127
	v_fmac_f32_e32 v182, s25, v128
	v_fmac_f32_e32 v183, s25, v129
	v_fmac_f32_e32 v184, s25, v130
	v_fmac_f32_e32 v185, s25, v131
	v_readlane_b32 s25, v247, 9
	v_cvt_f32_ubyte0_e32 v132, v42
	v_cvt_f32_ubyte1_e32 v133, v42
	v_cvt_f32_ubyte2_e32 v134, v42
	v_cvt_f32_ubyte3_e32 v135, v42
	v_cvt_f32_ubyte0_e32 v136, v43
	v_cvt_f32_ubyte1_e32 v137, v43
	v_cvt_f32_ubyte2_e32 v138, v43
	v_cvt_f32_ubyte3_e32 v139, v43
	s_lshl_b32 s30, s77, 12
	s_add_u32 s28, s26, s30
	s_addc_u32 s29, s27, 0
	global_load_dwordx2 v[42:43], v162, s[28:29]
	v_fmac_f32_e32 v178, s25, v132
	v_fmac_f32_e32 v179, s25, v133
	v_fmac_f32_e32 v180, s25, v134
	v_fmac_f32_e32 v181, s25, v135
	v_fmac_f32_e32 v182, s25, v136
	v_fmac_f32_e32 v183, s25, v137
	v_fmac_f32_e32 v184, s25, v138
	v_fmac_f32_e32 v185, s25, v139
	v_readlane_b32 s25, v247, 10
	v_cvt_f32_ubyte0_e32 v124, v44
	v_cvt_f32_ubyte1_e32 v125, v44
	v_cvt_f32_ubyte2_e32 v126, v44
	v_cvt_f32_ubyte3_e32 v127, v44
	v_cvt_f32_ubyte0_e32 v128, v45
	v_cvt_f32_ubyte1_e32 v129, v45
	v_cvt_f32_ubyte2_e32 v130, v45
	v_cvt_f32_ubyte3_e32 v131, v45
	s_lshl_b32 s30, s78, 12
	s_add_u32 s28, s26, s30
	s_addc_u32 s29, s27, 0
	global_load_dwordx2 v[44:45], v162, s[28:29]
	v_fmac_f32_e32 v178, s25, v124
	v_fmac_f32_e32 v179, s25, v125
	v_fmac_f32_e32 v180, s25, v126
	v_fmac_f32_e32 v181, s25, v127
	v_fmac_f32_e32 v182, s25, v128
	v_fmac_f32_e32 v183, s25, v129
	v_fmac_f32_e32 v184, s25, v130
	v_fmac_f32_e32 v185, s25, v131
	v_readlane_b32 s25, v247, 11
	v_cvt_f32_ubyte0_e32 v132, v46
	v_cvt_f32_ubyte1_e32 v133, v46
	v_cvt_f32_ubyte2_e32 v134, v46
	v_cvt_f32_ubyte3_e32 v135, v46
	v_cvt_f32_ubyte0_e32 v136, v47
	v_cvt_f32_ubyte1_e32 v137, v47
	v_cvt_f32_ubyte2_e32 v138, v47
	v_cvt_f32_ubyte3_e32 v139, v47
	s_lshl_b32 s30, s79, 12
	s_add_u32 s28, s26, s30
	s_addc_u32 s29, s27, 0
	global_load_dwordx2 v[46:47], v162, s[28:29]
	v_fmac_f32_e32 v178, s25, v132
	v_fmac_f32_e32 v179, s25, v133
	v_fmac_f32_e32 v180, s25, v134
	v_fmac_f32_e32 v181, s25, v135
	v_fmac_f32_e32 v182, s25, v136
	v_fmac_f32_e32 v183, s25, v137
	v_fmac_f32_e32 v184, s25, v138
	v_fmac_f32_e32 v185, s25, v139
	s_waitcnt vmcnt(32)
	v_readlane_b32 s25, v247, 12
	v_cvt_f32_ubyte0_e32 v124, v48
	v_cvt_f32_ubyte1_e32 v125, v48
	v_cvt_f32_ubyte2_e32 v126, v48
	v_cvt_f32_ubyte3_e32 v127, v48
	v_cvt_f32_ubyte0_e32 v128, v49
	v_cvt_f32_ubyte1_e32 v129, v49
	v_cvt_f32_ubyte2_e32 v130, v49
	v_cvt_f32_ubyte3_e32 v131, v49
	s_lshl_b32 s30, s80, 12
	s_add_u32 s28, s26, s30
	s_addc_u32 s29, s27, 0
	global_load_dwordx2 v[48:49], v162, s[28:29]
	v_fmac_f32_e32 v178, s25, v124
	v_fmac_f32_e32 v179, s25, v125
	v_fmac_f32_e32 v180, s25, v126
	v_fmac_f32_e32 v181, s25, v127
	v_fmac_f32_e32 v182, s25, v128
	v_fmac_f32_e32 v183, s25, v129
	v_fmac_f32_e32 v184, s25, v130
	v_fmac_f32_e32 v185, s25, v131
	v_readlane_b32 s25, v247, 13
	v_cvt_f32_ubyte0_e32 v132, v50
	v_cvt_f32_ubyte1_e32 v133, v50
	v_cvt_f32_ubyte2_e32 v134, v50
	v_cvt_f32_ubyte3_e32 v135, v50
	v_cvt_f32_ubyte0_e32 v136, v51
	v_cvt_f32_ubyte1_e32 v137, v51
	v_cvt_f32_ubyte2_e32 v138, v51
	v_cvt_f32_ubyte3_e32 v139, v51
	s_lshl_b32 s30, s81, 12
	s_add_u32 s28, s26, s30
	s_addc_u32 s29, s27, 0
	global_load_dwordx2 v[50:51], v162, s[28:29]
	v_fmac_f32_e32 v178, s25, v132
	v_fmac_f32_e32 v179, s25, v133
	v_fmac_f32_e32 v180, s25, v134
	v_fmac_f32_e32 v181, s25, v135
	v_fmac_f32_e32 v182, s25, v136
	v_fmac_f32_e32 v183, s25, v137
	v_fmac_f32_e32 v184, s25, v138
	v_fmac_f32_e32 v185, s25, v139
	v_readlane_b32 s25, v247, 14
	v_cvt_f32_ubyte0_e32 v124, v52
	v_cvt_f32_ubyte1_e32 v125, v52
	v_cvt_f32_ubyte2_e32 v126, v52
	v_cvt_f32_ubyte3_e32 v127, v52
	v_cvt_f32_ubyte0_e32 v128, v53
	v_cvt_f32_ubyte1_e32 v129, v53
	v_cvt_f32_ubyte2_e32 v130, v53
	v_cvt_f32_ubyte3_e32 v131, v53
	s_lshl_b32 s30, s82, 12
	s_add_u32 s28, s26, s30
	s_addc_u32 s29, s27, 0
	global_load_dwordx2 v[52:53], v162, s[28:29]
	v_fmac_f32_e32 v178, s25, v124
	v_fmac_f32_e32 v179, s25, v125
	v_fmac_f32_e32 v180, s25, v126
	v_fmac_f32_e32 v181, s25, v127
	v_fmac_f32_e32 v182, s25, v128
	v_fmac_f32_e32 v183, s25, v129
	v_fmac_f32_e32 v184, s25, v130
	v_fmac_f32_e32 v185, s25, v131
	v_readlane_b32 s25, v247, 15
	v_cvt_f32_ubyte0_e32 v132, v54
	v_cvt_f32_ubyte1_e32 v133, v54
	v_cvt_f32_ubyte2_e32 v134, v54
	v_cvt_f32_ubyte3_e32 v135, v54
	v_cvt_f32_ubyte0_e32 v136, v55
	v_cvt_f32_ubyte1_e32 v137, v55
	v_cvt_f32_ubyte2_e32 v138, v55
	v_cvt_f32_ubyte3_e32 v139, v55
	s_lshl_b32 s30, s83, 12
	s_add_u32 s28, s26, s30
	s_addc_u32 s29, s27, 0
	global_load_dwordx2 v[54:55], v162, s[28:29]
	v_fmac_f32_e32 v178, s25, v132
	v_fmac_f32_e32 v179, s25, v133
	v_fmac_f32_e32 v180, s25, v134
	v_fmac_f32_e32 v181, s25, v135
	v_fmac_f32_e32 v182, s25, v136
	v_fmac_f32_e32 v183, s25, v137
	v_fmac_f32_e32 v184, s25, v138
	v_fmac_f32_e32 v185, s25, v139
	s_waitcnt vmcnt(32)
	v_readlane_b32 s25, v247, 16
	v_cvt_f32_ubyte0_e32 v124, v56
	v_cvt_f32_ubyte1_e32 v125, v56
	v_cvt_f32_ubyte2_e32 v126, v56
	v_cvt_f32_ubyte3_e32 v127, v56
	v_cvt_f32_ubyte0_e32 v128, v57
	v_cvt_f32_ubyte1_e32 v129, v57
	v_cvt_f32_ubyte2_e32 v130, v57
	v_cvt_f32_ubyte3_e32 v131, v57
	s_waitcnt lgkmcnt(0)
	s_load_dwordx16 s[68:83], s[38:39], 0x0 glc
	s_lshl_b32 s30, s84, 12
	s_add_u32 s28, s26, s30
	s_addc_u32 s29, s27, 0
	global_load_dwordx2 v[56:57], v162, s[28:29]
	v_fmac_f32_e32 v178, s25, v124
	v_fmac_f32_e32 v179, s25, v125
	v_fmac_f32_e32 v180, s25, v126
	v_fmac_f32_e32 v181, s25, v127
	v_fmac_f32_e32 v182, s25, v128
	v_fmac_f32_e32 v183, s25, v129
	v_fmac_f32_e32 v184, s25, v130
	v_fmac_f32_e32 v185, s25, v131
	v_readlane_b32 s25, v247, 17
	v_cvt_f32_ubyte0_e32 v132, v58
	v_cvt_f32_ubyte1_e32 v133, v58
	v_cvt_f32_ubyte2_e32 v134, v58
	v_cvt_f32_ubyte3_e32 v135, v58
	v_cvt_f32_ubyte0_e32 v136, v59
	v_cvt_f32_ubyte1_e32 v137, v59
	v_cvt_f32_ubyte2_e32 v138, v59
	v_cvt_f32_ubyte3_e32 v139, v59
	s_lshl_b32 s30, s85, 12
	s_add_u32 s28, s26, s30
	s_addc_u32 s29, s27, 0
	global_load_dwordx2 v[58:59], v162, s[28:29]
	v_fmac_f32_e32 v178, s25, v132
	v_fmac_f32_e32 v179, s25, v133
	v_fmac_f32_e32 v180, s25, v134
	v_fmac_f32_e32 v181, s25, v135
	v_fmac_f32_e32 v182, s25, v136
	v_fmac_f32_e32 v183, s25, v137
	v_fmac_f32_e32 v184, s25, v138
	v_fmac_f32_e32 v185, s25, v139
	v_readlane_b32 s25, v247, 18
	v_cvt_f32_ubyte0_e32 v124, v60
	v_cvt_f32_ubyte1_e32 v125, v60
	v_cvt_f32_ubyte2_e32 v126, v60
	v_cvt_f32_ubyte3_e32 v127, v60
	v_cvt_f32_ubyte0_e32 v128, v61
	v_cvt_f32_ubyte1_e32 v129, v61
	v_cvt_f32_ubyte2_e32 v130, v61
	v_cvt_f32_ubyte3_e32 v131, v61
	s_lshl_b32 s30, s86, 12
	s_add_u32 s28, s26, s30
	s_addc_u32 s29, s27, 0
	global_load_dwordx2 v[60:61], v162, s[28:29]
	v_fmac_f32_e32 v178, s25, v124
	v_fmac_f32_e32 v179, s25, v125
	v_fmac_f32_e32 v180, s25, v126
	v_fmac_f32_e32 v181, s25, v127
	v_fmac_f32_e32 v182, s25, v128
	v_fmac_f32_e32 v183, s25, v129
	v_fmac_f32_e32 v184, s25, v130
	v_fmac_f32_e32 v185, s25, v131
	v_readlane_b32 s25, v247, 19
	v_cvt_f32_ubyte0_e32 v132, v62
	v_cvt_f32_ubyte1_e32 v133, v62
	v_cvt_f32_ubyte2_e32 v134, v62
	v_cvt_f32_ubyte3_e32 v135, v62
	v_cvt_f32_ubyte0_e32 v136, v63
	v_cvt_f32_ubyte1_e32 v137, v63
	v_cvt_f32_ubyte2_e32 v138, v63
	v_cvt_f32_ubyte3_e32 v139, v63
	s_lshl_b32 s30, s87, 12
	s_add_u32 s28, s26, s30
	s_addc_u32 s29, s27, 0
	global_load_dwordx2 v[62:63], v162, s[28:29]
	v_fmac_f32_e32 v178, s25, v132
	v_fmac_f32_e32 v179, s25, v133
	v_fmac_f32_e32 v180, s25, v134
	v_fmac_f32_e32 v181, s25, v135
	v_fmac_f32_e32 v182, s25, v136
	v_fmac_f32_e32 v183, s25, v137
	v_fmac_f32_e32 v184, s25, v138
	v_fmac_f32_e32 v185, s25, v139
	s_waitcnt vmcnt(32)
	v_readlane_b32 s25, v247, 20
	v_cvt_f32_ubyte0_e32 v124, v64
	v_cvt_f32_ubyte1_e32 v125, v64
	v_cvt_f32_ubyte2_e32 v126, v64
	v_cvt_f32_ubyte3_e32 v127, v64
	v_cvt_f32_ubyte0_e32 v128, v65
	v_cvt_f32_ubyte1_e32 v129, v65
	v_cvt_f32_ubyte2_e32 v130, v65
	v_cvt_f32_ubyte3_e32 v131, v65
	s_lshl_b32 s30, s88, 12
	s_add_u32 s28, s26, s30
	s_addc_u32 s29, s27, 0
	global_load_dwordx2 v[64:65], v162, s[28:29]
	v_fmac_f32_e32 v178, s25, v124
	v_fmac_f32_e32 v179, s25, v125
	v_fmac_f32_e32 v180, s25, v126
	v_fmac_f32_e32 v181, s25, v127
	v_fmac_f32_e32 v182, s25, v128
	v_fmac_f32_e32 v183, s25, v129
	v_fmac_f32_e32 v184, s25, v130
	v_fmac_f32_e32 v185, s25, v131
	v_readlane_b32 s25, v247, 21
	v_cvt_f32_ubyte0_e32 v132, v66
	v_cvt_f32_ubyte1_e32 v133, v66
	v_cvt_f32_ubyte2_e32 v134, v66
	v_cvt_f32_ubyte3_e32 v135, v66
	v_cvt_f32_ubyte0_e32 v136, v67
	v_cvt_f32_ubyte1_e32 v137, v67
	v_cvt_f32_ubyte2_e32 v138, v67
	v_cvt_f32_ubyte3_e32 v139, v67
	s_lshl_b32 s30, s89, 12
	s_add_u32 s28, s26, s30
	s_addc_u32 s29, s27, 0
	global_load_dwordx2 v[66:67], v162, s[28:29]
	v_fmac_f32_e32 v178, s25, v132
	v_fmac_f32_e32 v179, s25, v133
	v_fmac_f32_e32 v180, s25, v134
	v_fmac_f32_e32 v181, s25, v135
	v_fmac_f32_e32 v182, s25, v136
	v_fmac_f32_e32 v183, s25, v137
	v_fmac_f32_e32 v184, s25, v138
	v_fmac_f32_e32 v185, s25, v139
	v_readlane_b32 s25, v247, 22
	v_cvt_f32_ubyte0_e32 v124, v68
	v_cvt_f32_ubyte1_e32 v125, v68
	v_cvt_f32_ubyte2_e32 v126, v68
	v_cvt_f32_ubyte3_e32 v127, v68
	v_cvt_f32_ubyte0_e32 v128, v69
	v_cvt_f32_ubyte1_e32 v129, v69
	v_cvt_f32_ubyte2_e32 v130, v69
	v_cvt_f32_ubyte3_e32 v131, v69
	s_lshl_b32 s30, s90, 12
	s_add_u32 s28, s26, s30
	s_addc_u32 s29, s27, 0
	global_load_dwordx2 v[68:69], v162, s[28:29]
	v_fmac_f32_e32 v178, s25, v124
	v_fmac_f32_e32 v179, s25, v125
	v_fmac_f32_e32 v180, s25, v126
	v_fmac_f32_e32 v181, s25, v127
	v_fmac_f32_e32 v182, s25, v128
	v_fmac_f32_e32 v183, s25, v129
	v_fmac_f32_e32 v184, s25, v130
	v_fmac_f32_e32 v185, s25, v131
	v_readlane_b32 s25, v247, 23
	v_cvt_f32_ubyte0_e32 v132, v70
	v_cvt_f32_ubyte1_e32 v133, v70
	v_cvt_f32_ubyte2_e32 v134, v70
	v_cvt_f32_ubyte3_e32 v135, v70
	v_cvt_f32_ubyte0_e32 v136, v71
	v_cvt_f32_ubyte1_e32 v137, v71
	v_cvt_f32_ubyte2_e32 v138, v71
	v_cvt_f32_ubyte3_e32 v139, v71
	s_lshl_b32 s30, s91, 12
	s_add_u32 s28, s26, s30
	s_addc_u32 s29, s27, 0
	global_load_dwordx2 v[70:71], v162, s[28:29]
	v_fmac_f32_e32 v178, s25, v132
	v_fmac_f32_e32 v179, s25, v133
	v_fmac_f32_e32 v180, s25, v134
	v_fmac_f32_e32 v181, s25, v135
	v_fmac_f32_e32 v182, s25, v136
	v_fmac_f32_e32 v183, s25, v137
	v_fmac_f32_e32 v184, s25, v138
	v_fmac_f32_e32 v185, s25, v139
	s_waitcnt vmcnt(32)
	v_readlane_b32 s25, v247, 24
	v_cvt_f32_ubyte0_e32 v124, v72
	v_cvt_f32_ubyte1_e32 v125, v72
	v_cvt_f32_ubyte2_e32 v126, v72
	v_cvt_f32_ubyte3_e32 v127, v72
	v_cvt_f32_ubyte0_e32 v128, v73
	v_cvt_f32_ubyte1_e32 v129, v73
	v_cvt_f32_ubyte2_e32 v130, v73
	v_cvt_f32_ubyte3_e32 v131, v73
	s_lshl_b32 s30, s92, 12
	s_add_u32 s28, s26, s30
	s_addc_u32 s29, s27, 0
	global_load_dwordx2 v[72:73], v162, s[28:29]
	v_fmac_f32_e32 v178, s25, v124
	v_fmac_f32_e32 v179, s25, v125
	v_fmac_f32_e32 v180, s25, v126
	v_fmac_f32_e32 v181, s25, v127
	v_fmac_f32_e32 v182, s25, v128
	v_fmac_f32_e32 v183, s25, v129
	v_fmac_f32_e32 v184, s25, v130
	v_fmac_f32_e32 v185, s25, v131
	v_readlane_b32 s25, v247, 25
	v_cvt_f32_ubyte0_e32 v132, v74
	v_cvt_f32_ubyte1_e32 v133, v74
	v_cvt_f32_ubyte2_e32 v134, v74
	v_cvt_f32_ubyte3_e32 v135, v74
	v_cvt_f32_ubyte0_e32 v136, v75
	v_cvt_f32_ubyte1_e32 v137, v75
	v_cvt_f32_ubyte2_e32 v138, v75
	v_cvt_f32_ubyte3_e32 v139, v75
	s_lshl_b32 s30, s93, 12
	s_add_u32 s28, s26, s30
	s_addc_u32 s29, s27, 0
	global_load_dwordx2 v[74:75], v162, s[28:29]
	v_fmac_f32_e32 v178, s25, v132
	v_fmac_f32_e32 v179, s25, v133
	v_fmac_f32_e32 v180, s25, v134
	v_fmac_f32_e32 v181, s25, v135
	v_fmac_f32_e32 v182, s25, v136
	v_fmac_f32_e32 v183, s25, v137
	v_fmac_f32_e32 v184, s25, v138
	v_fmac_f32_e32 v185, s25, v139
	v_readlane_b32 s25, v247, 26
	v_cvt_f32_ubyte0_e32 v124, v76
	v_cvt_f32_ubyte1_e32 v125, v76
	v_cvt_f32_ubyte2_e32 v126, v76
	v_cvt_f32_ubyte3_e32 v127, v76
	v_cvt_f32_ubyte0_e32 v128, v77
	v_cvt_f32_ubyte1_e32 v129, v77
	v_cvt_f32_ubyte2_e32 v130, v77
	v_cvt_f32_ubyte3_e32 v131, v77
	s_lshl_b32 s30, s94, 12
	s_add_u32 s28, s26, s30
	s_addc_u32 s29, s27, 0
	global_load_dwordx2 v[76:77], v162, s[28:29]
	v_fmac_f32_e32 v178, s25, v124
	v_fmac_f32_e32 v179, s25, v125
	v_fmac_f32_e32 v180, s25, v126
	v_fmac_f32_e32 v181, s25, v127
	v_fmac_f32_e32 v182, s25, v128
	v_fmac_f32_e32 v183, s25, v129
	v_fmac_f32_e32 v184, s25, v130
	v_fmac_f32_e32 v185, s25, v131
	v_readlane_b32 s25, v247, 27
	v_cvt_f32_ubyte0_e32 v132, v78
	v_cvt_f32_ubyte1_e32 v133, v78
	v_cvt_f32_ubyte2_e32 v134, v78
	v_cvt_f32_ubyte3_e32 v135, v78
	v_cvt_f32_ubyte0_e32 v136, v79
	v_cvt_f32_ubyte1_e32 v137, v79
	v_cvt_f32_ubyte2_e32 v138, v79
	v_cvt_f32_ubyte3_e32 v139, v79
	s_lshl_b32 s30, s95, 12
	s_add_u32 s28, s26, s30
	s_addc_u32 s29, s27, 0
	global_load_dwordx2 v[78:79], v162, s[28:29]
	v_fmac_f32_e32 v178, s25, v132
	v_fmac_f32_e32 v179, s25, v133
	v_fmac_f32_e32 v180, s25, v134
	v_fmac_f32_e32 v181, s25, v135
	v_fmac_f32_e32 v182, s25, v136
	v_fmac_f32_e32 v183, s25, v137
	v_fmac_f32_e32 v184, s25, v138
	v_fmac_f32_e32 v185, s25, v139
	s_waitcnt vmcnt(32)
	v_readlane_b32 s25, v247, 28
	v_cvt_f32_ubyte0_e32 v124, v80
	v_cvt_f32_ubyte1_e32 v125, v80
	v_cvt_f32_ubyte2_e32 v126, v80
	v_cvt_f32_ubyte3_e32 v127, v80
	v_cvt_f32_ubyte0_e32 v128, v81
	v_cvt_f32_ubyte1_e32 v129, v81
	v_cvt_f32_ubyte2_e32 v130, v81
	v_cvt_f32_ubyte3_e32 v131, v81
	s_lshl_b32 s30, s96, 12
	s_add_u32 s28, s26, s30
	s_addc_u32 s29, s27, 0
	global_load_dwordx2 v[80:81], v162, s[28:29]
	v_fmac_f32_e32 v178, s25, v124
	v_fmac_f32_e32 v179, s25, v125
	v_fmac_f32_e32 v180, s25, v126
	v_fmac_f32_e32 v181, s25, v127
	v_fmac_f32_e32 v182, s25, v128
	v_fmac_f32_e32 v183, s25, v129
	v_fmac_f32_e32 v184, s25, v130
	v_fmac_f32_e32 v185, s25, v131
	v_readlane_b32 s25, v247, 29
	v_cvt_f32_ubyte0_e32 v132, v82
	v_cvt_f32_ubyte1_e32 v133, v82
	v_cvt_f32_ubyte2_e32 v134, v82
	v_cvt_f32_ubyte3_e32 v135, v82
	v_cvt_f32_ubyte0_e32 v136, v83
	v_cvt_f32_ubyte1_e32 v137, v83
	v_cvt_f32_ubyte2_e32 v138, v83
	v_cvt_f32_ubyte3_e32 v139, v83
	s_lshl_b32 s30, s97, 12
	s_add_u32 s28, s26, s30
	s_addc_u32 s29, s27, 0
	global_load_dwordx2 v[82:83], v162, s[28:29]
	v_fmac_f32_e32 v178, s25, v132
	v_fmac_f32_e32 v179, s25, v133
	v_fmac_f32_e32 v180, s25, v134
	v_fmac_f32_e32 v181, s25, v135
	v_fmac_f32_e32 v182, s25, v136
	v_fmac_f32_e32 v183, s25, v137
	v_fmac_f32_e32 v184, s25, v138
	v_fmac_f32_e32 v185, s25, v139
	v_readlane_b32 s25, v247, 30
	v_cvt_f32_ubyte0_e32 v124, v84
	v_cvt_f32_ubyte1_e32 v125, v84
	v_cvt_f32_ubyte2_e32 v126, v84
	v_cvt_f32_ubyte3_e32 v127, v84
	v_cvt_f32_ubyte0_e32 v128, v85
	v_cvt_f32_ubyte1_e32 v129, v85
	v_cvt_f32_ubyte2_e32 v130, v85
	v_cvt_f32_ubyte3_e32 v131, v85
	s_lshl_b32 s30, s98, 12
	s_add_u32 s28, s26, s30
	s_addc_u32 s29, s27, 0
	global_load_dwordx2 v[84:85], v162, s[28:29]
	v_fmac_f32_e32 v178, s25, v124
	v_fmac_f32_e32 v179, s25, v125
	v_fmac_f32_e32 v180, s25, v126
	v_fmac_f32_e32 v181, s25, v127
	v_fmac_f32_e32 v182, s25, v128
	v_fmac_f32_e32 v183, s25, v129
	v_fmac_f32_e32 v184, s25, v130
	v_fmac_f32_e32 v185, s25, v131
	v_readlane_b32 s25, v247, 31
	v_cvt_f32_ubyte0_e32 v132, v86
	v_cvt_f32_ubyte1_e32 v133, v86
	v_cvt_f32_ubyte2_e32 v134, v86
	v_cvt_f32_ubyte3_e32 v135, v86
	v_cvt_f32_ubyte0_e32 v136, v87
	v_cvt_f32_ubyte1_e32 v137, v87
	v_cvt_f32_ubyte2_e32 v138, v87
	v_cvt_f32_ubyte3_e32 v139, v87
	s_lshl_b32 s30, s99, 12
	s_add_u32 s28, s26, s30
	s_addc_u32 s29, s27, 0
	global_load_dwordx2 v[86:87], v162, s[28:29]
	v_fmac_f32_e32 v178, s25, v132
	v_fmac_f32_e32 v179, s25, v133
	v_fmac_f32_e32 v180, s25, v134
	v_fmac_f32_e32 v181, s25, v135
	v_fmac_f32_e32 v182, s25, v136
	v_fmac_f32_e32 v183, s25, v137
	v_fmac_f32_e32 v184, s25, v138
	v_fmac_f32_e32 v185, s25, v139
	s_waitcnt vmcnt(28)
	v_readlane_b32 s25, v247, 32
	v_cvt_f32_ubyte0_e32 v124, v24
	v_cvt_f32_ubyte1_e32 v125, v24
	v_cvt_f32_ubyte2_e32 v126, v24
	v_cvt_f32_ubyte3_e32 v127, v24
	v_cvt_f32_ubyte0_e32 v128, v25
	v_cvt_f32_ubyte1_e32 v129, v25
	v_cvt_f32_ubyte2_e32 v130, v25
	v_cvt_f32_ubyte3_e32 v131, v25
	v_fmac_f32_e32 v178, s25, v124
	v_fmac_f32_e32 v179, s25, v125
	v_fmac_f32_e32 v180, s25, v126
	v_fmac_f32_e32 v181, s25, v127
	v_fmac_f32_e32 v182, s25, v128
	v_fmac_f32_e32 v183, s25, v129
	v_fmac_f32_e32 v184, s25, v130
	v_fmac_f32_e32 v185, s25, v131
	v_readlane_b32 s25, v247, 33
	v_cvt_f32_ubyte0_e32 v132, v26
	v_cvt_f32_ubyte1_e32 v133, v26
	v_cvt_f32_ubyte2_e32 v134, v26
	v_cvt_f32_ubyte3_e32 v135, v26
	v_cvt_f32_ubyte0_e32 v136, v27
	v_cvt_f32_ubyte1_e32 v137, v27
	v_cvt_f32_ubyte2_e32 v138, v27
	v_cvt_f32_ubyte3_e32 v139, v27
	v_fmac_f32_e32 v178, s25, v132
	v_fmac_f32_e32 v179, s25, v133
	v_fmac_f32_e32 v180, s25, v134
	v_fmac_f32_e32 v181, s25, v135
	v_fmac_f32_e32 v182, s25, v136
	v_fmac_f32_e32 v183, s25, v137
	v_fmac_f32_e32 v184, s25, v138
	v_fmac_f32_e32 v185, s25, v139
	v_readlane_b32 s25, v247, 34
	v_cvt_f32_ubyte0_e32 v124, v28
	v_cvt_f32_ubyte1_e32 v125, v28
	v_cvt_f32_ubyte2_e32 v126, v28
	v_cvt_f32_ubyte3_e32 v127, v28
	v_cvt_f32_ubyte0_e32 v128, v29
	v_cvt_f32_ubyte1_e32 v129, v29
	v_cvt_f32_ubyte2_e32 v130, v29
	v_cvt_f32_ubyte3_e32 v131, v29
	v_fmac_f32_e32 v178, s25, v124
	v_fmac_f32_e32 v179, s25, v125
	v_fmac_f32_e32 v180, s25, v126
	v_fmac_f32_e32 v181, s25, v127
	v_fmac_f32_e32 v182, s25, v128
	v_fmac_f32_e32 v183, s25, v129
	v_fmac_f32_e32 v184, s25, v130
	v_fmac_f32_e32 v185, s25, v131
	v_readlane_b32 s25, v247, 35
	v_cvt_f32_ubyte0_e32 v132, v30
	v_cvt_f32_ubyte1_e32 v133, v30
	v_cvt_f32_ubyte2_e32 v134, v30
	v_cvt_f32_ubyte3_e32 v135, v30
	v_cvt_f32_ubyte0_e32 v136, v31
	v_cvt_f32_ubyte1_e32 v137, v31
	v_cvt_f32_ubyte2_e32 v138, v31
	v_cvt_f32_ubyte3_e32 v139, v31
	v_fmac_f32_e32 v178, s25, v132
	v_fmac_f32_e32 v179, s25, v133
	v_fmac_f32_e32 v180, s25, v134
	v_fmac_f32_e32 v181, s25, v135
	v_fmac_f32_e32 v182, s25, v136
	v_fmac_f32_e32 v183, s25, v137
	v_fmac_f32_e32 v184, s25, v138
	v_fmac_f32_e32 v185, s25, v139
	s_waitcnt vmcnt(24)
	v_readlane_b32 s25, v247, 36
	v_cvt_f32_ubyte0_e32 v124, v32
	v_cvt_f32_ubyte1_e32 v125, v32
	v_cvt_f32_ubyte2_e32 v126, v32
	v_cvt_f32_ubyte3_e32 v127, v32
	v_cvt_f32_ubyte0_e32 v128, v33
	v_cvt_f32_ubyte1_e32 v129, v33
	v_cvt_f32_ubyte2_e32 v130, v33
	v_cvt_f32_ubyte3_e32 v131, v33
	v_fmac_f32_e32 v178, s25, v124
	v_fmac_f32_e32 v179, s25, v125
	v_fmac_f32_e32 v180, s25, v126
	v_fmac_f32_e32 v181, s25, v127
	v_fmac_f32_e32 v182, s25, v128
	v_fmac_f32_e32 v183, s25, v129
	v_fmac_f32_e32 v184, s25, v130
	v_fmac_f32_e32 v185, s25, v131
	v_readlane_b32 s25, v247, 37
	v_cvt_f32_ubyte0_e32 v132, v34
	v_cvt_f32_ubyte1_e32 v133, v34
	v_cvt_f32_ubyte2_e32 v134, v34
	v_cvt_f32_ubyte3_e32 v135, v34
	v_cvt_f32_ubyte0_e32 v136, v35
	v_cvt_f32_ubyte1_e32 v137, v35
	v_cvt_f32_ubyte2_e32 v138, v35
	v_cvt_f32_ubyte3_e32 v139, v35
	v_fmac_f32_e32 v178, s25, v132
	v_fmac_f32_e32 v179, s25, v133
	v_fmac_f32_e32 v180, s25, v134
	v_fmac_f32_e32 v181, s25, v135
	v_fmac_f32_e32 v182, s25, v136
	v_fmac_f32_e32 v183, s25, v137
	v_fmac_f32_e32 v184, s25, v138
	v_fmac_f32_e32 v185, s25, v139
	v_readlane_b32 s25, v247, 38
	v_cvt_f32_ubyte0_e32 v124, v36
	v_cvt_f32_ubyte1_e32 v125, v36
	v_cvt_f32_ubyte2_e32 v126, v36
	v_cvt_f32_ubyte3_e32 v127, v36
	v_cvt_f32_ubyte0_e32 v128, v37
	v_cvt_f32_ubyte1_e32 v129, v37
	v_cvt_f32_ubyte2_e32 v130, v37
	v_cvt_f32_ubyte3_e32 v131, v37
	v_fmac_f32_e32 v178, s25, v124
	v_fmac_f32_e32 v179, s25, v125
	v_fmac_f32_e32 v180, s25, v126
	v_fmac_f32_e32 v181, s25, v127
	v_fmac_f32_e32 v182, s25, v128
	v_fmac_f32_e32 v183, s25, v129
	v_fmac_f32_e32 v184, s25, v130
	v_fmac_f32_e32 v185, s25, v131
	v_readlane_b32 s25, v247, 39
	v_cvt_f32_ubyte0_e32 v132, v38
	v_cvt_f32_ubyte1_e32 v133, v38
	v_cvt_f32_ubyte2_e32 v134, v38
	v_cvt_f32_ubyte3_e32 v135, v38
	v_cvt_f32_ubyte0_e32 v136, v39
	v_cvt_f32_ubyte1_e32 v137, v39
	v_cvt_f32_ubyte2_e32 v138, v39
	v_cvt_f32_ubyte3_e32 v139, v39
	v_fmac_f32_e32 v178, s25, v132
	v_fmac_f32_e32 v179, s25, v133
	v_fmac_f32_e32 v180, s25, v134
	v_fmac_f32_e32 v181, s25, v135
	v_fmac_f32_e32 v182, s25, v136
	v_fmac_f32_e32 v183, s25, v137
	v_fmac_f32_e32 v184, s25, v138
	v_fmac_f32_e32 v185, s25, v139
	s_waitcnt vmcnt(20)
	v_readlane_b32 s25, v247, 40
	v_cvt_f32_ubyte0_e32 v124, v40
	v_cvt_f32_ubyte1_e32 v125, v40
	v_cvt_f32_ubyte2_e32 v126, v40
	v_cvt_f32_ubyte3_e32 v127, v40
	v_cvt_f32_ubyte0_e32 v128, v41
	v_cvt_f32_ubyte1_e32 v129, v41
	v_cvt_f32_ubyte2_e32 v130, v41
	v_cvt_f32_ubyte3_e32 v131, v41
	v_fmac_f32_e32 v178, s25, v124
	v_fmac_f32_e32 v179, s25, v125
	v_fmac_f32_e32 v180, s25, v126
	v_fmac_f32_e32 v181, s25, v127
	v_fmac_f32_e32 v182, s25, v128
	v_fmac_f32_e32 v183, s25, v129
	v_fmac_f32_e32 v184, s25, v130
	v_fmac_f32_e32 v185, s25, v131
	v_readlane_b32 s25, v247, 41
	v_cvt_f32_ubyte0_e32 v132, v42
	v_cvt_f32_ubyte1_e32 v133, v42
	v_cvt_f32_ubyte2_e32 v134, v42
	v_cvt_f32_ubyte3_e32 v135, v42
	v_cvt_f32_ubyte0_e32 v136, v43
	v_cvt_f32_ubyte1_e32 v137, v43
	v_cvt_f32_ubyte2_e32 v138, v43
	v_cvt_f32_ubyte3_e32 v139, v43
	v_fmac_f32_e32 v178, s25, v132
	v_fmac_f32_e32 v179, s25, v133
	v_fmac_f32_e32 v180, s25, v134
	v_fmac_f32_e32 v181, s25, v135
	v_fmac_f32_e32 v182, s25, v136
	v_fmac_f32_e32 v183, s25, v137
	v_fmac_f32_e32 v184, s25, v138
	v_fmac_f32_e32 v185, s25, v139
	v_readlane_b32 s25, v247, 42
	v_cvt_f32_ubyte0_e32 v124, v44
	v_cvt_f32_ubyte1_e32 v125, v44
	v_cvt_f32_ubyte2_e32 v126, v44
	v_cvt_f32_ubyte3_e32 v127, v44
	v_cvt_f32_ubyte0_e32 v128, v45
	v_cvt_f32_ubyte1_e32 v129, v45
	v_cvt_f32_ubyte2_e32 v130, v45
	v_cvt_f32_ubyte3_e32 v131, v45
	v_fmac_f32_e32 v178, s25, v124
	v_fmac_f32_e32 v179, s25, v125
	v_fmac_f32_e32 v180, s25, v126
	v_fmac_f32_e32 v181, s25, v127
	v_fmac_f32_e32 v182, s25, v128
	v_fmac_f32_e32 v183, s25, v129
	v_fmac_f32_e32 v184, s25, v130
	v_fmac_f32_e32 v185, s25, v131
	v_readlane_b32 s25, v247, 43
	v_cvt_f32_ubyte0_e32 v132, v46
	v_cvt_f32_ubyte1_e32 v133, v46
	v_cvt_f32_ubyte2_e32 v134, v46
	v_cvt_f32_ubyte3_e32 v135, v46
	v_cvt_f32_ubyte0_e32 v136, v47
	v_cvt_f32_ubyte1_e32 v137, v47
	v_cvt_f32_ubyte2_e32 v138, v47
	v_cvt_f32_ubyte3_e32 v139, v47
	v_fmac_f32_e32 v178, s25, v132
	v_fmac_f32_e32 v179, s25, v133
	v_fmac_f32_e32 v180, s25, v134
	v_fmac_f32_e32 v181, s25, v135
	v_fmac_f32_e32 v182, s25, v136
	v_fmac_f32_e32 v183, s25, v137
	v_fmac_f32_e32 v184, s25, v138
	v_fmac_f32_e32 v185, s25, v139
	s_waitcnt vmcnt(16)
	v_readlane_b32 s25, v247, 44
	v_cvt_f32_ubyte0_e32 v124, v48
	v_cvt_f32_ubyte1_e32 v125, v48
	v_cvt_f32_ubyte2_e32 v126, v48
	v_cvt_f32_ubyte3_e32 v127, v48
	v_cvt_f32_ubyte0_e32 v128, v49
	v_cvt_f32_ubyte1_e32 v129, v49
	v_cvt_f32_ubyte2_e32 v130, v49
	v_cvt_f32_ubyte3_e32 v131, v49
	v_fmac_f32_e32 v178, s25, v124
	v_fmac_f32_e32 v179, s25, v125
	v_fmac_f32_e32 v180, s25, v126
	v_fmac_f32_e32 v181, s25, v127
	v_fmac_f32_e32 v182, s25, v128
	v_fmac_f32_e32 v183, s25, v129
	v_fmac_f32_e32 v184, s25, v130
	v_fmac_f32_e32 v185, s25, v131
	v_readlane_b32 s25, v247, 45
	v_cvt_f32_ubyte0_e32 v132, v50
	v_cvt_f32_ubyte1_e32 v133, v50
	v_cvt_f32_ubyte2_e32 v134, v50
	v_cvt_f32_ubyte3_e32 v135, v50
	v_cvt_f32_ubyte0_e32 v136, v51
	v_cvt_f32_ubyte1_e32 v137, v51
	v_cvt_f32_ubyte2_e32 v138, v51
	v_cvt_f32_ubyte3_e32 v139, v51
	v_fmac_f32_e32 v178, s25, v132
	v_fmac_f32_e32 v179, s25, v133
	v_fmac_f32_e32 v180, s25, v134
	v_fmac_f32_e32 v181, s25, v135
	v_fmac_f32_e32 v182, s25, v136
	v_fmac_f32_e32 v183, s25, v137
	v_fmac_f32_e32 v184, s25, v138
	v_fmac_f32_e32 v185, s25, v139
	v_readlane_b32 s25, v247, 46
	v_cvt_f32_ubyte0_e32 v124, v52
	v_cvt_f32_ubyte1_e32 v125, v52
	v_cvt_f32_ubyte2_e32 v126, v52
	v_cvt_f32_ubyte3_e32 v127, v52
	v_cvt_f32_ubyte0_e32 v128, v53
	v_cvt_f32_ubyte1_e32 v129, v53
	v_cvt_f32_ubyte2_e32 v130, v53
	v_cvt_f32_ubyte3_e32 v131, v53
	v_fmac_f32_e32 v178, s25, v124
	v_fmac_f32_e32 v179, s25, v125
	v_fmac_f32_e32 v180, s25, v126
	v_fmac_f32_e32 v181, s25, v127
	v_fmac_f32_e32 v182, s25, v128
	v_fmac_f32_e32 v183, s25, v129
	v_fmac_f32_e32 v184, s25, v130
	v_fmac_f32_e32 v185, s25, v131
	v_readlane_b32 s25, v247, 47
	v_cvt_f32_ubyte0_e32 v132, v54
	v_cvt_f32_ubyte1_e32 v133, v54
	v_cvt_f32_ubyte2_e32 v134, v54
	v_cvt_f32_ubyte3_e32 v135, v54
	v_cvt_f32_ubyte0_e32 v136, v55
	v_cvt_f32_ubyte1_e32 v137, v55
	v_cvt_f32_ubyte2_e32 v138, v55
	v_cvt_f32_ubyte3_e32 v139, v55
	v_fmac_f32_e32 v178, s25, v132
	v_fmac_f32_e32 v179, s25, v133
	v_fmac_f32_e32 v180, s25, v134
	v_fmac_f32_e32 v181, s25, v135
	v_fmac_f32_e32 v182, s25, v136
	v_fmac_f32_e32 v183, s25, v137
	v_fmac_f32_e32 v184, s25, v138
	v_fmac_f32_e32 v185, s25, v139
	s_waitcnt vmcnt(12)
	v_readlane_b32 s25, v247, 48
	v_cvt_f32_ubyte0_e32 v124, v56
	v_cvt_f32_ubyte1_e32 v125, v56
	v_cvt_f32_ubyte2_e32 v126, v56
	v_cvt_f32_ubyte3_e32 v127, v56
	v_cvt_f32_ubyte0_e32 v128, v57
	v_cvt_f32_ubyte1_e32 v129, v57
	v_cvt_f32_ubyte2_e32 v130, v57
	v_cvt_f32_ubyte3_e32 v131, v57
	v_fmac_f32_e32 v178, s25, v124
	v_fmac_f32_e32 v179, s25, v125
	v_fmac_f32_e32 v180, s25, v126
	v_fmac_f32_e32 v181, s25, v127
	v_fmac_f32_e32 v182, s25, v128
	v_fmac_f32_e32 v183, s25, v129
	v_fmac_f32_e32 v184, s25, v130
	v_fmac_f32_e32 v185, s25, v131
	v_readlane_b32 s25, v247, 49
	v_cvt_f32_ubyte0_e32 v132, v58
	v_cvt_f32_ubyte1_e32 v133, v58
	v_cvt_f32_ubyte2_e32 v134, v58
	v_cvt_f32_ubyte3_e32 v135, v58
	v_cvt_f32_ubyte0_e32 v136, v59
	v_cvt_f32_ubyte1_e32 v137, v59
	v_cvt_f32_ubyte2_e32 v138, v59
	v_cvt_f32_ubyte3_e32 v139, v59
	v_fmac_f32_e32 v178, s25, v132
	v_fmac_f32_e32 v179, s25, v133
	v_fmac_f32_e32 v180, s25, v134
	v_fmac_f32_e32 v181, s25, v135
	v_fmac_f32_e32 v182, s25, v136
	v_fmac_f32_e32 v183, s25, v137
	v_fmac_f32_e32 v184, s25, v138
	v_fmac_f32_e32 v185, s25, v139
	v_readlane_b32 s25, v247, 50
	v_cvt_f32_ubyte0_e32 v124, v60
	v_cvt_f32_ubyte1_e32 v125, v60
	v_cvt_f32_ubyte2_e32 v126, v60
	v_cvt_f32_ubyte3_e32 v127, v60
	v_cvt_f32_ubyte0_e32 v128, v61
	v_cvt_f32_ubyte1_e32 v129, v61
	v_cvt_f32_ubyte2_e32 v130, v61
	v_cvt_f32_ubyte3_e32 v131, v61
	v_fmac_f32_e32 v178, s25, v124
	v_fmac_f32_e32 v179, s25, v125
	v_fmac_f32_e32 v180, s25, v126
	v_fmac_f32_e32 v181, s25, v127
	v_fmac_f32_e32 v182, s25, v128
	v_fmac_f32_e32 v183, s25, v129
	v_fmac_f32_e32 v184, s25, v130
	v_fmac_f32_e32 v185, s25, v131
	v_readlane_b32 s25, v247, 51
	v_cvt_f32_ubyte0_e32 v132, v62
	v_cvt_f32_ubyte1_e32 v133, v62
	v_cvt_f32_ubyte2_e32 v134, v62
	v_cvt_f32_ubyte3_e32 v135, v62
	v_cvt_f32_ubyte0_e32 v136, v63
	v_cvt_f32_ubyte1_e32 v137, v63
	v_cvt_f32_ubyte2_e32 v138, v63
	v_cvt_f32_ubyte3_e32 v139, v63
	v_fmac_f32_e32 v178, s25, v132
	v_fmac_f32_e32 v179, s25, v133
	v_fmac_f32_e32 v180, s25, v134
	v_fmac_f32_e32 v181, s25, v135
	v_fmac_f32_e32 v182, s25, v136
	v_fmac_f32_e32 v183, s25, v137
	v_fmac_f32_e32 v184, s25, v138
	v_fmac_f32_e32 v185, s25, v139
	s_waitcnt vmcnt(8)
	v_readlane_b32 s25, v247, 52
	v_cvt_f32_ubyte0_e32 v124, v64
	v_cvt_f32_ubyte1_e32 v125, v64
	v_cvt_f32_ubyte2_e32 v126, v64
	v_cvt_f32_ubyte3_e32 v127, v64
	v_cvt_f32_ubyte0_e32 v128, v65
	v_cvt_f32_ubyte1_e32 v129, v65
	v_cvt_f32_ubyte2_e32 v130, v65
	v_cvt_f32_ubyte3_e32 v131, v65
	v_fmac_f32_e32 v178, s25, v124
	v_fmac_f32_e32 v179, s25, v125
	v_fmac_f32_e32 v180, s25, v126
	v_fmac_f32_e32 v181, s25, v127
	v_fmac_f32_e32 v182, s25, v128
	v_fmac_f32_e32 v183, s25, v129
	v_fmac_f32_e32 v184, s25, v130
	v_fmac_f32_e32 v185, s25, v131
	v_readlane_b32 s25, v247, 53
	v_cvt_f32_ubyte0_e32 v132, v66
	v_cvt_f32_ubyte1_e32 v133, v66
	v_cvt_f32_ubyte2_e32 v134, v66
	v_cvt_f32_ubyte3_e32 v135, v66
	v_cvt_f32_ubyte0_e32 v136, v67
	v_cvt_f32_ubyte1_e32 v137, v67
	v_cvt_f32_ubyte2_e32 v138, v67
	v_cvt_f32_ubyte3_e32 v139, v67
	v_fmac_f32_e32 v178, s25, v132
	v_fmac_f32_e32 v179, s25, v133
	v_fmac_f32_e32 v180, s25, v134
	v_fmac_f32_e32 v181, s25, v135
	v_fmac_f32_e32 v182, s25, v136
	v_fmac_f32_e32 v183, s25, v137
	v_fmac_f32_e32 v184, s25, v138
	v_fmac_f32_e32 v185, s25, v139
	v_readlane_b32 s25, v247, 54
	v_cvt_f32_ubyte0_e32 v124, v68
	v_cvt_f32_ubyte1_e32 v125, v68
	v_cvt_f32_ubyte2_e32 v126, v68
	v_cvt_f32_ubyte3_e32 v127, v68
	v_cvt_f32_ubyte0_e32 v128, v69
	v_cvt_f32_ubyte1_e32 v129, v69
	v_cvt_f32_ubyte2_e32 v130, v69
	v_cvt_f32_ubyte3_e32 v131, v69
	v_fmac_f32_e32 v178, s25, v124
	v_fmac_f32_e32 v179, s25, v125
	v_fmac_f32_e32 v180, s25, v126
	v_fmac_f32_e32 v181, s25, v127
	v_fmac_f32_e32 v182, s25, v128
	v_fmac_f32_e32 v183, s25, v129
	v_fmac_f32_e32 v184, s25, v130
	v_fmac_f32_e32 v185, s25, v131
	v_readlane_b32 s25, v247, 55
	v_cvt_f32_ubyte0_e32 v132, v70
	v_cvt_f32_ubyte1_e32 v133, v70
	v_cvt_f32_ubyte2_e32 v134, v70
	v_cvt_f32_ubyte3_e32 v135, v70
	v_cvt_f32_ubyte0_e32 v136, v71
	v_cvt_f32_ubyte1_e32 v137, v71
	v_cvt_f32_ubyte2_e32 v138, v71
	v_cvt_f32_ubyte3_e32 v139, v71
	v_fmac_f32_e32 v178, s25, v132
	v_fmac_f32_e32 v179, s25, v133
	v_fmac_f32_e32 v180, s25, v134
	v_fmac_f32_e32 v181, s25, v135
	v_fmac_f32_e32 v182, s25, v136
	v_fmac_f32_e32 v183, s25, v137
	v_fmac_f32_e32 v184, s25, v138
	v_fmac_f32_e32 v185, s25, v139
	s_waitcnt vmcnt(4)
	v_readlane_b32 s25, v247, 56
	v_cvt_f32_ubyte0_e32 v124, v72
	v_cvt_f32_ubyte1_e32 v125, v72
	v_cvt_f32_ubyte2_e32 v126, v72
	v_cvt_f32_ubyte3_e32 v127, v72
	v_cvt_f32_ubyte0_e32 v128, v73
	v_cvt_f32_ubyte1_e32 v129, v73
	v_cvt_f32_ubyte2_e32 v130, v73
	v_cvt_f32_ubyte3_e32 v131, v73
	v_fmac_f32_e32 v178, s25, v124
	v_fmac_f32_e32 v179, s25, v125
	v_fmac_f32_e32 v180, s25, v126
	v_fmac_f32_e32 v181, s25, v127
	v_fmac_f32_e32 v182, s25, v128
	v_fmac_f32_e32 v183, s25, v129
	v_fmac_f32_e32 v184, s25, v130
	v_fmac_f32_e32 v185, s25, v131
	v_readlane_b32 s25, v247, 57
	v_cvt_f32_ubyte0_e32 v132, v74
	v_cvt_f32_ubyte1_e32 v133, v74
	v_cvt_f32_ubyte2_e32 v134, v74
	v_cvt_f32_ubyte3_e32 v135, v74
	v_cvt_f32_ubyte0_e32 v136, v75
	v_cvt_f32_ubyte1_e32 v137, v75
	v_cvt_f32_ubyte2_e32 v138, v75
	v_cvt_f32_ubyte3_e32 v139, v75
	v_fmac_f32_e32 v178, s25, v132
	v_fmac_f32_e32 v179, s25, v133
	v_fmac_f32_e32 v180, s25, v134
	v_fmac_f32_e32 v181, s25, v135
	v_fmac_f32_e32 v182, s25, v136
	v_fmac_f32_e32 v183, s25, v137
	v_fmac_f32_e32 v184, s25, v138
	v_fmac_f32_e32 v185, s25, v139
	v_readlane_b32 s25, v247, 58
	v_cvt_f32_ubyte0_e32 v124, v76
	v_cvt_f32_ubyte1_e32 v125, v76
	v_cvt_f32_ubyte2_e32 v126, v76
	v_cvt_f32_ubyte3_e32 v127, v76
	v_cvt_f32_ubyte0_e32 v128, v77
	v_cvt_f32_ubyte1_e32 v129, v77
	v_cvt_f32_ubyte2_e32 v130, v77
	v_cvt_f32_ubyte3_e32 v131, v77
	v_fmac_f32_e32 v178, s25, v124
	v_fmac_f32_e32 v179, s25, v125
	v_fmac_f32_e32 v180, s25, v126
	v_fmac_f32_e32 v181, s25, v127
	v_fmac_f32_e32 v182, s25, v128
	v_fmac_f32_e32 v183, s25, v129
	v_fmac_f32_e32 v184, s25, v130
	v_fmac_f32_e32 v185, s25, v131
	v_readlane_b32 s25, v247, 59
	v_cvt_f32_ubyte0_e32 v132, v78
	v_cvt_f32_ubyte1_e32 v133, v78
	v_cvt_f32_ubyte2_e32 v134, v78
	v_cvt_f32_ubyte3_e32 v135, v78
	v_cvt_f32_ubyte0_e32 v136, v79
	v_cvt_f32_ubyte1_e32 v137, v79
	v_cvt_f32_ubyte2_e32 v138, v79
	v_cvt_f32_ubyte3_e32 v139, v79
	v_fmac_f32_e32 v178, s25, v132
	v_fmac_f32_e32 v179, s25, v133
	v_fmac_f32_e32 v180, s25, v134
	v_fmac_f32_e32 v181, s25, v135
	v_fmac_f32_e32 v182, s25, v136
	v_fmac_f32_e32 v183, s25, v137
	v_fmac_f32_e32 v184, s25, v138
	v_fmac_f32_e32 v185, s25, v139
	s_waitcnt vmcnt(0)
	v_readlane_b32 s25, v247, 60
	v_cvt_f32_ubyte0_e32 v124, v80
	v_cvt_f32_ubyte1_e32 v125, v80
	v_cvt_f32_ubyte2_e32 v126, v80
	v_cvt_f32_ubyte3_e32 v127, v80
	v_cvt_f32_ubyte0_e32 v128, v81
	v_cvt_f32_ubyte1_e32 v129, v81
	v_cvt_f32_ubyte2_e32 v130, v81
	v_cvt_f32_ubyte3_e32 v131, v81
	v_fmac_f32_e32 v178, s25, v124
	v_fmac_f32_e32 v179, s25, v125
	v_fmac_f32_e32 v180, s25, v126
	v_fmac_f32_e32 v181, s25, v127
	v_fmac_f32_e32 v182, s25, v128
	v_fmac_f32_e32 v183, s25, v129
	v_fmac_f32_e32 v184, s25, v130
	v_fmac_f32_e32 v185, s25, v131
	v_readlane_b32 s25, v247, 61
	v_cvt_f32_ubyte0_e32 v132, v82
	v_cvt_f32_ubyte1_e32 v133, v82
	v_cvt_f32_ubyte2_e32 v134, v82
	v_cvt_f32_ubyte3_e32 v135, v82
	v_cvt_f32_ubyte0_e32 v136, v83
	v_cvt_f32_ubyte1_e32 v137, v83
	v_cvt_f32_ubyte2_e32 v138, v83
	v_cvt_f32_ubyte3_e32 v139, v83
	v_fmac_f32_e32 v178, s25, v132
	v_fmac_f32_e32 v179, s25, v133
	v_fmac_f32_e32 v180, s25, v134
	v_fmac_f32_e32 v181, s25, v135
	v_fmac_f32_e32 v182, s25, v136
	v_fmac_f32_e32 v183, s25, v137
	v_fmac_f32_e32 v184, s25, v138
	v_fmac_f32_e32 v185, s25, v139
	v_readlane_b32 s25, v247, 62
	v_cvt_f32_ubyte0_e32 v124, v84
	v_cvt_f32_ubyte1_e32 v125, v84
	v_cvt_f32_ubyte2_e32 v126, v84
	v_cvt_f32_ubyte3_e32 v127, v84
	v_cvt_f32_ubyte0_e32 v128, v85
	v_cvt_f32_ubyte1_e32 v129, v85
	v_cvt_f32_ubyte2_e32 v130, v85
	v_cvt_f32_ubyte3_e32 v131, v85
	v_fmac_f32_e32 v178, s25, v124
	v_fmac_f32_e32 v179, s25, v125
	v_fmac_f32_e32 v180, s25, v126
	v_fmac_f32_e32 v181, s25, v127
	v_fmac_f32_e32 v182, s25, v128
	v_fmac_f32_e32 v183, s25, v129
	v_fmac_f32_e32 v184, s25, v130
	v_fmac_f32_e32 v185, s25, v131
	v_readlane_b32 s25, v247, 63
	v_cvt_f32_ubyte0_e32 v132, v86
	v_cvt_f32_ubyte1_e32 v133, v86
	v_cvt_f32_ubyte2_e32 v134, v86
	v_cvt_f32_ubyte3_e32 v135, v86
	v_cvt_f32_ubyte0_e32 v136, v87
	v_cvt_f32_ubyte1_e32 v137, v87
	v_cvt_f32_ubyte2_e32 v138, v87
	v_cvt_f32_ubyte3_e32 v139, v87
	v_fmac_f32_e32 v178, s25, v132
	v_fmac_f32_e32 v179, s25, v133
	v_fmac_f32_e32 v180, s25, v134
	v_fmac_f32_e32 v181, s25, v135
	v_fmac_f32_e32 v182, s25, v136
	v_fmac_f32_e32 v183, s25, v137
	v_fmac_f32_e32 v184, s25, v138
	v_fmac_f32_e32 v185, s25, v139
	v_lshlrev_b32_e32 v132, 16, v242
	v_and_b32_e32 v133, 0xffff0000, v242
	v_lshlrev_b32_e32 v134, 16, v243
	v_and_b32_e32 v135, 0xffff0000, v243
	v_lshlrev_b32_e32 v136, 16, v244
	v_and_b32_e32 v137, 0xffff0000, v244
	v_lshlrev_b32_e32 v138, 16, v245
	v_and_b32_e32 v139, 0xffff0000, v245
	v_add_f32_e32 v178, v178, v248
	v_add_f32_e32 v179, v179, v248
	v_add_f32_e32 v180, v180, v248
	v_add_f32_e32 v181, v181, v248
	v_add_f32_e32 v182, v182, v248
	v_add_f32_e32 v183, v183, v248
	v_add_f32_e32 v184, v184, v248
	v_add_f32_e32 v185, v185, v248
	v_add_f32_e32 v124, v132, v178
	v_add_f32_e32 v125, v133, v179
	v_add_f32_e32 v126, v134, v180
	v_add_f32_e32 v127, v135, v181
	v_add_f32_e32 v128, v136, v182
	v_add_f32_e32 v129, v137, v183
	v_add_f32_e32 v130, v138, v184
	v_add_f32_e32 v131, v139, v185
	v_mul_f32_e32 v16, v124, v124
	v_fmac_f32_e32 v16, v125, v125
	v_fmac_f32_e32 v16, v126, v126
	v_fmac_f32_e32 v16, v127, v127
	v_fmac_f32_e32 v16, v128, v128
	v_fmac_f32_e32 v16, v129, v129
	v_fmac_f32_e32 v16, v130, v130
	v_fmac_f32_e32 v16, v131, v131
	s_nop 1
	v_add_f32_dpp v17, v16, v16 quad_perm:[1,0,3,2] row_mask:0xf bank_mask:0xf
	s_nop 1
	v_add_f32_dpp v16, v17, v17 quad_perm:[2,3,0,1] row_mask:0xf bank_mask:0xf
	s_nop 1
	v_add_f32_dpp v17, v16, v16 row_half_mirror row_mask:0xf bank_mask:0xf
	s_nop 1
	v_add_f32_dpp v16, v17, v17 row_ror:8 row_mask:0xf bank_mask:0xf
	v_mov_b32_e32 v17, v16
	s_nop 1
	v_permlane16_swap_b32_e32 v16, v17
	v_add_f32_e32 v16, v16, v17
	v_mov_b32_e32 v17, v16
	s_nop 1
	v_permlane32_swap_b32_e32 v16, v17
	v_add_f32_e32 v16, v16, v17
	global_store_dwordx4 v[20:21], v[124:127], off
	global_store_dwordx4 v[20:21], v[128:131], off offset:16
	s_lshl_b32 s30, s16, 7
	s_add_u32 s28, s62, s30
	s_addc_u32 s29, s63, 0
	v_lshlrev_b32_e32 v18, 1, v1
	s_mov_b64 exec, s[2:3]
	global_store_dword v18, v16, s[28:29]
	s_mov_b64 exec, -1
	s_waitcnt lgkmcnt(0)
	s_load_dwordx16 s[84:99], s[38:39], 0x40 glc
	s_lshl_b32 s30, s68, 12
	s_add_u32 s28, s26, s30
	s_addc_u32 s29, s27, 0
	global_load_dwordx2 v[24:25], v162, s[28:29]
	s_lshl_b32 s30, s69, 12
	s_add_u32 s28, s26, s30
	s_addc_u32 s29, s27, 0
	global_load_dwordx2 v[26:27], v162, s[28:29]
	s_lshl_b32 s30, s70, 12
	s_add_u32 s28, s26, s30
	s_addc_u32 s29, s27, 0
	global_load_dwordx2 v[28:29], v162, s[28:29]
	s_lshl_b32 s30, s71, 12
	s_add_u32 s28, s26, s30
	s_addc_u32 s29, s27, 0
	global_load_dwordx2 v[30:31], v162, s[28:29]
	s_lshl_b32 s30, s72, 12
	s_add_u32 s28, s26, s30
	s_addc_u32 s29, s27, 0
	global_load_dwordx2 v[32:33], v162, s[28:29]
	s_lshl_b32 s30, s73, 12
	s_add_u32 s28, s26, s30
	s_addc_u32 s29, s27, 0
	global_load_dwordx2 v[34:35], v162, s[28:29]
	s_lshl_b32 s30, s74, 12
	s_add_u32 s28, s26, s30
	s_addc_u32 s29, s27, 0
	global_load_dwordx2 v[36:37], v162, s[28:29]
	s_lshl_b32 s30, s75, 12
	s_add_u32 s28, s26, s30
	s_addc_u32 s29, s27, 0
	global_load_dwordx2 v[38:39], v162, s[28:29]
	s_lshl_b32 s30, s76, 12
	s_add_u32 s28, s26, s30
	s_addc_u32 s29, s27, 0
	global_load_dwordx2 v[40:41], v162, s[28:29]
	s_lshl_b32 s30, s77, 12
	s_add_u32 s28, s26, s30
	s_addc_u32 s29, s27, 0
	global_load_dwordx2 v[42:43], v162, s[28:29]
	s_lshl_b32 s30, s78, 12
	s_add_u32 s28, s26, s30
	s_addc_u32 s29, s27, 0
	global_load_dwordx2 v[44:45], v162, s[28:29]
	s_lshl_b32 s30, s79, 12
	s_add_u32 s28, s26, s30
	s_addc_u32 s29, s27, 0
	global_load_dwordx2 v[46:47], v162, s[28:29]
	s_lshl_b32 s30, s80, 12
	s_add_u32 s28, s26, s30
	s_addc_u32 s29, s27, 0
	global_load_dwordx2 v[48:49], v162, s[28:29]
	s_lshl_b32 s30, s81, 12
	s_add_u32 s28, s26, s30
	s_addc_u32 s29, s27, 0
	global_load_dwordx2 v[50:51], v162, s[28:29]
	s_lshl_b32 s30, s82, 12
	s_add_u32 s28, s26, s30
	s_addc_u32 s29, s27, 0
	global_load_dwordx2 v[52:53], v162, s[28:29]
	s_lshl_b32 s30, s83, 12
	s_add_u32 s28, s26, s30
	s_addc_u32 s29, s27, 0
	global_load_dwordx2 v[54:55], v162, s[28:29]
	s_waitcnt lgkmcnt(0)
	s_load_dwordx16 s[68:83], s[38:39], 0x80 glc
	s_lshl_b32 s30, s84, 12
	s_add_u32 s28, s26, s30
	s_addc_u32 s29, s27, 0
	global_load_dwordx2 v[56:57], v162, s[28:29]
	s_lshl_b32 s30, s85, 12
	s_add_u32 s28, s26, s30
	s_addc_u32 s29, s27, 0
	global_load_dwordx2 v[58:59], v162, s[28:29]
	s_lshl_b32 s30, s86, 12
	s_add_u32 s28, s26, s30
	s_addc_u32 s29, s27, 0
	global_load_dwordx2 v[60:61], v162, s[28:29]
	s_lshl_b32 s30, s87, 12
	s_add_u32 s28, s26, s30
	s_addc_u32 s29, s27, 0
	global_load_dwordx2 v[62:63], v162, s[28:29]
	s_lshl_b32 s30, s88, 12
	s_add_u32 s28, s26, s30
	s_addc_u32 s29, s27, 0
	global_load_dwordx2 v[64:65], v162, s[28:29]
	s_lshl_b32 s30, s89, 12
	s_add_u32 s28, s26, s30
	s_addc_u32 s29, s27, 0
	global_load_dwordx2 v[66:67], v162, s[28:29]
	s_lshl_b32 s30, s90, 12
	s_add_u32 s28, s26, s30
	s_addc_u32 s29, s27, 0
	global_load_dwordx2 v[68:69], v162, s[28:29]
	s_lshl_b32 s30, s91, 12
	s_add_u32 s28, s26, s30
	s_addc_u32 s29, s27, 0
	global_load_dwordx2 v[70:71], v162, s[28:29]
	s_lshl_b32 s30, s92, 12
	s_add_u32 s28, s26, s30
	s_addc_u32 s29, s27, 0
	global_load_dwordx2 v[72:73], v162, s[28:29]
	s_lshl_b32 s30, s93, 12
	s_add_u32 s28, s26, s30
	s_addc_u32 s29, s27, 0
	global_load_dwordx2 v[74:75], v162, s[28:29]
	s_lshl_b32 s30, s94, 12
	s_add_u32 s28, s26, s30
	s_addc_u32 s29, s27, 0
	global_load_dwordx2 v[76:77], v162, s[28:29]
	s_lshl_b32 s30, s95, 12
	s_add_u32 s28, s26, s30
	s_addc_u32 s29, s27, 0
	global_load_dwordx2 v[78:79], v162, s[28:29]
	s_lshl_b32 s30, s96, 12
	s_add_u32 s28, s26, s30
	s_addc_u32 s29, s27, 0
	global_load_dwordx2 v[80:81], v162, s[28:29]
	s_lshl_b32 s30, s97, 12
	s_add_u32 s28, s26, s30
	s_addc_u32 s29, s27, 0
	global_load_dwordx2 v[82:83], v162, s[28:29]
	s_lshl_b32 s30, s98, 12
	s_add_u32 s28, s26, s30
	s_addc_u32 s29, s27, 0
	global_load_dwordx2 v[84:85], v162, s[28:29]
	s_lshl_b32 s30, s99, 12
	s_add_u32 s28, s26, s30
	s_addc_u32 s29, s27, 0
	global_load_dwordx2 v[86:87], v162, s[28:29]
	s_add_i32 s16, s16, 1
	s_cmp_lt_i32 s16, s17
	s_cbranch_scc1 .Lpb_tok
	s_waitcnt vmcnt(0)
	s_waitcnt vmcnt(0)
	v_cmp_eq_u32_e32 vcc, 0, v0
	s_waitcnt vmcnt(0) lgkmcnt(0)
	s_barrier
	s_and_saveexec_b64 s[2:3], vcc
	s_cbranch_execz .Lgbc_1444
	v_readlane_b32 s4, v237, 5
	s_waitcnt vmcnt(0) expcnt(0) lgkmcnt(0)
	s_nop 0
	v_mov_b32_e32 v1, s4
	ds_read_b32 v3, v1
	ds_read_b32 v1, v1 offset:4
	s_waitcnt lgkmcnt(1)
	v_cmp_ne_u32_e32 vcc, 0, v3
	s_branch .Lgbc_1412
	v_readlane_b32 s4, v237, 2
	v_readlane_b32 s5, v237, 3
	s_load_dwordx2 s[8:9], s[6:7], 0x4
	s_lshl_b64 s[4:5], s[4:5], 2
	v_readlane_b32 s6, v237, 0
	s_add_u32 s4, s6, s4
	v_readlane_b32 s6, v237, 1
	s_addc_u32 s5, s6, s5
	s_add_u32 s6, s4, 0x1000
	s_addc_u32 s7, s5, 0
	s_waitcnt lgkmcnt(0)
	s_mul_i32 s20, s8, s38
	s_add_u32 s8, s4, 0x1100
	s_mul_i32 s20, s20, s9
	s_addc_u32 s9, s5, 0
	s_add_u32 s10, s4, 0x1200
	s_addc_u32 s11, s5, 0
	s_add_u32 s12, s4, 0x1300
	s_addc_u32 s13, s5, 0
	s_mov_b32 s21, 1
	v_mov_b32_e32 v17, 0
	s_branch .Lgbc_1400
